# snake order of independent MFMAs in every GEMM K-loop segment (consecutive MFMAs share one operand; bit-identical math)
# speedup vs baseline: 1.0007x; 1.0007x over previous
.LBB0_286:
	s_lshl_b32 s10, s51, 19
	s_add_u32 s10, s20, s10
	s_addc_u32 s11, s21, 0
	s_and_b64 s[16:17], s[4:5], exec
	s_cselect_b32 s54, s11, s31
	s_cselect_b32 s55, s10, s30
	s_lshl_b32 s14, s50, 19
	s_add_u32 s16, s15, s14
	s_addc_u32 s17, s26, 0
	s_and_b64 s[36:37], s[4:5], exec
	s_cselect_b32 s56, s17, s23
	s_cselect_b32 s57, s16, s22
	s_add_i32 s60, 0, 0x10000
	v_add_u32_e32 v198, s60, v196
	s_add_i32 s62, 0, 0x14000
	v_add_u32_e32 v199, s62, v196
	ds_read_b128 v[160:163], v198
	ds_read_b128 v[152:155], v198 offset:1024
	ds_read_b128 v[156:159], v198 offset:2048
	ds_read_b128 v[148:151], v198 offset:3072
	ds_read_b128 v[144:147], v199
	ds_read_b128 v[136:139], v199 offset:1024
	ds_read_b128 v[140:143], v199 offset:2048
	ds_read_b128 v[132:135], v199 offset:3072
	s_add_u32 s36, s30, 0x40080
	s_addc_u32 s37, s31, 0
	s_add_i32 s58, s41, 0xc000
	v_lshl_add_u64 v[174:175], s[36:37], 0, v[168:169]
	s_mov_b32 m0, s58
	s_add_i32 s59, s41, 0xe000
	ds_read_b128 v[178:181], v197
	ds_read_b128 v[182:185], v197 offset:1024
	ds_read_b128 v[190:193], v197 offset:2048
	ds_read_b128 v[200:203], v197 offset:3072
	ds_read_b128 v[204:207], v197 offset:4096
	ds_read_b128 v[208:211], v197 offset:5120
	ds_read_b128 v[212:215], v197 offset:6144
	ds_read_b128 v[216:219], v197 offset:7168
	global_load_lds_dwordx4 v[174:175], off
	v_lshl_add_u64 v[174:175], s[36:37], 0, v[166:167]
	s_mov_b32 m0, s59
	s_nop 0
	global_load_lds_dwordx4 v[174:175], off
	s_waitcnt vmcnt(8)
	s_waitcnt lgkmcnt(0)
	s_barrier
	s_setprio 1
	s_waitcnt lgkmcnt(0)
	v_mfma_f32_16x16x32_bf16 v[128:131], v[160:163], v[178:181], 0
	v_mfma_f32_16x16x32_bf16 v[124:127], v[156:159], v[178:181], 0
	v_mfma_f32_16x16x32_bf16 v[116:119], v[156:159], v[190:193], 0
	v_mfma_f32_16x16x32_bf16 v[120:123], v[160:163], v[190:193], 0
	v_mfma_f32_16x16x32_bf16 v[112:115], v[160:163], v[204:207], 0
	v_mfma_f32_16x16x32_bf16 v[108:111], v[156:159], v[204:207], 0
	v_mfma_f32_16x16x32_bf16 v[100:103], v[156:159], v[212:215], 0
	v_mfma_f32_16x16x32_bf16 v[104:107], v[160:163], v[212:215], 0
	s_nop 0
	v_mfma_f32_16x16x32_bf16 v[128:131], v[152:155], v[182:185], v[128:131]
	v_mfma_f32_16x16x32_bf16 v[124:127], v[148:151], v[182:185], v[124:127]
	v_mfma_f32_16x16x32_bf16 v[116:119], v[148:151], v[200:203], v[116:119]
	v_mfma_f32_16x16x32_bf16 v[120:123], v[152:155], v[200:203], v[120:123]
	v_mfma_f32_16x16x32_bf16 v[112:115], v[152:155], v[208:211], v[112:115]
	v_mfma_f32_16x16x32_bf16 v[108:111], v[148:151], v[208:211], v[108:111]
	v_mfma_f32_16x16x32_bf16 v[100:103], v[148:151], v[216:219], v[100:103]
	v_mfma_f32_16x16x32_bf16 v[104:107], v[152:155], v[216:219], v[104:107]
	s_setprio 0
	s_setprio 1
	v_mfma_f32_16x16x32_bf16 v[96:99], v[144:147], v[178:181], 0
	v_mfma_f32_16x16x32_bf16 v[92:95], v[140:143], v[178:181], 0
	v_mfma_f32_16x16x32_bf16 v[84:87], v[140:143], v[190:193], 0
	v_mfma_f32_16x16x32_bf16 v[88:91], v[144:147], v[190:193], 0
	v_mfma_f32_16x16x32_bf16 v[80:83], v[144:147], v[204:207], 0
	v_mfma_f32_16x16x32_bf16 v[76:79], v[140:143], v[204:207], 0
	v_mfma_f32_16x16x32_bf16 v[68:71], v[140:143], v[212:215], 0
	v_mfma_f32_16x16x32_bf16 v[72:75], v[144:147], v[212:215], 0
	s_nop 0
	v_mfma_f32_16x16x32_bf16 v[96:99], v[136:139], v[182:185], v[96:99]
	v_mfma_f32_16x16x32_bf16 v[92:95], v[132:135], v[182:185], v[92:95]
	v_mfma_f32_16x16x32_bf16 v[84:87], v[132:135], v[200:203], v[84:87]
	v_mfma_f32_16x16x32_bf16 v[88:91], v[136:139], v[200:203], v[88:91]
	v_mfma_f32_16x16x32_bf16 v[80:83], v[136:139], v[208:211], v[80:83]
	v_mfma_f32_16x16x32_bf16 v[76:79], v[132:135], v[208:211], v[76:79]
	v_mfma_f32_16x16x32_bf16 v[68:71], v[132:135], v[216:219], v[68:71]
	v_mfma_f32_16x16x32_bf16 v[72:75], v[136:139], v[216:219], v[72:75]
	s_setprio 0
	s_barrier
	v_lshl_add_u64 v[174:175], s[22:23], 0, v[34:35]
	s_add_i32 s60, s60, s40
	v_lshl_add_u64 v[190:191], v[174:175], 0, s[28:29]
	s_mov_b32 m0, s60
	s_add_i32 s61, s60, 0x2000
	ds_read_b128 v[178:181], v197 offset:16384
	ds_read_b128 v[182:185], v197 offset:17408
	ds_read_b128 v[200:203], v197 offset:18432
	ds_read_b128 v[204:207], v197 offset:19456
	ds_read_b128 v[208:211], v197 offset:20480
	ds_read_b128 v[212:215], v197 offset:21504
	ds_read_b128 v[216:219], v197 offset:22528
	ds_read_b128 v[222:225], v197 offset:23552
	global_load_lds_dwordx4 v[190:191], off
	v_lshl_add_u64 v[190:191], s[22:23], 0, v[164:165]
	s_add_u32 s36, s22, 0x40100
	v_lshl_add_u64 v[192:193], v[190:191], 0, s[28:29]
	s_mov_b32 m0, s61
	s_addc_u32 s37, s23, 0
	s_add_i32 s62, s62, s40
	global_load_lds_dwordx4 v[192:193], off
	v_lshl_add_u64 v[192:193], s[36:37], 0, v[34:35]
	s_mov_b32 m0, s62
	s_add_i32 s63, s62, 0x2000
	global_load_lds_dwordx4 v[192:193], off
	v_lshl_add_u64 v[192:193], s[36:37], 0, v[164:165]
	s_mov_b32 m0, s63
	s_nop 0
	global_load_lds_dwordx4 v[192:193], off
	v_lshl_add_u64 v[192:193], s[30:31], 0, v[168:169]
	v_lshl_add_u64 v[194:195], v[192:193], 0, s[28:29]
	s_mov_b32 m0, s41
	s_nop 0
	global_load_lds_dwordx4 v[194:195], off
	v_lshl_add_u64 v[194:195], s[30:31], 0, v[166:167]
	v_lshl_add_u64 v[226:227], v[194:195], 0, s[28:29]
	s_mov_b32 m0, s42
	s_nop 0
	global_load_lds_dwordx4 v[226:227], off
	s_waitcnt vmcnt(8)
	s_waitcnt lgkmcnt(0)
	s_barrier
	s_setprio 1
	s_waitcnt lgkmcnt(0)
	v_mfma_f32_16x16x32_bf16 v[64:67], v[160:163], v[178:181], 0
	v_mfma_f32_16x16x32_bf16 v[60:63], v[156:159], v[178:181], 0
	v_mfma_f32_16x16x32_bf16 v[52:55], v[156:159], v[200:203], 0
	v_mfma_f32_16x16x32_bf16 v[56:59], v[160:163], v[200:203], 0
	v_mfma_f32_16x16x32_bf16 v[48:51], v[160:163], v[208:211], 0
	v_mfma_f32_16x16x32_bf16 v[44:47], v[156:159], v[208:211], 0
	v_mfma_f32_16x16x32_bf16 v[36:39], v[156:159], v[216:219], 0
	v_mfma_f32_16x16x32_bf16 v[40:43], v[160:163], v[216:219], 0
	s_nop 0
	v_mfma_f32_16x16x32_bf16 v[64:67], v[152:155], v[182:185], v[64:67]
	v_mfma_f32_16x16x32_bf16 v[60:63], v[148:151], v[182:185], v[60:63]
	v_mfma_f32_16x16x32_bf16 v[52:55], v[148:151], v[204:207], v[52:55]
	v_mfma_f32_16x16x32_bf16 v[56:59], v[152:155], v[204:207], v[56:59]
	v_mfma_f32_16x16x32_bf16 v[48:51], v[152:155], v[212:215], v[48:51]
	v_mfma_f32_16x16x32_bf16 v[44:47], v[148:151], v[212:215], v[44:47]
	v_mfma_f32_16x16x32_bf16 v[36:39], v[148:151], v[222:225], v[36:39]
	v_mfma_f32_16x16x32_bf16 v[40:43], v[152:155], v[222:225], v[40:43]
	s_setprio 0
	s_setprio 1
	v_mfma_f32_16x16x32_bf16 v[30:33], v[144:147], v[178:181], 0
	v_mfma_f32_16x16x32_bf16 v[26:29], v[140:143], v[178:181], 0
	v_mfma_f32_16x16x32_bf16 v[18:21], v[140:143], v[200:203], 0
	v_mfma_f32_16x16x32_bf16 v[22:25], v[144:147], v[200:203], 0
	v_mfma_f32_16x16x32_bf16 v[14:17], v[144:147], v[208:211], 0
	v_mfma_f32_16x16x32_bf16 v[10:13], v[140:143], v[208:211], 0
	v_mfma_f32_16x16x32_bf16 v[2:5], v[140:143], v[216:219], 0
	v_mfma_f32_16x16x32_bf16 v[6:9], v[144:147], v[216:219], 0
	s_nop 0
	v_mfma_f32_16x16x32_bf16 v[30:33], v[136:139], v[182:185], v[30:33]
	v_mfma_f32_16x16x32_bf16 v[26:29], v[132:135], v[182:185], v[26:29]
	v_mfma_f32_16x16x32_bf16 v[18:21], v[132:135], v[204:207], v[18:21]
	v_mfma_f32_16x16x32_bf16 v[22:25], v[136:139], v[204:207], v[22:25]
	v_mfma_f32_16x16x32_bf16 v[14:17], v[136:139], v[212:215], v[14:17]
	v_mfma_f32_16x16x32_bf16 v[10:13], v[132:135], v[212:215], v[10:13]
	v_mfma_f32_16x16x32_bf16 v[2:5], v[132:135], v[222:225], v[2:5]
	v_mfma_f32_16x16x32_bf16 v[6:9], v[136:139], v[222:225], v[6:9]
	s_setprio 0
	s_barrier
	s_add_i32 s64, 0, 0x18000
	s_add_i32 s66, 0, 0x1c000
	v_add_u32_e32 v132, s64, v196
	v_add_u32_e32 v133, s66, v196
	ds_read_b128 v[134:137], v132
	ds_read_b128 v[138:141], v132 offset:1024
	ds_read_b128 v[142:145], v132 offset:2048
	ds_read_b128 v[146:149], v132 offset:3072
	ds_read_b128 v[150:153], v133
	ds_read_b128 v[154:157], v133 offset:1024
	ds_read_b128 v[158:161], v133 offset:2048
	ds_read_b128 v[178:181], v133 offset:3072
	s_add_u32 s36, s30, 0x40100
	s_addc_u32 s37, s31, 0
	s_mov_b32 m0, s43
	v_lshl_add_u64 v[162:163], s[36:37], 0, v[168:169]
	ds_read_b128 v[182:185], v197 offset:32768
	ds_read_b128 v[200:203], v197 offset:33792
	ds_read_b128 v[204:207], v197 offset:34816
	ds_read_b128 v[208:211], v197 offset:35840
	ds_read_b128 v[212:215], v197 offset:36864
	ds_read_b128 v[216:219], v197 offset:37888
	ds_read_b128 v[222:225], v197 offset:38912
	ds_read_b128 v[226:229], v197 offset:39936
	global_load_lds_dwordx4 v[162:163], off
	v_lshl_add_u64 v[162:163], s[36:37], 0, v[166:167]
	s_mov_b32 m0, s44
	s_nop 0
	global_load_lds_dwordx4 v[162:163], off
	s_waitcnt vmcnt(8)
	s_waitcnt lgkmcnt(0)
	s_barrier
	s_setprio 1
	s_waitcnt lgkmcnt(0)
	v_mfma_f32_16x16x32_bf16 v[128:131], v[134:137], v[182:185], v[128:131]
	v_mfma_f32_16x16x32_bf16 v[124:127], v[142:145], v[182:185], v[124:127]
	v_mfma_f32_16x16x32_bf16 v[116:119], v[142:145], v[204:207], v[116:119]
	v_mfma_f32_16x16x32_bf16 v[120:123], v[134:137], v[204:207], v[120:123]
	v_mfma_f32_16x16x32_bf16 v[112:115], v[134:137], v[212:215], v[112:115]
	v_mfma_f32_16x16x32_bf16 v[108:111], v[142:145], v[212:215], v[108:111]
	v_mfma_f32_16x16x32_bf16 v[100:103], v[142:145], v[222:225], v[100:103]
	v_mfma_f32_16x16x32_bf16 v[104:107], v[134:137], v[222:225], v[104:107]
	v_mfma_f32_16x16x32_bf16 v[128:131], v[138:141], v[200:203], v[128:131]
	v_mfma_f32_16x16x32_bf16 v[124:127], v[146:149], v[200:203], v[124:127]
	v_mfma_f32_16x16x32_bf16 v[116:119], v[146:149], v[208:211], v[116:119]
	v_mfma_f32_16x16x32_bf16 v[120:123], v[138:141], v[208:211], v[120:123]
	v_mfma_f32_16x16x32_bf16 v[112:115], v[138:141], v[216:219], v[112:115]
	v_mfma_f32_16x16x32_bf16 v[108:111], v[146:149], v[216:219], v[108:111]
	v_mfma_f32_16x16x32_bf16 v[100:103], v[146:149], v[226:229], v[100:103]
	v_mfma_f32_16x16x32_bf16 v[104:107], v[138:141], v[226:229], v[104:107]
	s_setprio 0
	s_setprio 1
	v_mfma_f32_16x16x32_bf16 v[96:99], v[150:153], v[182:185], v[96:99]
	v_mfma_f32_16x16x32_bf16 v[92:95], v[158:161], v[182:185], v[92:95]
	v_mfma_f32_16x16x32_bf16 v[84:87], v[158:161], v[204:207], v[84:87]
	v_mfma_f32_16x16x32_bf16 v[88:91], v[150:153], v[204:207], v[88:91]
	v_mfma_f32_16x16x32_bf16 v[80:83], v[150:153], v[212:215], v[80:83]
	v_mfma_f32_16x16x32_bf16 v[76:79], v[158:161], v[212:215], v[76:79]
	v_mfma_f32_16x16x32_bf16 v[68:71], v[158:161], v[222:225], v[68:71]
	v_mfma_f32_16x16x32_bf16 v[72:75], v[150:153], v[222:225], v[72:75]
	v_mfma_f32_16x16x32_bf16 v[96:99], v[154:157], v[200:203], v[96:99]
	v_mfma_f32_16x16x32_bf16 v[92:95], v[178:181], v[200:203], v[92:95]
	v_mfma_f32_16x16x32_bf16 v[84:87], v[178:181], v[208:211], v[84:87]
	v_mfma_f32_16x16x32_bf16 v[88:91], v[154:157], v[208:211], v[88:91]
	v_mfma_f32_16x16x32_bf16 v[80:83], v[154:157], v[216:219], v[80:83]
	v_mfma_f32_16x16x32_bf16 v[76:79], v[178:181], v[216:219], v[76:79]
	v_mfma_f32_16x16x32_bf16 v[68:71], v[178:181], v[226:229], v[68:71]
	v_mfma_f32_16x16x32_bf16 v[72:75], v[154:157], v[226:229], v[72:75]
	s_setprio 0
	s_barrier
	s_add_i32 s64, s64, s40
	s_mov_b64 s[24:25], 0x180
	s_add_i32 s65, s64, 0x2000
	v_lshl_add_u64 v[162:163], v[174:175], 0, s[24:25]
	s_mov_b32 m0, s64
	s_add_u32 s36, s22, 0x40180
	ds_read_b128 v[182:185], v197 offset:49152
	ds_read_b128 v[200:203], v197 offset:50176
	ds_read_b128 v[204:207], v197 offset:51200
	ds_read_b128 v[208:211], v197 offset:52224
	ds_read_b128 v[212:215], v197 offset:53248
	ds_read_b128 v[216:219], v197 offset:54272
	ds_read_b128 v[222:225], v197 offset:55296
	ds_read_b128 v[226:229], v197 offset:56320
	global_load_lds_dwordx4 v[162:163], off
	v_lshl_add_u64 v[162:163], v[190:191], 0, s[24:25]
	s_mov_b32 m0, s65
	s_addc_u32 s37, s23, 0
	s_add_i32 s66, s66, s40
	global_load_lds_dwordx4 v[162:163], off
	v_lshl_add_u64 v[162:163], s[36:37], 0, v[34:35]
	s_mov_b32 m0, s66
	s_add_i32 s67, s66, 0x2000
	global_load_lds_dwordx4 v[162:163], off
	v_lshl_add_u64 v[162:163], s[36:37], 0, v[164:165]
	s_mov_b32 m0, s67
	s_nop 0
	global_load_lds_dwordx4 v[162:163], off
	v_lshl_add_u64 v[162:163], v[192:193], 0, s[24:25]
	s_mov_b32 m0, s47
	s_nop 0
	global_load_lds_dwordx4 v[162:163], off
	v_lshl_add_u64 v[162:163], v[194:195], 0, s[24:25]
	s_mov_b32 m0, s48
	s_nop 0
	global_load_lds_dwordx4 v[162:163], off
	s_waitcnt vmcnt(8)
	s_waitcnt lgkmcnt(0)
	s_barrier
	s_setprio 1
	s_waitcnt lgkmcnt(0)
	v_mfma_f32_16x16x32_bf16 v[64:67], v[134:137], v[182:185], v[64:67]
	v_mfma_f32_16x16x32_bf16 v[60:63], v[142:145], v[182:185], v[60:63]
	v_mfma_f32_16x16x32_bf16 v[52:55], v[142:145], v[204:207], v[52:55]
	v_mfma_f32_16x16x32_bf16 v[56:59], v[134:137], v[204:207], v[56:59]
	v_mfma_f32_16x16x32_bf16 v[48:51], v[134:137], v[212:215], v[48:51]
	v_mfma_f32_16x16x32_bf16 v[44:47], v[142:145], v[212:215], v[44:47]
	v_mfma_f32_16x16x32_bf16 v[36:39], v[142:145], v[222:225], v[36:39]
	v_mfma_f32_16x16x32_bf16 v[40:43], v[134:137], v[222:225], v[40:43]
	v_mfma_f32_16x16x32_bf16 v[64:67], v[138:141], v[200:203], v[64:67]
	v_mfma_f32_16x16x32_bf16 v[60:63], v[146:149], v[200:203], v[60:63]
	v_mfma_f32_16x16x32_bf16 v[52:55], v[146:149], v[208:211], v[52:55]
	v_mfma_f32_16x16x32_bf16 v[56:59], v[138:141], v[208:211], v[56:59]
	v_mfma_f32_16x16x32_bf16 v[48:51], v[138:141], v[216:219], v[48:51]
	v_mfma_f32_16x16x32_bf16 v[44:47], v[146:149], v[216:219], v[44:47]
	v_mfma_f32_16x16x32_bf16 v[36:39], v[146:149], v[226:229], v[36:39]
	v_mfma_f32_16x16x32_bf16 v[40:43], v[138:141], v[226:229], v[40:43]
	s_setprio 0
	s_setprio 1
	v_mfma_f32_16x16x32_bf16 v[30:33], v[150:153], v[182:185], v[30:33]
	v_mfma_f32_16x16x32_bf16 v[26:29], v[158:161], v[182:185], v[26:29]
	v_mfma_f32_16x16x32_bf16 v[18:21], v[158:161], v[204:207], v[18:21]
	v_mfma_f32_16x16x32_bf16 v[22:25], v[150:153], v[204:207], v[22:25]
	v_mfma_f32_16x16x32_bf16 v[14:17], v[150:153], v[212:215], v[14:17]
	v_mfma_f32_16x16x32_bf16 v[10:13], v[158:161], v[212:215], v[10:13]
	v_mfma_f32_16x16x32_bf16 v[2:5], v[158:161], v[222:225], v[2:5]
	v_mfma_f32_16x16x32_bf16 v[6:9], v[150:153], v[222:225], v[6:9]
	v_mfma_f32_16x16x32_bf16 v[30:33], v[154:157], v[200:203], v[30:33]
	v_mfma_f32_16x16x32_bf16 v[26:29], v[178:181], v[200:203], v[26:29]
	v_mfma_f32_16x16x32_bf16 v[18:21], v[178:181], v[208:211], v[18:21]
	v_mfma_f32_16x16x32_bf16 v[22:25], v[154:157], v[208:211], v[22:25]
	v_mfma_f32_16x16x32_bf16 v[14:17], v[154:157], v[216:219], v[14:17]
	v_mfma_f32_16x16x32_bf16 v[10:13], v[178:181], v[216:219], v[10:13]
	v_mfma_f32_16x16x32_bf16 v[2:5], v[178:181], v[226:229], v[2:5]
	v_mfma_f32_16x16x32_bf16 v[6:9], v[154:157], v[226:229], v[6:9]
	s_setprio 0
	s_barrier
	s_add_u32 s30, s30, 0x40180
	s_addc_u32 s31, s31, 0
	s_add_u32 s68, s22, 0x200
	s_addc_u32 s69, s23, 0
	s_mov_b32 s70, 0
.LBB0_287:
	ds_read_b128 v[134:137], v198
	ds_read_b128 v[138:141], v198 offset:1024
	ds_read_b128 v[142:145], v198 offset:2048
	ds_read_b128 v[146:149], v198 offset:3072
	ds_read_b128 v[150:153], v199
	ds_read_b128 v[154:157], v199 offset:1024
	ds_read_b128 v[158:161], v199 offset:2048
	ds_read_b128 v[178:181], v199 offset:3072
	s_add_u32 s14, s30, 0xfffc0080
	s_addc_u32 s22, s31, -1
	s_cmp_eq_u32 s70, 12
	s_cselect_b32 s37, s54, s22
	s_cselect_b32 s36, s55, s14
	s_cselect_b32 s23, s56, s69
	s_cselect_b32 s22, s57, s68
	s_mov_b32 m0, s58
	v_lshl_add_u64 v[162:163], s[30:31], 0, v[170:171]
	ds_read_b128 v[182:185], v197
	ds_read_b128 v[190:193], v197 offset:1024
	ds_read_b128 v[200:203], v197 offset:2048
	ds_read_b128 v[204:207], v197 offset:3072
	ds_read_b128 v[208:211], v197 offset:4096
	ds_read_b128 v[212:215], v197 offset:5120
	ds_read_b128 v[216:219], v197 offset:6144
	ds_read_b128 v[222:225], v197 offset:7168
	global_load_lds_dwordx4 v[162:163], off
	v_lshl_add_u64 v[162:163], s[30:31], 0, v[172:173]
	s_mov_b32 m0, s59
	s_nop 0
	global_load_lds_dwordx4 v[162:163], off
	s_waitcnt vmcnt(8)
	s_waitcnt lgkmcnt(0)
	s_barrier
	s_setprio 1
	s_waitcnt lgkmcnt(0)
	v_mfma_f32_16x16x32_bf16 v[128:131], v[134:137], v[182:185], v[128:131]
	v_mfma_f32_16x16x32_bf16 v[124:127], v[142:145], v[182:185], v[124:127]
	v_mfma_f32_16x16x32_bf16 v[116:119], v[142:145], v[200:203], v[116:119]
	v_mfma_f32_16x16x32_bf16 v[120:123], v[134:137], v[200:203], v[120:123]
	v_mfma_f32_16x16x32_bf16 v[112:115], v[134:137], v[208:211], v[112:115]
	v_mfma_f32_16x16x32_bf16 v[108:111], v[142:145], v[208:211], v[108:111]
	v_mfma_f32_16x16x32_bf16 v[100:103], v[142:145], v[216:219], v[100:103]
	v_mfma_f32_16x16x32_bf16 v[104:107], v[134:137], v[216:219], v[104:107]
	v_mfma_f32_16x16x32_bf16 v[128:131], v[138:141], v[190:193], v[128:131]
	v_mfma_f32_16x16x32_bf16 v[124:127], v[146:149], v[190:193], v[124:127]
	v_mfma_f32_16x16x32_bf16 v[116:119], v[146:149], v[204:207], v[116:119]
	v_mfma_f32_16x16x32_bf16 v[120:123], v[138:141], v[204:207], v[120:123]
	v_mfma_f32_16x16x32_bf16 v[112:115], v[138:141], v[212:215], v[112:115]
	v_mfma_f32_16x16x32_bf16 v[108:111], v[146:149], v[212:215], v[108:111]
	v_mfma_f32_16x16x32_bf16 v[100:103], v[146:149], v[222:225], v[100:103]
	v_mfma_f32_16x16x32_bf16 v[104:107], v[138:141], v[222:225], v[104:107]
	s_setprio 0
	s_setprio 1
	v_mfma_f32_16x16x32_bf16 v[96:99], v[150:153], v[182:185], v[96:99]
	v_mfma_f32_16x16x32_bf16 v[92:95], v[158:161], v[182:185], v[92:95]
	v_mfma_f32_16x16x32_bf16 v[84:87], v[158:161], v[200:203], v[84:87]
	v_mfma_f32_16x16x32_bf16 v[88:91], v[150:153], v[200:203], v[88:91]
	v_mfma_f32_16x16x32_bf16 v[80:83], v[150:153], v[208:211], v[80:83]
	v_mfma_f32_16x16x32_bf16 v[76:79], v[158:161], v[208:211], v[76:79]
	v_mfma_f32_16x16x32_bf16 v[68:71], v[158:161], v[216:219], v[68:71]
	v_mfma_f32_16x16x32_bf16 v[72:75], v[150:153], v[216:219], v[72:75]
	v_mfma_f32_16x16x32_bf16 v[96:99], v[154:157], v[190:193], v[96:99]
	v_mfma_f32_16x16x32_bf16 v[92:95], v[178:181], v[190:193], v[92:95]
	v_mfma_f32_16x16x32_bf16 v[84:87], v[178:181], v[204:207], v[84:87]
	v_mfma_f32_16x16x32_bf16 v[88:91], v[154:157], v[204:207], v[88:91]
	v_mfma_f32_16x16x32_bf16 v[80:83], v[154:157], v[212:215], v[80:83]
	v_mfma_f32_16x16x32_bf16 v[76:79], v[178:181], v[212:215], v[76:79]
	v_mfma_f32_16x16x32_bf16 v[68:71], v[178:181], v[222:225], v[68:71]
	v_mfma_f32_16x16x32_bf16 v[72:75], v[154:157], v[222:225], v[72:75]
	s_setprio 0
	s_barrier
	s_mov_b32 m0, s60
	v_lshl_add_u64 v[162:163], s[22:23], 0, v[34:35]
	s_add_u32 s72, s22, 0x40000
	ds_read_b128 v[182:185], v197 offset:16384
	ds_read_b128 v[190:193], v197 offset:17408
	ds_read_b128 v[200:203], v197 offset:18432
	ds_read_b128 v[204:207], v197 offset:19456
	ds_read_b128 v[208:211], v197 offset:20480
	ds_read_b128 v[212:215], v197 offset:21504
	ds_read_b128 v[216:219], v197 offset:22528
	ds_read_b128 v[222:225], v197 offset:23552
	global_load_lds_dwordx4 v[162:163], off
	v_lshl_add_u64 v[174:175], s[22:23], 0, v[164:165]
	s_mov_b32 m0, s61
	s_addc_u32 s73, s23, 0
	global_load_lds_dwordx4 v[174:175], off
	v_lshl_add_u64 v[194:195], s[72:73], 0, v[34:35]
	s_mov_b32 m0, s62
	v_lshl_add_u64 v[226:227], s[36:37], 0, v[166:167]
	global_load_lds_dwordx4 v[194:195], off
	v_lshl_add_u64 v[194:195], s[72:73], 0, v[164:165]
	s_mov_b32 m0, s63
	s_nop 0
	global_load_lds_dwordx4 v[194:195], off
	v_lshl_add_u64 v[194:195], s[36:37], 0, v[168:169]
	s_mov_b32 m0, s41
	s_nop 0
	global_load_lds_dwordx4 v[194:195], off
	s_mov_b32 m0, s42
	s_nop 0
	global_load_lds_dwordx4 v[226:227], off
	s_waitcnt vmcnt(8)
	s_waitcnt lgkmcnt(0)
	s_barrier
	s_setprio 1
	s_waitcnt lgkmcnt(0)
	v_mfma_f32_16x16x32_bf16 v[64:67], v[134:137], v[182:185], v[64:67]
	v_mfma_f32_16x16x32_bf16 v[60:63], v[142:145], v[182:185], v[60:63]
	v_mfma_f32_16x16x32_bf16 v[52:55], v[142:145], v[200:203], v[52:55]
	v_mfma_f32_16x16x32_bf16 v[56:59], v[134:137], v[200:203], v[56:59]
	v_mfma_f32_16x16x32_bf16 v[48:51], v[134:137], v[208:211], v[48:51]
	v_mfma_f32_16x16x32_bf16 v[44:47], v[142:145], v[208:211], v[44:47]
	v_mfma_f32_16x16x32_bf16 v[36:39], v[142:145], v[216:219], v[36:39]
	v_mfma_f32_16x16x32_bf16 v[40:43], v[134:137], v[216:219], v[40:43]
	v_mfma_f32_16x16x32_bf16 v[64:67], v[138:141], v[190:193], v[64:67]
	v_mfma_f32_16x16x32_bf16 v[60:63], v[146:149], v[190:193], v[60:63]
	v_mfma_f32_16x16x32_bf16 v[52:55], v[146:149], v[204:207], v[52:55]
	v_mfma_f32_16x16x32_bf16 v[56:59], v[138:141], v[204:207], v[56:59]
	v_mfma_f32_16x16x32_bf16 v[48:51], v[138:141], v[212:215], v[48:51]
	v_mfma_f32_16x16x32_bf16 v[44:47], v[146:149], v[212:215], v[44:47]
	v_mfma_f32_16x16x32_bf16 v[36:39], v[146:149], v[222:225], v[36:39]
	v_mfma_f32_16x16x32_bf16 v[40:43], v[138:141], v[222:225], v[40:43]
	s_setprio 0
	s_setprio 1
	v_mfma_f32_16x16x32_bf16 v[30:33], v[150:153], v[182:185], v[30:33]
	v_mfma_f32_16x16x32_bf16 v[26:29], v[158:161], v[182:185], v[26:29]
	v_mfma_f32_16x16x32_bf16 v[18:21], v[158:161], v[200:203], v[18:21]
	v_mfma_f32_16x16x32_bf16 v[22:25], v[150:153], v[200:203], v[22:25]
	v_mfma_f32_16x16x32_bf16 v[14:17], v[150:153], v[208:211], v[14:17]
	v_mfma_f32_16x16x32_bf16 v[10:13], v[158:161], v[208:211], v[10:13]
	v_mfma_f32_16x16x32_bf16 v[2:5], v[158:161], v[216:219], v[2:5]
	v_mfma_f32_16x16x32_bf16 v[6:9], v[150:153], v[216:219], v[6:9]
	v_mfma_f32_16x16x32_bf16 v[30:33], v[154:157], v[190:193], v[30:33]
	v_mfma_f32_16x16x32_bf16 v[26:29], v[178:181], v[190:193], v[26:29]
	v_mfma_f32_16x16x32_bf16 v[18:21], v[178:181], v[204:207], v[18:21]
	v_mfma_f32_16x16x32_bf16 v[22:25], v[154:157], v[204:207], v[22:25]
	v_mfma_f32_16x16x32_bf16 v[14:17], v[154:157], v[212:215], v[14:17]
	v_mfma_f32_16x16x32_bf16 v[10:13], v[178:181], v[212:215], v[10:13]
	v_mfma_f32_16x16x32_bf16 v[2:5], v[178:181], v[222:225], v[2:5]
	v_mfma_f32_16x16x32_bf16 v[6:9], v[154:157], v[222:225], v[6:9]
	s_setprio 0
	s_barrier
	ds_read_b128 v[134:137], v132
	ds_read_b128 v[138:141], v132 offset:1024
	ds_read_b128 v[142:145], v132 offset:2048
	ds_read_b128 v[146:149], v132 offset:3072
	ds_read_b128 v[150:153], v133
	ds_read_b128 v[154:157], v133 offset:1024
	ds_read_b128 v[158:161], v133 offset:2048
	ds_read_b128 v[178:181], v133 offset:3072
	s_add_u32 s36, s36, 0x40000
	s_addc_u32 s37, s37, 0
	s_mov_b32 m0, s43
	v_lshl_add_u64 v[228:229], s[36:37], 0, v[168:169]
	ds_read_b128 v[182:185], v197 offset:32768
	ds_read_b128 v[190:193], v197 offset:33792
	ds_read_b128 v[200:203], v197 offset:34816
	ds_read_b128 v[204:207], v197 offset:35840
	ds_read_b128 v[208:211], v197 offset:36864
	ds_read_b128 v[212:215], v197 offset:37888
	ds_read_b128 v[216:219], v197 offset:38912
	ds_read_b128 v[222:225], v197 offset:39936
	global_load_lds_dwordx4 v[228:229], off
	v_lshl_add_u64 v[228:229], s[36:37], 0, v[166:167]
	s_mov_b32 m0, s44
	s_nop 0
	global_load_lds_dwordx4 v[228:229], off
	s_waitcnt vmcnt(8)
	s_waitcnt lgkmcnt(0)
	s_barrier
	s_setprio 1
	s_waitcnt lgkmcnt(0)
	v_mfma_f32_16x16x32_bf16 v[128:131], v[134:137], v[182:185], v[128:131]
	v_mfma_f32_16x16x32_bf16 v[124:127], v[142:145], v[182:185], v[124:127]
	v_mfma_f32_16x16x32_bf16 v[116:119], v[142:145], v[200:203], v[116:119]
	v_mfma_f32_16x16x32_bf16 v[120:123], v[134:137], v[200:203], v[120:123]
	v_mfma_f32_16x16x32_bf16 v[112:115], v[134:137], v[208:211], v[112:115]
	v_mfma_f32_16x16x32_bf16 v[108:111], v[142:145], v[208:211], v[108:111]
	v_mfma_f32_16x16x32_bf16 v[100:103], v[142:145], v[216:219], v[100:103]
	v_mfma_f32_16x16x32_bf16 v[104:107], v[134:137], v[216:219], v[104:107]
	v_mfma_f32_16x16x32_bf16 v[128:131], v[138:141], v[190:193], v[128:131]
	v_mfma_f32_16x16x32_bf16 v[124:127], v[146:149], v[190:193], v[124:127]
	v_mfma_f32_16x16x32_bf16 v[116:119], v[146:149], v[204:207], v[116:119]
	v_mfma_f32_16x16x32_bf16 v[120:123], v[138:141], v[204:207], v[120:123]
	v_mfma_f32_16x16x32_bf16 v[112:115], v[138:141], v[212:215], v[112:115]
	v_mfma_f32_16x16x32_bf16 v[108:111], v[146:149], v[212:215], v[108:111]
	v_mfma_f32_16x16x32_bf16 v[100:103], v[146:149], v[222:225], v[100:103]
	v_mfma_f32_16x16x32_bf16 v[104:107], v[138:141], v[222:225], v[104:107]
	s_setprio 0
	s_setprio 1
	v_mfma_f32_16x16x32_bf16 v[96:99], v[150:153], v[182:185], v[96:99]
	v_mfma_f32_16x16x32_bf16 v[92:95], v[158:161], v[182:185], v[92:95]
	v_mfma_f32_16x16x32_bf16 v[84:87], v[158:161], v[200:203], v[84:87]
	v_mfma_f32_16x16x32_bf16 v[88:91], v[150:153], v[200:203], v[88:91]
	v_mfma_f32_16x16x32_bf16 v[80:83], v[150:153], v[208:211], v[80:83]
	v_mfma_f32_16x16x32_bf16 v[76:79], v[158:161], v[208:211], v[76:79]
	v_mfma_f32_16x16x32_bf16 v[68:71], v[158:161], v[216:219], v[68:71]
	v_mfma_f32_16x16x32_bf16 v[72:75], v[150:153], v[216:219], v[72:75]
	v_mfma_f32_16x16x32_bf16 v[96:99], v[154:157], v[190:193], v[96:99]
	v_mfma_f32_16x16x32_bf16 v[92:95], v[178:181], v[190:193], v[92:95]
	v_mfma_f32_16x16x32_bf16 v[84:87], v[178:181], v[204:207], v[84:87]
	v_mfma_f32_16x16x32_bf16 v[88:91], v[154:157], v[204:207], v[88:91]
	v_mfma_f32_16x16x32_bf16 v[80:83], v[154:157], v[212:215], v[80:83]
	v_mfma_f32_16x16x32_bf16 v[76:79], v[178:181], v[212:215], v[76:79]
	v_mfma_f32_16x16x32_bf16 v[68:71], v[178:181], v[222:225], v[68:71]
	v_mfma_f32_16x16x32_bf16 v[72:75], v[154:157], v[222:225], v[72:75]
	s_setprio 0
	s_barrier
	s_mov_b32 m0, s64
	v_lshl_add_u64 v[162:163], v[162:163], 0, s[18:19]
	s_add_u32 s22, s22, 0x40080
	ds_read_b128 v[182:185], v197 offset:49152
	ds_read_b128 v[190:193], v197 offset:50176
	ds_read_b128 v[200:203], v197 offset:51200
	ds_read_b128 v[204:207], v197 offset:52224
	ds_read_b128 v[208:211], v197 offset:53248
	ds_read_b128 v[212:215], v197 offset:54272
	ds_read_b128 v[216:219], v197 offset:55296
	ds_read_b128 v[222:225], v197 offset:56320
	global_load_lds_dwordx4 v[162:163], off
	v_lshl_add_u64 v[162:163], v[174:175], 0, s[18:19]
	s_mov_b32 m0, s65
	s_addc_u32 s23, s23, 0
	global_load_lds_dwordx4 v[162:163], off
	v_lshl_add_u64 v[162:163], s[22:23], 0, v[34:35]
	s_mov_b32 m0, s66
	s_nop 0
	global_load_lds_dwordx4 v[162:163], off
	v_lshl_add_u64 v[162:163], s[22:23], 0, v[164:165]
	s_mov_b32 m0, s67
	s_nop 0
	global_load_lds_dwordx4 v[162:163], off
	v_lshl_add_u64 v[162:163], v[194:195], 0, s[18:19]
	s_mov_b32 m0, s47
	s_nop 0
	global_load_lds_dwordx4 v[162:163], off
	v_lshl_add_u64 v[162:163], v[226:227], 0, s[18:19]
	s_mov_b32 m0, s48
	s_nop 0
	global_load_lds_dwordx4 v[162:163], off
	s_waitcnt vmcnt(8)
	s_waitcnt lgkmcnt(0)
	s_barrier
	s_setprio 1
	s_waitcnt lgkmcnt(0)
	v_mfma_f32_16x16x32_bf16 v[64:67], v[134:137], v[182:185], v[64:67]
	v_mfma_f32_16x16x32_bf16 v[60:63], v[142:145], v[182:185], v[60:63]
	v_mfma_f32_16x16x32_bf16 v[52:55], v[142:145], v[200:203], v[52:55]
	v_mfma_f32_16x16x32_bf16 v[56:59], v[134:137], v[200:203], v[56:59]
	v_mfma_f32_16x16x32_bf16 v[48:51], v[134:137], v[208:211], v[48:51]
	v_mfma_f32_16x16x32_bf16 v[44:47], v[142:145], v[208:211], v[44:47]
	v_mfma_f32_16x16x32_bf16 v[36:39], v[142:145], v[216:219], v[36:39]
	v_mfma_f32_16x16x32_bf16 v[40:43], v[134:137], v[216:219], v[40:43]
	v_mfma_f32_16x16x32_bf16 v[64:67], v[138:141], v[190:193], v[64:67]
	v_mfma_f32_16x16x32_bf16 v[60:63], v[146:149], v[190:193], v[60:63]
	v_mfma_f32_16x16x32_bf16 v[52:55], v[146:149], v[204:207], v[52:55]
	v_mfma_f32_16x16x32_bf16 v[56:59], v[138:141], v[204:207], v[56:59]
	v_mfma_f32_16x16x32_bf16 v[48:51], v[138:141], v[212:215], v[48:51]
	v_mfma_f32_16x16x32_bf16 v[44:47], v[146:149], v[212:215], v[44:47]
	v_mfma_f32_16x16x32_bf16 v[36:39], v[146:149], v[222:225], v[36:39]
	v_mfma_f32_16x16x32_bf16 v[40:43], v[138:141], v[222:225], v[40:43]
	s_setprio 0
	s_setprio 1
	v_mfma_f32_16x16x32_bf16 v[30:33], v[150:153], v[182:185], v[30:33]
	v_mfma_f32_16x16x32_bf16 v[26:29], v[158:161], v[182:185], v[26:29]
	v_mfma_f32_16x16x32_bf16 v[18:21], v[158:161], v[200:203], v[18:21]
	v_mfma_f32_16x16x32_bf16 v[22:25], v[150:153], v[200:203], v[22:25]
	v_mfma_f32_16x16x32_bf16 v[14:17], v[150:153], v[208:211], v[14:17]
	v_mfma_f32_16x16x32_bf16 v[10:13], v[158:161], v[208:211], v[10:13]
	v_mfma_f32_16x16x32_bf16 v[2:5], v[158:161], v[216:219], v[2:5]
	v_mfma_f32_16x16x32_bf16 v[6:9], v[150:153], v[216:219], v[6:9]
	v_mfma_f32_16x16x32_bf16 v[30:33], v[154:157], v[190:193], v[30:33]
	v_mfma_f32_16x16x32_bf16 v[26:29], v[178:181], v[190:193], v[26:29]
	v_mfma_f32_16x16x32_bf16 v[18:21], v[178:181], v[204:207], v[18:21]
	v_mfma_f32_16x16x32_bf16 v[22:25], v[154:157], v[204:207], v[22:25]
	v_mfma_f32_16x16x32_bf16 v[14:17], v[154:157], v[212:215], v[14:17]
	v_mfma_f32_16x16x32_bf16 v[10:13], v[178:181], v[212:215], v[10:13]
	v_mfma_f32_16x16x32_bf16 v[2:5], v[178:181], v[222:225], v[2:5]
	v_mfma_f32_16x16x32_bf16 v[6:9], v[154:157], v[222:225], v[6:9]
	s_setprio 0
	s_barrier
	s_add_i32 s70, s70, 2
	s_add_u32 s30, s30, 0x100
	s_addc_u32 s31, s31, 0
	s_add_u32 s68, s68, 0x100
	s_addc_u32 s69, s69, 0
	s_cmp_gt_u32 s70, 13
	s_cbranch_scc0 .LBB0_287
	s_and_b64 vcc, exec, s[8:9]
	s_cbranch_vccz .LBB0_290
	s_barrier

.LBB0_540:
	s_lshl_b32 s14, s55, 19
	v_readlane_b32 s16, v253, 53
	v_readlane_b32 s17, v253, 54
	s_add_u32 s16, s16, s14
	s_addc_u32 s17, s17, 0
	s_and_b64 s[22:23], s[4:5], exec
	s_cselect_b32 s58, s17, s37
	s_cselect_b32 s59, s16, s36
	s_lshl_b32 s14, s54, 19
	s_add_u32 s22, s15, s14
	s_addc_u32 s23, s26, 0
	s_and_b64 s[40:41], s[4:5], exec
	s_cselect_b32 s60, s23, s31
	s_cselect_b32 s61, s22, s30
	s_add_i32 s64, 0, 0x10000
	v_add_u32_e32 v172, s64, v222
	s_add_i32 s66, 0, 0x14000
	v_add_u32_e32 v173, s66, v222
	ds_read_b128 v[160:163], v172
	ds_read_b128 v[152:155], v172 offset:1024
	ds_read_b128 v[156:159], v172 offset:2048
	ds_read_b128 v[148:151], v172 offset:3072
	ds_read_b128 v[144:147], v173
	ds_read_b128 v[136:139], v173 offset:1024
	ds_read_b128 v[140:143], v173 offset:2048
	ds_read_b128 v[132:135], v173 offset:3072
	s_add_u32 s40, s36, 0x40080
	s_addc_u32 s41, s37, 0
	s_add_i32 s62, s43, 0xc000
	v_lshl_add_u64 v[174:175], s[40:41], 0, v[194:195]
	s_mov_b32 m0, s62
	s_add_i32 s63, s43, 0xe000
	ds_read_b128 v[164:167], v223
	ds_read_b128 v[168:171], v223 offset:1024
	ds_read_b128 v[178:181], v223 offset:2048
	ds_read_b128 v[182:185], v223 offset:3072
	ds_read_b128 v[200:203], v223 offset:4096
	ds_read_b128 v[204:207], v223 offset:5120
	ds_read_b128 v[208:211], v223 offset:6144
	ds_read_b128 v[212:215], v223 offset:7168
	global_load_lds_dwordx4 v[174:175], off
	v_lshl_add_u64 v[174:175], s[40:41], 0, v[192:193]
	s_mov_b32 m0, s63
	s_nop 0
	global_load_lds_dwordx4 v[174:175], off
	s_waitcnt vmcnt(8)
	s_waitcnt lgkmcnt(0)
	s_barrier
	s_setprio 1
	s_waitcnt lgkmcnt(0)
	v_mfma_f32_16x16x32_bf16 v[128:131], v[160:163], v[164:167], 0
	v_mfma_f32_16x16x32_bf16 v[124:127], v[156:159], v[164:167], 0
	v_mfma_f32_16x16x32_bf16 v[116:119], v[156:159], v[178:181], 0
	v_mfma_f32_16x16x32_bf16 v[120:123], v[160:163], v[178:181], 0
	v_mfma_f32_16x16x32_bf16 v[112:115], v[160:163], v[200:203], 0
	v_mfma_f32_16x16x32_bf16 v[108:111], v[156:159], v[200:203], 0
	v_mfma_f32_16x16x32_bf16 v[100:103], v[156:159], v[208:211], 0
	v_mfma_f32_16x16x32_bf16 v[104:107], v[160:163], v[208:211], 0
	s_nop 0
	v_mfma_f32_16x16x32_bf16 v[128:131], v[152:155], v[168:171], v[128:131]
	v_mfma_f32_16x16x32_bf16 v[124:127], v[148:151], v[168:171], v[124:127]
	v_mfma_f32_16x16x32_bf16 v[116:119], v[148:151], v[182:185], v[116:119]
	v_mfma_f32_16x16x32_bf16 v[120:123], v[152:155], v[182:185], v[120:123]
	v_mfma_f32_16x16x32_bf16 v[112:115], v[152:155], v[204:207], v[112:115]
	v_mfma_f32_16x16x32_bf16 v[108:111], v[148:151], v[204:207], v[108:111]
	v_mfma_f32_16x16x32_bf16 v[100:103], v[148:151], v[212:215], v[100:103]
	v_mfma_f32_16x16x32_bf16 v[104:107], v[152:155], v[212:215], v[104:107]
	s_setprio 0
	s_setprio 1
	v_mfma_f32_16x16x32_bf16 v[96:99], v[144:147], v[164:167], 0
	v_mfma_f32_16x16x32_bf16 v[92:95], v[140:143], v[164:167], 0
	v_mfma_f32_16x16x32_bf16 v[84:87], v[140:143], v[178:181], 0
	v_mfma_f32_16x16x32_bf16 v[88:91], v[144:147], v[178:181], 0
	v_mfma_f32_16x16x32_bf16 v[80:83], v[144:147], v[200:203], 0
	v_mfma_f32_16x16x32_bf16 v[76:79], v[140:143], v[200:203], 0
	v_mfma_f32_16x16x32_bf16 v[68:71], v[140:143], v[208:211], 0
	v_mfma_f32_16x16x32_bf16 v[72:75], v[144:147], v[208:211], 0
	s_nop 0
	v_mfma_f32_16x16x32_bf16 v[96:99], v[136:139], v[168:171], v[96:99]
	v_mfma_f32_16x16x32_bf16 v[92:95], v[132:135], v[168:171], v[92:95]
	v_mfma_f32_16x16x32_bf16 v[84:87], v[132:135], v[182:185], v[84:87]
	v_mfma_f32_16x16x32_bf16 v[88:91], v[136:139], v[182:185], v[88:91]
	v_mfma_f32_16x16x32_bf16 v[80:83], v[136:139], v[204:207], v[80:83]
	v_mfma_f32_16x16x32_bf16 v[76:79], v[132:135], v[204:207], v[76:79]
	v_mfma_f32_16x16x32_bf16 v[68:71], v[132:135], v[212:215], v[68:71]
	v_mfma_f32_16x16x32_bf16 v[72:75], v[136:139], v[212:215], v[72:75]
	s_setprio 0
	s_barrier
	v_lshl_add_u64 v[164:165], s[30:31], 0, v[34:35]
	s_add_i32 s64, s64, s42
	v_lshl_add_u64 v[166:167], v[164:165], 0, s[28:29]
	s_mov_b32 m0, s64
	s_add_i32 s65, s64, 0x2000
	ds_read_b128 v[178:181], v223 offset:16384
	ds_read_b128 v[182:185], v223 offset:17408
	ds_read_b128 v[200:203], v223 offset:18432
	ds_read_b128 v[204:207], v223 offset:19456
	ds_read_b128 v[208:211], v223 offset:20480
	ds_read_b128 v[212:215], v223 offset:21504
	ds_read_b128 v[216:219], v223 offset:22528
	ds_read_b128 v[224:227], v223 offset:23552
	global_load_lds_dwordx4 v[166:167], off
	v_lshl_add_u64 v[166:167], s[30:31], 0, v[190:191]
	s_add_u32 s40, s30, 0x40100
	v_lshl_add_u64 v[168:169], v[166:167], 0, s[28:29]
	s_mov_b32 m0, s65
	s_addc_u32 s41, s31, 0
	s_add_i32 s66, s66, s42
	global_load_lds_dwordx4 v[168:169], off
	v_lshl_add_u64 v[168:169], s[40:41], 0, v[34:35]
	s_mov_b32 m0, s66
	s_add_i32 s67, s66, 0x2000
	global_load_lds_dwordx4 v[168:169], off
	v_lshl_add_u64 v[168:169], s[40:41], 0, v[190:191]
	s_mov_b32 m0, s67
	s_nop 0
	global_load_lds_dwordx4 v[168:169], off
	v_lshl_add_u64 v[168:169], s[36:37], 0, v[194:195]
	v_lshl_add_u64 v[170:171], v[168:169], 0, s[28:29]
	s_mov_b32 m0, s43
	s_nop 0
	global_load_lds_dwordx4 v[170:171], off
	v_lshl_add_u64 v[170:171], s[36:37], 0, v[192:193]
	v_lshl_add_u64 v[174:175], v[170:171], 0, s[28:29]
	s_mov_b32 m0, s44
	s_nop 0
	global_load_lds_dwordx4 v[174:175], off
	s_waitcnt vmcnt(8)
	s_waitcnt lgkmcnt(0)
	s_barrier
	s_setprio 1
	s_waitcnt lgkmcnt(0)
	v_mfma_f32_16x16x32_bf16 v[64:67], v[160:163], v[178:181], 0
	v_mfma_f32_16x16x32_bf16 v[60:63], v[156:159], v[178:181], 0
	v_mfma_f32_16x16x32_bf16 v[52:55], v[156:159], v[200:203], 0
	v_mfma_f32_16x16x32_bf16 v[56:59], v[160:163], v[200:203], 0
	v_mfma_f32_16x16x32_bf16 v[48:51], v[160:163], v[208:211], 0
	v_mfma_f32_16x16x32_bf16 v[44:47], v[156:159], v[208:211], 0
	v_mfma_f32_16x16x32_bf16 v[36:39], v[156:159], v[216:219], 0
	v_mfma_f32_16x16x32_bf16 v[40:43], v[160:163], v[216:219], 0
	s_nop 0
	v_mfma_f32_16x16x32_bf16 v[64:67], v[152:155], v[182:185], v[64:67]
	v_mfma_f32_16x16x32_bf16 v[60:63], v[148:151], v[182:185], v[60:63]
	v_mfma_f32_16x16x32_bf16 v[52:55], v[148:151], v[204:207], v[52:55]
	v_mfma_f32_16x16x32_bf16 v[56:59], v[152:155], v[204:207], v[56:59]
	v_mfma_f32_16x16x32_bf16 v[48:51], v[152:155], v[212:215], v[48:51]
	v_mfma_f32_16x16x32_bf16 v[44:47], v[148:151], v[212:215], v[44:47]
	v_mfma_f32_16x16x32_bf16 v[36:39], v[148:151], v[224:227], v[36:39]
	v_mfma_f32_16x16x32_bf16 v[40:43], v[152:155], v[224:227], v[40:43]
	s_setprio 0
	s_setprio 1
	v_mfma_f32_16x16x32_bf16 v[30:33], v[144:147], v[178:181], 0
	v_mfma_f32_16x16x32_bf16 v[26:29], v[140:143], v[178:181], 0
	v_mfma_f32_16x16x32_bf16 v[18:21], v[140:143], v[200:203], 0
	v_mfma_f32_16x16x32_bf16 v[22:25], v[144:147], v[200:203], 0
	v_mfma_f32_16x16x32_bf16 v[14:17], v[144:147], v[208:211], 0
	v_mfma_f32_16x16x32_bf16 v[10:13], v[140:143], v[208:211], 0
	v_mfma_f32_16x16x32_bf16 v[2:5], v[140:143], v[216:219], 0
	v_mfma_f32_16x16x32_bf16 v[6:9], v[144:147], v[216:219], 0
	s_nop 0
	v_mfma_f32_16x16x32_bf16 v[30:33], v[136:139], v[182:185], v[30:33]
	v_mfma_f32_16x16x32_bf16 v[26:29], v[132:135], v[182:185], v[26:29]
	v_mfma_f32_16x16x32_bf16 v[18:21], v[132:135], v[204:207], v[18:21]
	v_mfma_f32_16x16x32_bf16 v[22:25], v[136:139], v[204:207], v[22:25]
	v_mfma_f32_16x16x32_bf16 v[14:17], v[136:139], v[212:215], v[14:17]
	v_mfma_f32_16x16x32_bf16 v[10:13], v[132:135], v[212:215], v[10:13]
	v_mfma_f32_16x16x32_bf16 v[2:5], v[132:135], v[224:227], v[2:5]
	v_mfma_f32_16x16x32_bf16 v[6:9], v[136:139], v[224:227], v[6:9]
	s_setprio 0
	s_barrier
	s_add_i32 s68, 0, 0x18000
	s_add_i32 s70, 0, 0x1c000
	v_add_u32_e32 v132, s68, v222
	v_add_u32_e32 v133, s70, v222
	ds_read_b128 v[134:137], v132
	ds_read_b128 v[138:141], v132 offset:1024
	ds_read_b128 v[142:145], v132 offset:2048
	ds_read_b128 v[146:149], v132 offset:3072
	ds_read_b128 v[150:153], v133
	ds_read_b128 v[154:157], v133 offset:1024
	ds_read_b128 v[158:161], v133 offset:2048
	ds_read_b128 v[178:181], v133 offset:3072
	s_add_u32 s40, s36, 0x40100
	s_addc_u32 s41, s37, 0
	s_mov_b32 m0, s45
	v_lshl_add_u64 v[162:163], s[40:41], 0, v[194:195]
	ds_read_b128 v[182:185], v223 offset:32768
	ds_read_b128 v[200:203], v223 offset:33792
	ds_read_b128 v[204:207], v223 offset:34816
	ds_read_b128 v[208:211], v223 offset:35840
	ds_read_b128 v[212:215], v223 offset:36864
	ds_read_b128 v[216:219], v223 offset:37888
	ds_read_b128 v[224:227], v223 offset:38912
	ds_read_b128 v[228:231], v223 offset:39936
	global_load_lds_dwordx4 v[162:163], off
	v_lshl_add_u64 v[162:163], s[40:41], 0, v[192:193]
	s_mov_b32 m0, s46
	s_nop 0
	global_load_lds_dwordx4 v[162:163], off
	s_waitcnt vmcnt(8)
	s_waitcnt lgkmcnt(0)
	s_barrier
	s_setprio 1
	s_waitcnt lgkmcnt(0)
	v_mfma_f32_16x16x32_bf16 v[128:131], v[134:137], v[182:185], v[128:131]
	v_mfma_f32_16x16x32_bf16 v[124:127], v[142:145], v[182:185], v[124:127]
	v_mfma_f32_16x16x32_bf16 v[116:119], v[142:145], v[204:207], v[116:119]
	v_mfma_f32_16x16x32_bf16 v[120:123], v[134:137], v[204:207], v[120:123]
	v_mfma_f32_16x16x32_bf16 v[112:115], v[134:137], v[212:215], v[112:115]
	v_mfma_f32_16x16x32_bf16 v[108:111], v[142:145], v[212:215], v[108:111]
	v_mfma_f32_16x16x32_bf16 v[100:103], v[142:145], v[224:227], v[100:103]
	v_mfma_f32_16x16x32_bf16 v[104:107], v[134:137], v[224:227], v[104:107]
	v_mfma_f32_16x16x32_bf16 v[128:131], v[138:141], v[200:203], v[128:131]
	v_mfma_f32_16x16x32_bf16 v[124:127], v[146:149], v[200:203], v[124:127]
	v_mfma_f32_16x16x32_bf16 v[116:119], v[146:149], v[208:211], v[116:119]
	v_mfma_f32_16x16x32_bf16 v[120:123], v[138:141], v[208:211], v[120:123]
	v_mfma_f32_16x16x32_bf16 v[112:115], v[138:141], v[216:219], v[112:115]
	v_mfma_f32_16x16x32_bf16 v[108:111], v[146:149], v[216:219], v[108:111]
	v_mfma_f32_16x16x32_bf16 v[100:103], v[146:149], v[228:231], v[100:103]
	v_mfma_f32_16x16x32_bf16 v[104:107], v[138:141], v[228:231], v[104:107]
	s_setprio 0
	s_setprio 1
	v_mfma_f32_16x16x32_bf16 v[96:99], v[150:153], v[182:185], v[96:99]
	v_mfma_f32_16x16x32_bf16 v[92:95], v[158:161], v[182:185], v[92:95]
	v_mfma_f32_16x16x32_bf16 v[84:87], v[158:161], v[204:207], v[84:87]
	v_mfma_f32_16x16x32_bf16 v[88:91], v[150:153], v[204:207], v[88:91]
	v_mfma_f32_16x16x32_bf16 v[80:83], v[150:153], v[212:215], v[80:83]
	v_mfma_f32_16x16x32_bf16 v[76:79], v[158:161], v[212:215], v[76:79]
	v_mfma_f32_16x16x32_bf16 v[68:71], v[158:161], v[224:227], v[68:71]
	v_mfma_f32_16x16x32_bf16 v[72:75], v[150:153], v[224:227], v[72:75]
	v_mfma_f32_16x16x32_bf16 v[96:99], v[154:157], v[200:203], v[96:99]
	v_mfma_f32_16x16x32_bf16 v[92:95], v[178:181], v[200:203], v[92:95]
	v_mfma_f32_16x16x32_bf16 v[84:87], v[178:181], v[208:211], v[84:87]
	v_mfma_f32_16x16x32_bf16 v[88:91], v[154:157], v[208:211], v[88:91]
	v_mfma_f32_16x16x32_bf16 v[80:83], v[154:157], v[216:219], v[80:83]
	v_mfma_f32_16x16x32_bf16 v[76:79], v[178:181], v[216:219], v[76:79]
	v_mfma_f32_16x16x32_bf16 v[68:71], v[178:181], v[228:231], v[68:71]
	v_mfma_f32_16x16x32_bf16 v[72:75], v[154:157], v[228:231], v[72:75]
	s_setprio 0
	s_barrier
	s_add_i32 s68, s68, s42
	s_mov_b64 s[24:25], 0x180
	s_add_i32 s69, s68, 0x2000
	v_lshl_add_u64 v[162:163], v[164:165], 0, s[24:25]
	s_mov_b32 m0, s68
	s_add_u32 s40, s30, 0x40180
	ds_read_b128 v[182:185], v223 offset:49152
	ds_read_b128 v[200:203], v223 offset:50176
	ds_read_b128 v[204:207], v223 offset:51200
	ds_read_b128 v[208:211], v223 offset:52224
	ds_read_b128 v[212:215], v223 offset:53248
	ds_read_b128 v[216:219], v223 offset:54272
	ds_read_b128 v[224:227], v223 offset:55296
	ds_read_b128 v[228:231], v223 offset:56320
	global_load_lds_dwordx4 v[162:163], off
	v_lshl_add_u64 v[162:163], v[166:167], 0, s[24:25]
	s_mov_b32 m0, s69
	s_addc_u32 s41, s31, 0
	s_add_i32 s70, s70, s42
	global_load_lds_dwordx4 v[162:163], off
	v_lshl_add_u64 v[162:163], s[40:41], 0, v[34:35]
	s_mov_b32 m0, s70
	s_add_i32 s71, s70, 0x2000
	global_load_lds_dwordx4 v[162:163], off
	v_lshl_add_u64 v[162:163], s[40:41], 0, v[190:191]
	s_mov_b32 m0, s71
	s_nop 0
	global_load_lds_dwordx4 v[162:163], off
	v_lshl_add_u64 v[162:163], v[168:169], 0, s[24:25]
	s_mov_b32 m0, s51
	s_nop 0
	global_load_lds_dwordx4 v[162:163], off
	v_lshl_add_u64 v[162:163], v[170:171], 0, s[24:25]
	s_mov_b32 m0, s52
	s_nop 0
	global_load_lds_dwordx4 v[162:163], off
	s_waitcnt vmcnt(8)
	s_waitcnt lgkmcnt(0)
	s_barrier
	s_setprio 1
	s_waitcnt lgkmcnt(0)
	v_mfma_f32_16x16x32_bf16 v[64:67], v[134:137], v[182:185], v[64:67]
	v_mfma_f32_16x16x32_bf16 v[60:63], v[142:145], v[182:185], v[60:63]
	v_mfma_f32_16x16x32_bf16 v[52:55], v[142:145], v[204:207], v[52:55]
	v_mfma_f32_16x16x32_bf16 v[56:59], v[134:137], v[204:207], v[56:59]
	v_mfma_f32_16x16x32_bf16 v[48:51], v[134:137], v[212:215], v[48:51]
	v_mfma_f32_16x16x32_bf16 v[44:47], v[142:145], v[212:215], v[44:47]
	v_mfma_f32_16x16x32_bf16 v[36:39], v[142:145], v[224:227], v[36:39]
	v_mfma_f32_16x16x32_bf16 v[40:43], v[134:137], v[224:227], v[40:43]
	v_mfma_f32_16x16x32_bf16 v[64:67], v[138:141], v[200:203], v[64:67]
	v_mfma_f32_16x16x32_bf16 v[60:63], v[146:149], v[200:203], v[60:63]
	v_mfma_f32_16x16x32_bf16 v[52:55], v[146:149], v[208:211], v[52:55]
	v_mfma_f32_16x16x32_bf16 v[56:59], v[138:141], v[208:211], v[56:59]
	v_mfma_f32_16x16x32_bf16 v[48:51], v[138:141], v[216:219], v[48:51]
	v_mfma_f32_16x16x32_bf16 v[44:47], v[146:149], v[216:219], v[44:47]
	v_mfma_f32_16x16x32_bf16 v[36:39], v[146:149], v[228:231], v[36:39]
	v_mfma_f32_16x16x32_bf16 v[40:43], v[138:141], v[228:231], v[40:43]
	s_setprio 0
	s_setprio 1
	v_mfma_f32_16x16x32_bf16 v[30:33], v[150:153], v[182:185], v[30:33]
	v_mfma_f32_16x16x32_bf16 v[26:29], v[158:161], v[182:185], v[26:29]
	v_mfma_f32_16x16x32_bf16 v[18:21], v[158:161], v[204:207], v[18:21]
	v_mfma_f32_16x16x32_bf16 v[22:25], v[150:153], v[204:207], v[22:25]
	v_mfma_f32_16x16x32_bf16 v[14:17], v[150:153], v[212:215], v[14:17]
	v_mfma_f32_16x16x32_bf16 v[10:13], v[158:161], v[212:215], v[10:13]
	v_mfma_f32_16x16x32_bf16 v[2:5], v[158:161], v[224:227], v[2:5]
	v_mfma_f32_16x16x32_bf16 v[6:9], v[150:153], v[224:227], v[6:9]
	v_mfma_f32_16x16x32_bf16 v[30:33], v[154:157], v[200:203], v[30:33]
	v_mfma_f32_16x16x32_bf16 v[26:29], v[178:181], v[200:203], v[26:29]
	v_mfma_f32_16x16x32_bf16 v[18:21], v[178:181], v[208:211], v[18:21]
	v_mfma_f32_16x16x32_bf16 v[22:25], v[154:157], v[208:211], v[22:25]
	v_mfma_f32_16x16x32_bf16 v[14:17], v[154:157], v[216:219], v[14:17]
	v_mfma_f32_16x16x32_bf16 v[10:13], v[178:181], v[216:219], v[10:13]
	v_mfma_f32_16x16x32_bf16 v[2:5], v[178:181], v[228:231], v[2:5]
	v_mfma_f32_16x16x32_bf16 v[6:9], v[154:157], v[228:231], v[6:9]
	s_setprio 0
	s_barrier
	s_add_u32 s36, s36, 0x40180
	s_addc_u32 s37, s37, 0
	s_add_u32 s72, s30, 0x200
	s_addc_u32 s73, s31, 0
	s_mov_b32 s74, 0
.LBB0_541:
	ds_read_b128 v[134:137], v172
	ds_read_b128 v[138:141], v172 offset:1024
	ds_read_b128 v[142:145], v172 offset:2048
	ds_read_b128 v[146:149], v172 offset:3072
	ds_read_b128 v[150:153], v173
	ds_read_b128 v[154:157], v173 offset:1024
	ds_read_b128 v[158:161], v173 offset:2048
	ds_read_b128 v[162:165], v173 offset:3072
	s_add_u32 s14, s36, 0xfffc0080
	s_addc_u32 s30, s37, -1
	s_cmp_eq_u32 s74, 12
	s_cselect_b32 s41, s58, s30
	s_cselect_b32 s40, s59, s14
	s_cselect_b32 s31, s60, s73
	s_cselect_b32 s30, s61, s72
	s_mov_b32 m0, s62
	v_lshl_add_u64 v[170:171], s[36:37], 0, v[196:197]
	ds_read_b128 v[166:169], v223
	ds_read_b128 v[178:181], v223 offset:1024
	ds_read_b128 v[182:185], v223 offset:2048
	ds_read_b128 v[200:203], v223 offset:3072
	ds_read_b128 v[204:207], v223 offset:4096
	ds_read_b128 v[208:211], v223 offset:5120
	ds_read_b128 v[212:215], v223 offset:6144
	ds_read_b128 v[216:219], v223 offset:7168
	global_load_lds_dwordx4 v[170:171], off
	v_lshl_add_u64 v[170:171], s[36:37], 0, v[198:199]
	s_mov_b32 m0, s63
	s_nop 0
	global_load_lds_dwordx4 v[170:171], off
	s_waitcnt vmcnt(8)
	s_waitcnt lgkmcnt(0)
	s_barrier
	s_setprio 1
	s_waitcnt lgkmcnt(0)
	v_mfma_f32_16x16x32_bf16 v[128:131], v[134:137], v[166:169], v[128:131]
	v_mfma_f32_16x16x32_bf16 v[124:127], v[142:145], v[166:169], v[124:127]
	v_mfma_f32_16x16x32_bf16 v[116:119], v[142:145], v[182:185], v[116:119]
	v_mfma_f32_16x16x32_bf16 v[120:123], v[134:137], v[182:185], v[120:123]
	v_mfma_f32_16x16x32_bf16 v[112:115], v[134:137], v[204:207], v[112:115]
	v_mfma_f32_16x16x32_bf16 v[108:111], v[142:145], v[204:207], v[108:111]
	v_mfma_f32_16x16x32_bf16 v[100:103], v[142:145], v[212:215], v[100:103]
	v_mfma_f32_16x16x32_bf16 v[104:107], v[134:137], v[212:215], v[104:107]
	v_mfma_f32_16x16x32_bf16 v[128:131], v[138:141], v[178:181], v[128:131]
	v_mfma_f32_16x16x32_bf16 v[124:127], v[146:149], v[178:181], v[124:127]
	v_mfma_f32_16x16x32_bf16 v[116:119], v[146:149], v[200:203], v[116:119]
	v_mfma_f32_16x16x32_bf16 v[120:123], v[138:141], v[200:203], v[120:123]
	v_mfma_f32_16x16x32_bf16 v[112:115], v[138:141], v[208:211], v[112:115]
	v_mfma_f32_16x16x32_bf16 v[108:111], v[146:149], v[208:211], v[108:111]
	v_mfma_f32_16x16x32_bf16 v[100:103], v[146:149], v[216:219], v[100:103]
	v_mfma_f32_16x16x32_bf16 v[104:107], v[138:141], v[216:219], v[104:107]
	s_setprio 0
	s_setprio 1
	v_mfma_f32_16x16x32_bf16 v[96:99], v[150:153], v[166:169], v[96:99]
	v_mfma_f32_16x16x32_bf16 v[92:95], v[158:161], v[166:169], v[92:95]
	v_mfma_f32_16x16x32_bf16 v[84:87], v[158:161], v[182:185], v[84:87]
	v_mfma_f32_16x16x32_bf16 v[88:91], v[150:153], v[182:185], v[88:91]
	v_mfma_f32_16x16x32_bf16 v[80:83], v[150:153], v[204:207], v[80:83]
	v_mfma_f32_16x16x32_bf16 v[76:79], v[158:161], v[204:207], v[76:79]
	v_mfma_f32_16x16x32_bf16 v[68:71], v[158:161], v[212:215], v[68:71]
	v_mfma_f32_16x16x32_bf16 v[72:75], v[150:153], v[212:215], v[72:75]
	v_mfma_f32_16x16x32_bf16 v[96:99], v[154:157], v[178:181], v[96:99]
	v_mfma_f32_16x16x32_bf16 v[92:95], v[162:165], v[178:181], v[92:95]
	v_mfma_f32_16x16x32_bf16 v[84:87], v[162:165], v[200:203], v[84:87]
	v_mfma_f32_16x16x32_bf16 v[88:91], v[154:157], v[200:203], v[88:91]
	v_mfma_f32_16x16x32_bf16 v[80:83], v[154:157], v[208:211], v[80:83]
	v_mfma_f32_16x16x32_bf16 v[76:79], v[162:165], v[208:211], v[76:79]
	v_mfma_f32_16x16x32_bf16 v[68:71], v[162:165], v[216:219], v[68:71]
	v_mfma_f32_16x16x32_bf16 v[72:75], v[154:157], v[216:219], v[72:75]
	s_setprio 0
	s_barrier
	s_mov_b32 m0, s64
	v_lshl_add_u64 v[170:171], s[30:31], 0, v[34:35]
	s_add_u32 s76, s30, 0x40000
	ds_read_b128 v[166:169], v223 offset:16384
	ds_read_b128 v[178:181], v223 offset:17408
	ds_read_b128 v[182:185], v223 offset:18432
	ds_read_b128 v[200:203], v223 offset:19456
	ds_read_b128 v[204:207], v223 offset:20480
	ds_read_b128 v[208:211], v223 offset:21504
	ds_read_b128 v[212:215], v223 offset:22528
	ds_read_b128 v[216:219], v223 offset:23552
	global_load_lds_dwordx4 v[170:171], off
	v_lshl_add_u64 v[174:175], s[30:31], 0, v[190:191]
	s_mov_b32 m0, s65
	s_addc_u32 s77, s31, 0
	global_load_lds_dwordx4 v[174:175], off
	v_lshl_add_u64 v[224:225], s[76:77], 0, v[34:35]
	s_mov_b32 m0, s66
	v_lshl_add_u64 v[226:227], s[40:41], 0, v[192:193]
	global_load_lds_dwordx4 v[224:225], off
	v_lshl_add_u64 v[224:225], s[76:77], 0, v[190:191]
	s_mov_b32 m0, s67
	s_nop 0
	global_load_lds_dwordx4 v[224:225], off
	v_lshl_add_u64 v[224:225], s[40:41], 0, v[194:195]
	s_mov_b32 m0, s43
	s_nop 0
	global_load_lds_dwordx4 v[224:225], off
	s_mov_b32 m0, s44
	s_nop 0
	global_load_lds_dwordx4 v[226:227], off
	s_waitcnt vmcnt(8)
	s_waitcnt lgkmcnt(0)
	s_barrier
	s_setprio 1
	s_waitcnt lgkmcnt(0)
	v_mfma_f32_16x16x32_bf16 v[64:67], v[134:137], v[166:169], v[64:67]
	v_mfma_f32_16x16x32_bf16 v[60:63], v[142:145], v[166:169], v[60:63]
	v_mfma_f32_16x16x32_bf16 v[52:55], v[142:145], v[182:185], v[52:55]
	v_mfma_f32_16x16x32_bf16 v[56:59], v[134:137], v[182:185], v[56:59]
	v_mfma_f32_16x16x32_bf16 v[48:51], v[134:137], v[204:207], v[48:51]
	v_mfma_f32_16x16x32_bf16 v[44:47], v[142:145], v[204:207], v[44:47]
	v_mfma_f32_16x16x32_bf16 v[36:39], v[142:145], v[212:215], v[36:39]
	v_mfma_f32_16x16x32_bf16 v[40:43], v[134:137], v[212:215], v[40:43]
	v_mfma_f32_16x16x32_bf16 v[64:67], v[138:141], v[178:181], v[64:67]
	v_mfma_f32_16x16x32_bf16 v[60:63], v[146:149], v[178:181], v[60:63]
	v_mfma_f32_16x16x32_bf16 v[52:55], v[146:149], v[200:203], v[52:55]
	v_mfma_f32_16x16x32_bf16 v[56:59], v[138:141], v[200:203], v[56:59]
	v_mfma_f32_16x16x32_bf16 v[48:51], v[138:141], v[208:211], v[48:51]
	v_mfma_f32_16x16x32_bf16 v[44:47], v[146:149], v[208:211], v[44:47]
	v_mfma_f32_16x16x32_bf16 v[36:39], v[146:149], v[216:219], v[36:39]
	v_mfma_f32_16x16x32_bf16 v[40:43], v[138:141], v[216:219], v[40:43]
	s_setprio 0
	s_setprio 1
	v_mfma_f32_16x16x32_bf16 v[30:33], v[150:153], v[166:169], v[30:33]
	v_mfma_f32_16x16x32_bf16 v[26:29], v[158:161], v[166:169], v[26:29]
	v_mfma_f32_16x16x32_bf16 v[18:21], v[158:161], v[182:185], v[18:21]
	v_mfma_f32_16x16x32_bf16 v[22:25], v[150:153], v[182:185], v[22:25]
	v_mfma_f32_16x16x32_bf16 v[14:17], v[150:153], v[204:207], v[14:17]
	v_mfma_f32_16x16x32_bf16 v[10:13], v[158:161], v[204:207], v[10:13]
	v_mfma_f32_16x16x32_bf16 v[2:5], v[158:161], v[212:215], v[2:5]
	v_mfma_f32_16x16x32_bf16 v[6:9], v[150:153], v[212:215], v[6:9]
	v_mfma_f32_16x16x32_bf16 v[30:33], v[154:157], v[178:181], v[30:33]
	v_mfma_f32_16x16x32_bf16 v[26:29], v[162:165], v[178:181], v[26:29]
	v_mfma_f32_16x16x32_bf16 v[18:21], v[162:165], v[200:203], v[18:21]
	v_mfma_f32_16x16x32_bf16 v[22:25], v[154:157], v[200:203], v[22:25]
	v_mfma_f32_16x16x32_bf16 v[14:17], v[154:157], v[208:211], v[14:17]
	v_mfma_f32_16x16x32_bf16 v[10:13], v[162:165], v[208:211], v[10:13]
	v_mfma_f32_16x16x32_bf16 v[2:5], v[162:165], v[216:219], v[2:5]
	v_mfma_f32_16x16x32_bf16 v[6:9], v[154:157], v[216:219], v[6:9]
	s_setprio 0
	s_barrier
	ds_read_b128 v[134:137], v132
	ds_read_b128 v[138:141], v132 offset:1024
	ds_read_b128 v[142:145], v132 offset:2048
	ds_read_b128 v[146:149], v132 offset:3072
	ds_read_b128 v[150:153], v133
	ds_read_b128 v[154:157], v133 offset:1024
	ds_read_b128 v[158:161], v133 offset:2048
	ds_read_b128 v[162:165], v133 offset:3072
	s_add_u32 s40, s40, 0x40000
	s_addc_u32 s41, s41, 0
	s_mov_b32 m0, s45
	v_lshl_add_u64 v[228:229], s[40:41], 0, v[194:195]
	ds_read_b128 v[166:169], v223 offset:32768
	ds_read_b128 v[178:181], v223 offset:33792
	ds_read_b128 v[182:185], v223 offset:34816
	ds_read_b128 v[200:203], v223 offset:35840
	ds_read_b128 v[204:207], v223 offset:36864
	ds_read_b128 v[208:211], v223 offset:37888
	ds_read_b128 v[212:215], v223 offset:38912
	ds_read_b128 v[216:219], v223 offset:39936
	global_load_lds_dwordx4 v[228:229], off
	v_lshl_add_u64 v[228:229], s[40:41], 0, v[192:193]
	s_mov_b32 m0, s46
	s_nop 0
	global_load_lds_dwordx4 v[228:229], off
	s_waitcnt vmcnt(8)
	s_waitcnt lgkmcnt(0)
	s_barrier
	s_setprio 1
	s_waitcnt lgkmcnt(0)
	v_mfma_f32_16x16x32_bf16 v[128:131], v[134:137], v[166:169], v[128:131]
	v_mfma_f32_16x16x32_bf16 v[124:127], v[142:145], v[166:169], v[124:127]
	v_mfma_f32_16x16x32_bf16 v[116:119], v[142:145], v[182:185], v[116:119]
	v_mfma_f32_16x16x32_bf16 v[120:123], v[134:137], v[182:185], v[120:123]
	v_mfma_f32_16x16x32_bf16 v[112:115], v[134:137], v[204:207], v[112:115]
	v_mfma_f32_16x16x32_bf16 v[108:111], v[142:145], v[204:207], v[108:111]
	v_mfma_f32_16x16x32_bf16 v[100:103], v[142:145], v[212:215], v[100:103]
	v_mfma_f32_16x16x32_bf16 v[104:107], v[134:137], v[212:215], v[104:107]
	v_mfma_f32_16x16x32_bf16 v[128:131], v[138:141], v[178:181], v[128:131]
	v_mfma_f32_16x16x32_bf16 v[124:127], v[146:149], v[178:181], v[124:127]
	v_mfma_f32_16x16x32_bf16 v[116:119], v[146:149], v[200:203], v[116:119]
	v_mfma_f32_16x16x32_bf16 v[120:123], v[138:141], v[200:203], v[120:123]
	v_mfma_f32_16x16x32_bf16 v[112:115], v[138:141], v[208:211], v[112:115]
	v_mfma_f32_16x16x32_bf16 v[108:111], v[146:149], v[208:211], v[108:111]
	v_mfma_f32_16x16x32_bf16 v[100:103], v[146:149], v[216:219], v[100:103]
	v_mfma_f32_16x16x32_bf16 v[104:107], v[138:141], v[216:219], v[104:107]
	s_setprio 0
	s_setprio 1
	v_mfma_f32_16x16x32_bf16 v[96:99], v[150:153], v[166:169], v[96:99]
	v_mfma_f32_16x16x32_bf16 v[92:95], v[158:161], v[166:169], v[92:95]
	v_mfma_f32_16x16x32_bf16 v[84:87], v[158:161], v[182:185], v[84:87]
	v_mfma_f32_16x16x32_bf16 v[88:91], v[150:153], v[182:185], v[88:91]
	v_mfma_f32_16x16x32_bf16 v[80:83], v[150:153], v[204:207], v[80:83]
	v_mfma_f32_16x16x32_bf16 v[76:79], v[158:161], v[204:207], v[76:79]
	v_mfma_f32_16x16x32_bf16 v[68:71], v[158:161], v[212:215], v[68:71]
	v_mfma_f32_16x16x32_bf16 v[72:75], v[150:153], v[212:215], v[72:75]
	v_mfma_f32_16x16x32_bf16 v[96:99], v[154:157], v[178:181], v[96:99]
	v_mfma_f32_16x16x32_bf16 v[92:95], v[162:165], v[178:181], v[92:95]
	v_mfma_f32_16x16x32_bf16 v[84:87], v[162:165], v[200:203], v[84:87]
	v_mfma_f32_16x16x32_bf16 v[88:91], v[154:157], v[200:203], v[88:91]
	v_mfma_f32_16x16x32_bf16 v[80:83], v[154:157], v[208:211], v[80:83]
	v_mfma_f32_16x16x32_bf16 v[76:79], v[162:165], v[208:211], v[76:79]
	v_mfma_f32_16x16x32_bf16 v[68:71], v[162:165], v[216:219], v[68:71]
	v_mfma_f32_16x16x32_bf16 v[72:75], v[154:157], v[216:219], v[72:75]
	s_setprio 0
	s_barrier
	s_mov_b32 m0, s68
	v_lshl_add_u64 v[170:171], v[170:171], 0, s[18:19]
	s_add_u32 s30, s30, 0x40080
	ds_read_b128 v[166:169], v223 offset:49152
	ds_read_b128 v[178:181], v223 offset:50176
	ds_read_b128 v[182:185], v223 offset:51200
	ds_read_b128 v[200:203], v223 offset:52224
	ds_read_b128 v[204:207], v223 offset:53248
	ds_read_b128 v[208:211], v223 offset:54272
	ds_read_b128 v[212:215], v223 offset:55296
	ds_read_b128 v[216:219], v223 offset:56320
	global_load_lds_dwordx4 v[170:171], off
	v_lshl_add_u64 v[170:171], v[174:175], 0, s[18:19]
	s_mov_b32 m0, s69
	s_addc_u32 s31, s31, 0
	global_load_lds_dwordx4 v[170:171], off
	v_lshl_add_u64 v[170:171], s[30:31], 0, v[34:35]
	s_mov_b32 m0, s70
	s_nop 0
	global_load_lds_dwordx4 v[170:171], off
	v_lshl_add_u64 v[170:171], s[30:31], 0, v[190:191]
	s_mov_b32 m0, s71
	s_nop 0
	global_load_lds_dwordx4 v[170:171], off
	v_lshl_add_u64 v[170:171], v[224:225], 0, s[18:19]
	s_mov_b32 m0, s51
	s_nop 0
	global_load_lds_dwordx4 v[170:171], off
	v_lshl_add_u64 v[170:171], v[226:227], 0, s[18:19]
	s_mov_b32 m0, s52
	s_nop 0
	global_load_lds_dwordx4 v[170:171], off
	s_waitcnt vmcnt(8)
	s_waitcnt lgkmcnt(0)
	s_barrier
	s_setprio 1
	s_waitcnt lgkmcnt(0)
	v_mfma_f32_16x16x32_bf16 v[64:67], v[134:137], v[166:169], v[64:67]
	v_mfma_f32_16x16x32_bf16 v[60:63], v[142:145], v[166:169], v[60:63]
	v_mfma_f32_16x16x32_bf16 v[52:55], v[142:145], v[182:185], v[52:55]
	v_mfma_f32_16x16x32_bf16 v[56:59], v[134:137], v[182:185], v[56:59]
	v_mfma_f32_16x16x32_bf16 v[48:51], v[134:137], v[204:207], v[48:51]
	v_mfma_f32_16x16x32_bf16 v[44:47], v[142:145], v[204:207], v[44:47]
	v_mfma_f32_16x16x32_bf16 v[36:39], v[142:145], v[212:215], v[36:39]
	v_mfma_f32_16x16x32_bf16 v[40:43], v[134:137], v[212:215], v[40:43]
	v_mfma_f32_16x16x32_bf16 v[64:67], v[138:141], v[178:181], v[64:67]
	v_mfma_f32_16x16x32_bf16 v[60:63], v[146:149], v[178:181], v[60:63]
	v_mfma_f32_16x16x32_bf16 v[52:55], v[146:149], v[200:203], v[52:55]
	v_mfma_f32_16x16x32_bf16 v[56:59], v[138:141], v[200:203], v[56:59]
	v_mfma_f32_16x16x32_bf16 v[48:51], v[138:141], v[208:211], v[48:51]
	v_mfma_f32_16x16x32_bf16 v[44:47], v[146:149], v[208:211], v[44:47]
	v_mfma_f32_16x16x32_bf16 v[36:39], v[146:149], v[216:219], v[36:39]
	v_mfma_f32_16x16x32_bf16 v[40:43], v[138:141], v[216:219], v[40:43]
	s_setprio 0
	s_setprio 1
	v_mfma_f32_16x16x32_bf16 v[30:33], v[150:153], v[166:169], v[30:33]
	v_mfma_f32_16x16x32_bf16 v[26:29], v[158:161], v[166:169], v[26:29]
	v_mfma_f32_16x16x32_bf16 v[18:21], v[158:161], v[182:185], v[18:21]
	v_mfma_f32_16x16x32_bf16 v[22:25], v[150:153], v[182:185], v[22:25]
	v_mfma_f32_16x16x32_bf16 v[14:17], v[150:153], v[204:207], v[14:17]
	v_mfma_f32_16x16x32_bf16 v[10:13], v[158:161], v[204:207], v[10:13]
	v_mfma_f32_16x16x32_bf16 v[2:5], v[158:161], v[212:215], v[2:5]
	v_mfma_f32_16x16x32_bf16 v[6:9], v[150:153], v[212:215], v[6:9]
	v_mfma_f32_16x16x32_bf16 v[30:33], v[154:157], v[178:181], v[30:33]
	v_mfma_f32_16x16x32_bf16 v[26:29], v[162:165], v[178:181], v[26:29]
	v_mfma_f32_16x16x32_bf16 v[18:21], v[162:165], v[200:203], v[18:21]
	v_mfma_f32_16x16x32_bf16 v[22:25], v[154:157], v[200:203], v[22:25]
	v_mfma_f32_16x16x32_bf16 v[14:17], v[154:157], v[208:211], v[14:17]
	v_mfma_f32_16x16x32_bf16 v[10:13], v[162:165], v[208:211], v[10:13]
	v_mfma_f32_16x16x32_bf16 v[2:5], v[162:165], v[216:219], v[2:5]
	v_mfma_f32_16x16x32_bf16 v[6:9], v[154:157], v[216:219], v[6:9]
	s_setprio 0
	s_barrier
	s_add_i32 s74, s74, 2
	s_add_u32 s36, s36, 0x100
	s_addc_u32 s37, s37, 0
	s_add_u32 s72, s72, 0x100
	s_addc_u32 s73, s73, 0
	s_cmp_gt_u32 s74, 13
	s_cbranch_scc0 .LBB0_541
	v_readlane_b32 s74, v255, 3
	s_and_b64 vcc, exec, s[10:11]
	v_readlane_b32 s75, v255, 4
	s_mov_b32 s58, 0x19b00000
	v_readlane_b32 s59, v255, 10
	s_mov_b32 s60, 0xff61b1e6
	s_mov_b64 s[62:63], 0x800
	s_mov_b32 s64, 0x3b000000
	s_cbranch_vccz .LBB0_544
	s_barrier

.LBB0_819:
	s_add_u32 s81, s30, 0x200
	s_addc_u32 s82, s31, 0
	s_add_i32 s55, 0, 0x14000
	s_add_i32 s52, 0, 0x10000
	v_add_u32_e32 v199, s55, v167
	v_add_u32_e32 v200, s52, v167
	ds_read_b128 v[10:13], v199
	ds_read_b128 v[14:17], v199 offset:1024
	ds_read_b128 v[2:5], v199 offset:2048
	ds_read_b128 v[6:9], v199 offset:3072
	ds_read_b128 v[22:25], v200 offset:3072
	ds_read_b128 v[18:21], v200 offset:2048
	ds_read_b128 v[30:33], v200 offset:1024
	ds_read_b128 v[26:29], v200
	s_lshl_b32 s14, s80, 10
	s_add_i32 s83, s14, 0
	s_add_i32 s83, s83, 0x20400
	v_mov_b32_e32 v191, v35
	v_mov_b32_e32 v175, v35
	s_add_i32 s84, s69, 0xc000
	v_readlane_b32 s26, v253, 28
	s_mov_b32 m0, s84
	v_readlane_b32 s27, v253, 29
	s_add_i32 s53, s69, 0xe000
	ds_read_b128 v[202:205], v169
	ds_read_b128 v[206:209], v169 offset:1024
	ds_read_b128 v[222:225], v169 offset:2048
	ds_read_b128 v[226:229], v169 offset:3072
	ds_read_b128 v[230:233], v169 offset:4096
	ds_read_b128 v[234:237], v169 offset:5120
	ds_read_b128 v[238:241], v169 offset:6144
	ds_read_b128 v[242:245], v169 offset:7168
	global_load_lds_dwordx4 v190, s[26:27]
	s_mov_b32 m0, s53
	s_nop 0
	global_load_lds_dwordx4 v174, s[26:27]
	s_waitcnt vmcnt(8)
	s_waitcnt lgkmcnt(0)
	s_barrier
	s_setprio 1
	s_waitcnt lgkmcnt(0)
	v_mfma_f32_16x16x128_f8f6f4 v[160:163], v[26:33], v[202:209], 0
	v_mfma_f32_16x16x128_f8f6f4 v[156:159], v[18:25], v[202:209], 0
	v_mfma_f32_16x16x128_f8f6f4 v[148:151], v[18:25], v[222:229], 0
	v_mfma_f32_16x16x128_f8f6f4 v[152:155], v[26:33], v[222:229], 0
	v_mfma_f32_16x16x128_f8f6f4 v[144:147], v[26:33], v[230:237], 0
	v_mfma_f32_16x16x128_f8f6f4 v[140:143], v[18:25], v[230:237], 0
	v_mfma_f32_16x16x128_f8f6f4 v[132:135], v[18:25], v[238:245], 0
	v_mfma_f32_16x16x128_f8f6f4 v[136:139], v[26:33], v[238:245], 0
	s_setprio 0
	s_setprio 1
	v_mfma_f32_16x16x128_f8f6f4 v[128:131], v[10:17], v[202:209], 0
	v_mfma_f32_16x16x128_f8f6f4 v[124:127], v[2:9], v[202:209], 0
	v_mfma_f32_16x16x128_f8f6f4 v[116:119], v[2:9], v[222:229], 0
	v_mfma_f32_16x16x128_f8f6f4 v[120:123], v[10:17], v[222:229], 0
	v_mfma_f32_16x16x128_f8f6f4 v[112:115], v[10:17], v[230:237], 0
	v_mfma_f32_16x16x128_f8f6f4 v[108:111], v[2:9], v[230:237], 0
	v_mfma_f32_16x16x128_f8f6f4 v[100:103], v[2:9], v[238:245], 0
	v_mfma_f32_16x16x128_f8f6f4 v[104:107], v[10:17], v[238:245], 0
	s_setprio 0
	s_barrier
	s_add_i32 s52, s52, s68
	v_lshl_add_u64 v[194:195], s[30:31], 0, v[170:171]
	s_add_i32 s85, s52, 0x2000
	v_lshl_add_u64 v[178:179], v[194:195], 0, s[28:29]
	s_mov_b32 m0, s52
	v_lshl_add_u64 v[196:197], s[30:31], 0, v[172:173]
	s_add_u32 s36, s30, 0x20100
	ds_read_b128 v[202:205], v169 offset:16384
	ds_read_b128 v[206:209], v169 offset:17408
	ds_read_b128 v[222:225], v169 offset:18432
	ds_read_b128 v[226:229], v169 offset:19456
	ds_read_b128 v[230:233], v169 offset:20480
	ds_read_b128 v[234:237], v169 offset:21504
	ds_read_b128 v[238:241], v169 offset:22528
	ds_read_b128 v[242:245], v169 offset:23552
	global_load_lds_dwordx4 v[178:179], off
	v_lshl_add_u64 v[178:179], v[196:197], 0, s[28:29]
	s_mov_b32 m0, s85
	s_addc_u32 s37, s31, 0
	s_add_i32 s55, s55, s68
	global_load_lds_dwordx4 v[178:179], off
	v_lshl_add_u64 v[178:179], s[36:37], 0, v[170:171]
	s_mov_b32 m0, s55
	s_add_i32 s65, s55, 0x2000
	global_load_lds_dwordx4 v[178:179], off
	v_lshl_add_u64 v[178:179], s[36:37], 0, v[172:173]
	s_mov_b32 m0, s65
	v_readlane_b32 s26, v253, 37
	global_load_lds_dwordx4 v[178:179], off
	s_mov_b32 m0, s69
	v_readlane_b32 s27, v253, 38
	s_nop 4
	global_load_lds_dwordx4 v34, s[26:27]
	s_mov_b32 m0, s70
	s_nop 0
	global_load_lds_dwordx4 v192, s[26:27]
	s_waitcnt vmcnt(8)
	s_waitcnt lgkmcnt(0)
	s_barrier
	s_setprio 1
	s_waitcnt lgkmcnt(0)
	v_mfma_f32_16x16x128_f8f6f4 v[96:99], v[26:33], v[202:209], 0
	v_mfma_f32_16x16x128_f8f6f4 v[92:95], v[18:25], v[202:209], 0
	v_mfma_f32_16x16x128_f8f6f4 v[84:87], v[18:25], v[222:229], 0
	v_mfma_f32_16x16x128_f8f6f4 v[88:91], v[26:33], v[222:229], 0
	v_mfma_f32_16x16x128_f8f6f4 v[80:83], v[26:33], v[230:237], 0
	v_mfma_f32_16x16x128_f8f6f4 v[76:79], v[18:25], v[230:237], 0
	v_mfma_f32_16x16x128_f8f6f4 v[68:71], v[18:25], v[238:245], 0
	v_mfma_f32_16x16x128_f8f6f4 v[72:75], v[26:33], v[238:245], 0
	s_setprio 0
	s_setprio 1
	v_mfma_f32_16x16x128_f8f6f4 v[64:67], v[10:17], v[202:209], 0
	v_mfma_f32_16x16x128_f8f6f4 v[60:63], v[2:9], v[202:209], 0
	v_mfma_f32_16x16x128_f8f6f4 v[52:55], v[2:9], v[222:229], 0
	v_mfma_f32_16x16x128_f8f6f4 v[56:59], v[10:17], v[222:229], 0
	v_mfma_f32_16x16x128_f8f6f4 v[48:51], v[10:17], v[230:237], 0
	v_mfma_f32_16x16x128_f8f6f4 v[44:47], v[2:9], v[230:237], 0
	v_mfma_f32_16x16x128_f8f6f4 v[36:39], v[2:9], v[238:245], 0
	v_mfma_f32_16x16x128_f8f6f4 v[40:43], v[10:17], v[238:245], 0
	s_setprio 0
	s_barrier
	s_add_i32 s54, 0, 0x18000
	s_add_i32 s51, 0, 0x1c000
	v_add_u32_e32 v201, s54, v167
	v_add_u32_e32 v202, s51, v167
	ds_read_b128 v[26:29], v201
	ds_read_b128 v[30:33], v201 offset:1024
	ds_read_b128 v[18:21], v201 offset:2048
	ds_read_b128 v[22:25], v201 offset:3072
	ds_read_b128 v[10:13], v202
	ds_read_b128 v[14:17], v202 offset:1024
	ds_read_b128 v[2:5], v202 offset:2048
	ds_read_b128 v[6:9], v202 offset:3072
	s_mov_b32 m0, s71
	ds_read_b128 v[204:207], v169 offset:32768
	ds_read_b128 v[208:211], v169 offset:33792
	ds_read_b128 v[222:225], v169 offset:34816
	ds_read_b128 v[226:229], v169 offset:35840
	ds_read_b128 v[230:233], v169 offset:36864
	ds_read_b128 v[234:237], v169 offset:37888
	ds_read_b128 v[238:241], v169 offset:38912
	ds_read_b128 v[242:245], v169 offset:39936
	global_load_lds_dwordx4 v189, s[26:27]
	s_mov_b32 m0, s72
	s_nop 0
	global_load_lds_dwordx4 v198, s[26:27]
	s_waitcnt vmcnt(8)
	s_waitcnt lgkmcnt(0)
	s_barrier
	s_setprio 1
	s_waitcnt lgkmcnt(0)
	v_mfma_f32_16x16x128_f8f6f4 v[160:163], v[26:33], v[204:211], v[160:163]
	v_mfma_f32_16x16x128_f8f6f4 v[156:159], v[18:25], v[204:211], v[156:159]
	v_mfma_f32_16x16x128_f8f6f4 v[148:151], v[18:25], v[222:229], v[148:151]
	v_mfma_f32_16x16x128_f8f6f4 v[152:155], v[26:33], v[222:229], v[152:155]
	v_mfma_f32_16x16x128_f8f6f4 v[144:147], v[26:33], v[230:237], v[144:147]
	v_mfma_f32_16x16x128_f8f6f4 v[140:143], v[18:25], v[230:237], v[140:143]
	v_mfma_f32_16x16x128_f8f6f4 v[132:135], v[18:25], v[238:245], v[132:135]
	v_mfma_f32_16x16x128_f8f6f4 v[136:139], v[26:33], v[238:245], v[136:139]
	s_setprio 0
	s_setprio 1
	v_mfma_f32_16x16x128_f8f6f4 v[128:131], v[10:17], v[204:211], v[128:131]
	v_mfma_f32_16x16x128_f8f6f4 v[124:127], v[2:9], v[204:211], v[124:127]
	v_mfma_f32_16x16x128_f8f6f4 v[116:119], v[2:9], v[222:229], v[116:119]
	v_mfma_f32_16x16x128_f8f6f4 v[120:123], v[10:17], v[222:229], v[120:123]
	v_mfma_f32_16x16x128_f8f6f4 v[112:115], v[10:17], v[230:237], v[112:115]
	v_mfma_f32_16x16x128_f8f6f4 v[108:111], v[2:9], v[230:237], v[108:111]
	v_mfma_f32_16x16x128_f8f6f4 v[100:103], v[2:9], v[238:245], v[100:103]
	v_mfma_f32_16x16x128_f8f6f4 v[104:107], v[10:17], v[238:245], v[104:107]
	s_setprio 0
	s_barrier
	s_add_i32 s54, s54, s68
	s_mov_b64 s[26:27], 0x180
	s_add_i32 s50, s54, 0x2000
	v_lshl_add_u64 v[178:179], v[194:195], 0, s[26:27]
	s_mov_b32 m0, s54
	s_add_u32 s30, s30, 0x20180
	ds_read_b128 v[204:207], v169 offset:49152
	ds_read_b128 v[208:211], v169 offset:50176
	ds_read_b128 v[222:225], v169 offset:51200
	ds_read_b128 v[226:229], v169 offset:52224
	ds_read_b128 v[230:233], v169 offset:53248
	ds_read_b128 v[234:237], v169 offset:54272
	ds_read_b128 v[238:241], v169 offset:55296
	ds_read_b128 v[242:245], v169 offset:56320
	global_load_lds_dwordx4 v[178:179], off
	v_lshl_add_u64 v[178:179], v[196:197], 0, s[26:27]
	s_mov_b32 m0, s50
	s_addc_u32 s31, s31, 0
	s_add_i32 s51, s51, s68
	global_load_lds_dwordx4 v[178:179], off
	v_lshl_add_u64 v[178:179], s[30:31], 0, v[170:171]
	s_mov_b32 m0, s51
	s_add_i32 s64, s51, 0x2000
	global_load_lds_dwordx4 v[178:179], off
	v_lshl_add_u64 v[178:179], s[30:31], 0, v[172:173]
	s_mov_b32 m0, s64
	v_readlane_b32 s26, v253, 39
	global_load_lds_dwordx4 v[178:179], off
	s_mov_b32 m0, s75
	v_readlane_b32 s27, v253, 40
	s_nop 4
	global_load_lds_dwordx4 v34, s[26:27]
	s_mov_b32 m0, s76
	s_nop 0
	global_load_lds_dwordx4 v192, s[26:27]
	s_waitcnt vmcnt(8)
	s_waitcnt lgkmcnt(0)
	s_barrier
	s_setprio 1
	s_waitcnt lgkmcnt(0)
	v_mfma_f32_16x16x128_f8f6f4 v[96:99], v[26:33], v[204:211], v[96:99]
	v_mfma_f32_16x16x128_f8f6f4 v[92:95], v[18:25], v[204:211], v[92:95]
	v_mfma_f32_16x16x128_f8f6f4 v[84:87], v[18:25], v[222:229], v[84:87]
	v_mfma_f32_16x16x128_f8f6f4 v[88:91], v[26:33], v[222:229], v[88:91]
	v_mfma_f32_16x16x128_f8f6f4 v[80:83], v[26:33], v[230:237], v[80:83]
	v_mfma_f32_16x16x128_f8f6f4 v[76:79], v[18:25], v[230:237], v[76:79]
	v_mfma_f32_16x16x128_f8f6f4 v[68:71], v[18:25], v[238:245], v[68:71]
	v_mfma_f32_16x16x128_f8f6f4 v[72:75], v[26:33], v[238:245], v[72:75]
	s_setprio 0
	s_setprio 1
	v_mfma_f32_16x16x128_f8f6f4 v[64:67], v[10:17], v[204:211], v[64:67]
	v_mfma_f32_16x16x128_f8f6f4 v[60:63], v[2:9], v[204:211], v[60:63]
	v_mfma_f32_16x16x128_f8f6f4 v[52:55], v[2:9], v[222:229], v[52:55]
	v_mfma_f32_16x16x128_f8f6f4 v[56:59], v[10:17], v[222:229], v[56:59]
	v_mfma_f32_16x16x128_f8f6f4 v[48:51], v[10:17], v[230:237], v[48:51]
	v_mfma_f32_16x16x128_f8f6f4 v[44:47], v[2:9], v[230:237], v[44:47]
	v_mfma_f32_16x16x128_f8f6f4 v[36:39], v[2:9], v[238:245], v[36:39]
	v_mfma_f32_16x16x128_f8f6f4 v[40:43], v[10:17], v[238:245], v[40:43]
	s_setprio 0
	s_barrier
	v_lshl_add_u64 v[18:19], s[26:27], 0, v[174:175]
	v_lshl_add_u64 v[20:21], s[26:27], 0, v[190:191]
	s_mov_b32 s63, 0
	s_mov_b64 s[30:31], 0
	s_branch .LBB0_821
.LBB0_820:
	ds_read_b128 v[204:207], v200
	ds_read_b128 v[208:211], v200 offset:1024
	ds_read_b128 v[222:225], v200 offset:2048
	ds_read_b128 v[226:229], v200 offset:3072
	ds_read_b128 v[10:13], v199
	ds_read_b128 v[14:17], v199 offset:1024
	ds_read_b128 v[2:5], v199 offset:2048
	ds_read_b128 v[6:9], v199 offset:3072
	s_add_u32 s14, s30, 0x200
	s_addc_u32 s86, s31, 0
	s_and_b64 s[40:41], s[36:37], exec
	s_cselect_b32 s14, 0, s14
	s_cselect_b32 s41, 0, s86
	s_add_u32 s40, s20, s14
	s_addc_u32 s41, s21, s41
	s_add_u32 s14, s81, s30
	s_addc_u32 s86, s82, s31
	s_and_b64 s[36:37], s[36:37], exec
	s_cselect_b32 s37, s23, s86
	s_cselect_b32 s36, s22, s14
	s_mov_b32 m0, s84
	v_lshl_add_u64 v[30:31], v[20:21], 0, s[30:31]
	ds_read_b128 v[22:25], v169
	ds_read_b128 v[26:29], v169 offset:1024
	ds_read_b128 v[230:233], v169 offset:2048
	ds_read_b128 v[234:237], v169 offset:3072
	ds_read_b128 v[238:241], v169 offset:4096
	ds_read_b128 v[242:245], v169 offset:5120
	ds_read_b128 v[178:181], v169 offset:6144
	ds_read_b128 v[182:185], v169 offset:7168
	global_load_lds_dwordx4 v[30:31], off
	v_lshl_add_u64 v[30:31], v[18:19], 0, s[30:31]
	s_mov_b32 m0, s53
	s_nop 0
	global_load_lds_dwordx4 v[30:31], off
	s_waitcnt vmcnt(8)
	s_waitcnt lgkmcnt(0)
	s_barrier
	s_setprio 1
	s_waitcnt lgkmcnt(0)
	v_mfma_f32_16x16x128_f8f6f4 v[160:163], v[204:211], v[22:29], v[160:163]
	v_mfma_f32_16x16x128_f8f6f4 v[156:159], v[222:229], v[22:29], v[156:159]
	v_mfma_f32_16x16x128_f8f6f4 v[148:151], v[222:229], v[230:237], v[148:151]
	v_mfma_f32_16x16x128_f8f6f4 v[152:155], v[204:211], v[230:237], v[152:155]
	v_mfma_f32_16x16x128_f8f6f4 v[144:147], v[204:211], v[238:245], v[144:147]
	v_mfma_f32_16x16x128_f8f6f4 v[140:143], v[222:229], v[238:245], v[140:143]
	v_mfma_f32_16x16x128_f8f6f4 v[132:135], v[222:229], v[178:185], v[132:135]
	v_mfma_f32_16x16x128_f8f6f4 v[136:139], v[204:211], v[178:185], v[136:139]
	s_setprio 0
	s_setprio 1
	v_mfma_f32_16x16x128_f8f6f4 v[128:131], v[10:17], v[22:29], v[128:131]
	v_mfma_f32_16x16x128_f8f6f4 v[124:127], v[2:9], v[22:29], v[124:127]
	v_mfma_f32_16x16x128_f8f6f4 v[116:119], v[2:9], v[230:237], v[116:119]
	v_mfma_f32_16x16x128_f8f6f4 v[120:123], v[10:17], v[230:237], v[120:123]
	v_mfma_f32_16x16x128_f8f6f4 v[112:115], v[10:17], v[238:245], v[112:115]
	v_mfma_f32_16x16x128_f8f6f4 v[108:111], v[2:9], v[238:245], v[108:111]
	v_mfma_f32_16x16x128_f8f6f4 v[100:103], v[2:9], v[178:185], v[100:103]
	v_mfma_f32_16x16x128_f8f6f4 v[104:107], v[10:17], v[178:185], v[104:107]
	s_setprio 0
	s_barrier
	s_mov_b32 m0, s52
	v_lshl_add_u64 v[22:23], s[36:37], 0, v[170:171]
	s_add_u32 s86, s36, 0x20000
	ds_read_b128 v[178:181], v169 offset:16384
	ds_read_b128 v[182:185], v169 offset:17408
	ds_read_b128 v[230:233], v169 offset:18432
	ds_read_b128 v[234:237], v169 offset:19456
	ds_read_b128 v[238:241], v169 offset:20480
	ds_read_b128 v[242:245], v169 offset:21504
	ds_read_b128 v[212:215], v169 offset:22528
	ds_read_b128 v[216:219], v169 offset:23552
	global_load_lds_dwordx4 v[22:23], off
	v_lshl_add_u64 v[24:25], s[36:37], 0, v[172:173]
	s_mov_b32 m0, s85
	s_addc_u32 s87, s37, 0
	global_load_lds_dwordx4 v[24:25], off
	v_lshl_add_u64 v[26:27], s[86:87], 0, v[170:171]
	s_mov_b32 m0, s55
	v_mov_b32_e32 v193, v35
	global_load_lds_dwordx4 v[26:27], off
	v_lshl_add_u64 v[26:27], s[86:87], 0, v[172:173]
	s_mov_b32 m0, s65
	v_lshl_add_u64 v[28:29], s[40:41], 0, v[34:35]
	global_load_lds_dwordx4 v[26:27], off
	s_mov_b32 m0, s69
	v_lshl_add_u64 v[26:27], s[40:41], 0, v[192:193]
	global_load_lds_dwordx4 v34, s[40:41]
	s_mov_b32 m0, s70
	s_nop 0
	global_load_lds_dwordx4 v192, s[40:41]
	s_waitcnt vmcnt(8)
	s_waitcnt lgkmcnt(0)
	s_barrier
	s_setprio 1
	s_waitcnt lgkmcnt(0)
	v_mfma_f32_16x16x128_f8f6f4 v[96:99], v[204:211], v[178:185], v[96:99]
	v_mfma_f32_16x16x128_f8f6f4 v[92:95], v[222:229], v[178:185], v[92:95]
	v_mfma_f32_16x16x128_f8f6f4 v[84:87], v[222:229], v[230:237], v[84:87]
	v_mfma_f32_16x16x128_f8f6f4 v[88:91], v[204:211], v[230:237], v[88:91]
	v_mfma_f32_16x16x128_f8f6f4 v[80:83], v[204:211], v[238:245], v[80:83]
	v_mfma_f32_16x16x128_f8f6f4 v[76:79], v[222:229], v[238:245], v[76:79]
	v_mfma_f32_16x16x128_f8f6f4 v[68:71], v[222:229], v[212:219], v[68:71]
	v_mfma_f32_16x16x128_f8f6f4 v[72:75], v[204:211], v[212:219], v[72:75]
	s_setprio 0
	s_setprio 1
	v_mfma_f32_16x16x128_f8f6f4 v[64:67], v[10:17], v[178:185], v[64:67]
	v_mfma_f32_16x16x128_f8f6f4 v[60:63], v[2:9], v[178:185], v[60:63]
	v_mfma_f32_16x16x128_f8f6f4 v[52:55], v[2:9], v[230:237], v[52:55]
	v_mfma_f32_16x16x128_f8f6f4 v[56:59], v[10:17], v[230:237], v[56:59]
	v_mfma_f32_16x16x128_f8f6f4 v[48:51], v[10:17], v[238:245], v[48:51]
	v_mfma_f32_16x16x128_f8f6f4 v[44:47], v[2:9], v[238:245], v[44:47]
	v_mfma_f32_16x16x128_f8f6f4 v[36:39], v[2:9], v[212:219], v[36:39]
	v_mfma_f32_16x16x128_f8f6f4 v[40:43], v[10:17], v[212:219], v[40:43]
	s_setprio 0
	s_barrier
	ds_read_b128 v[178:181], v201
	ds_read_b128 v[182:185], v201 offset:1024
	ds_read_b128 v[204:207], v201 offset:2048
	ds_read_b128 v[208:211], v201 offset:3072
	ds_read_b128 v[10:13], v202
	ds_read_b128 v[14:17], v202 offset:1024
	ds_read_b128 v[2:5], v202 offset:2048
	ds_read_b128 v[6:9], v202 offset:3072
	s_mov_b32 m0, s71
	ds_read_b128 v[212:215], v169 offset:32768
	ds_read_b128 v[216:219], v169 offset:33792
	ds_read_b128 v[222:225], v169 offset:34816
	ds_read_b128 v[226:229], v169 offset:35840
	ds_read_b128 v[230:233], v169 offset:36864
	ds_read_b128 v[234:237], v169 offset:37888
	ds_read_b128 v[238:241], v169 offset:38912
	ds_read_b128 v[242:245], v169 offset:39936
	global_load_lds_dwordx4 v189, s[40:41]
	s_mov_b32 m0, s72
	s_nop 0
	global_load_lds_dwordx4 v198, s[40:41]
	s_waitcnt vmcnt(8)
	s_waitcnt lgkmcnt(0)
	s_barrier
	s_setprio 1
	s_waitcnt lgkmcnt(0)
	v_mfma_f32_16x16x128_f8f6f4 v[160:163], v[178:185], v[212:219], v[160:163]
	v_mfma_f32_16x16x128_f8f6f4 v[156:159], v[204:211], v[212:219], v[156:159]
	v_mfma_f32_16x16x128_f8f6f4 v[148:151], v[204:211], v[222:229], v[148:151]
	v_mfma_f32_16x16x128_f8f6f4 v[152:155], v[178:185], v[222:229], v[152:155]
	v_mfma_f32_16x16x128_f8f6f4 v[144:147], v[178:185], v[230:237], v[144:147]
	v_mfma_f32_16x16x128_f8f6f4 v[140:143], v[204:211], v[230:237], v[140:143]
	v_mfma_f32_16x16x128_f8f6f4 v[132:135], v[204:211], v[238:245], v[132:135]
	v_mfma_f32_16x16x128_f8f6f4 v[136:139], v[178:185], v[238:245], v[136:139]
	s_setprio 0
	s_setprio 1
	v_mfma_f32_16x16x128_f8f6f4 v[128:131], v[10:17], v[212:219], v[128:131]
	v_mfma_f32_16x16x128_f8f6f4 v[124:127], v[2:9], v[212:219], v[124:127]
	v_mfma_f32_16x16x128_f8f6f4 v[116:119], v[2:9], v[222:229], v[116:119]
	v_mfma_f32_16x16x128_f8f6f4 v[120:123], v[10:17], v[222:229], v[120:123]
	v_mfma_f32_16x16x128_f8f6f4 v[112:115], v[10:17], v[230:237], v[112:115]
	v_mfma_f32_16x16x128_f8f6f4 v[108:111], v[2:9], v[230:237], v[108:111]
	v_mfma_f32_16x16x128_f8f6f4 v[100:103], v[2:9], v[238:245], v[100:103]
	v_mfma_f32_16x16x128_f8f6f4 v[104:107], v[10:17], v[238:245], v[104:107]
	s_setprio 0
	s_barrier
	s_mov_b32 m0, s54
	v_lshl_add_u64 v[22:23], v[22:23], 0, s[18:19]
	s_add_u32 s36, s36, 0x20080
	ds_read_b128 v[212:215], v169 offset:49152
	ds_read_b128 v[216:219], v169 offset:50176
	ds_read_b128 v[222:225], v169 offset:51200
	ds_read_b128 v[226:229], v169 offset:52224
	ds_read_b128 v[230:233], v169 offset:53248
	ds_read_b128 v[234:237], v169 offset:54272
	ds_read_b128 v[238:241], v169 offset:55296
	ds_read_b128 v[242:245], v169 offset:56320
	global_load_lds_dwordx4 v[22:23], off
	v_lshl_add_u64 v[22:23], v[24:25], 0, s[18:19]
	s_mov_b32 m0, s50
	s_addc_u32 s37, s37, 0
	global_load_lds_dwordx4 v[22:23], off
	v_lshl_add_u64 v[22:23], s[36:37], 0, v[170:171]
	s_mov_b32 m0, s51
	s_nop 0
	global_load_lds_dwordx4 v[22:23], off
	v_lshl_add_u64 v[22:23], s[36:37], 0, v[172:173]
	s_mov_b32 m0, s64
	s_nop 0
	global_load_lds_dwordx4 v[22:23], off
	v_lshl_add_u64 v[22:23], v[28:29], 0, s[18:19]
	s_mov_b32 m0, s75
	s_nop 0
	global_load_lds_dwordx4 v[22:23], off
	v_lshl_add_u64 v[22:23], v[26:27], 0, s[18:19]
	s_mov_b32 m0, s76
	s_nop 0
	global_load_lds_dwordx4 v[22:23], off
	s_waitcnt vmcnt(8)
	s_waitcnt lgkmcnt(0)
	s_barrier
	s_setprio 1
	s_waitcnt lgkmcnt(0)
	v_mfma_f32_16x16x128_f8f6f4 v[96:99], v[178:185], v[212:219], v[96:99]
	v_mfma_f32_16x16x128_f8f6f4 v[92:95], v[204:211], v[212:219], v[92:95]
	v_mfma_f32_16x16x128_f8f6f4 v[84:87], v[204:211], v[222:229], v[84:87]
	v_mfma_f32_16x16x128_f8f6f4 v[88:91], v[178:185], v[222:229], v[88:91]
	v_mfma_f32_16x16x128_f8f6f4 v[80:83], v[178:185], v[230:237], v[80:83]
	v_mfma_f32_16x16x128_f8f6f4 v[76:79], v[204:211], v[230:237], v[76:79]
	v_mfma_f32_16x16x128_f8f6f4 v[68:71], v[204:211], v[238:245], v[68:71]
	v_mfma_f32_16x16x128_f8f6f4 v[72:75], v[178:185], v[238:245], v[72:75]
	s_setprio 0
	s_setprio 1
	v_mfma_f32_16x16x128_f8f6f4 v[64:67], v[10:17], v[212:219], v[64:67]
	v_mfma_f32_16x16x128_f8f6f4 v[60:63], v[2:9], v[212:219], v[60:63]
	v_mfma_f32_16x16x128_f8f6f4 v[52:55], v[2:9], v[222:229], v[52:55]
	v_mfma_f32_16x16x128_f8f6f4 v[56:59], v[10:17], v[222:229], v[56:59]
	v_mfma_f32_16x16x128_f8f6f4 v[48:51], v[10:17], v[230:237], v[48:51]
	v_mfma_f32_16x16x128_f8f6f4 v[44:47], v[2:9], v[230:237], v[44:47]
	v_mfma_f32_16x16x128_f8f6f4 v[36:39], v[2:9], v[238:245], v[36:39]
	v_mfma_f32_16x16x128_f8f6f4 v[40:43], v[10:17], v[238:245], v[40:43]
	s_setprio 0
	s_barrier
	s_add_i32 s63, s63, 2
	s_add_u32 s30, s30, 0x100
	s_addc_u32 s31, s31, 0
	s_cmp_gt_u32 s63, 5
	s_cbranch_scc1 .LBB0_823

.LBB0_899:
	s_mul_i32 s14, s81, 0xe0000
	s_add_u32 s40, s44, s14
	s_addc_u32 s41, s45, 0
	s_and_b64 s[6:7], s[6:7], exec
	s_cselect_b32 s52, s41, s43
	s_cselect_b32 s53, s40, s42
	s_add_i32 s54, 0, 0x10000
	s_add_i32 s65, 0, 0x14000
	v_add_u32_e32 v34, s54, v167
	v_add_u32_e32 v206, s65, v167
	ds_read_b128 v[26:29], v34
	ds_read_b128 v[30:33], v34 offset:1024
	ds_read_b128 v[18:21], v34 offset:2048
	ds_read_b128 v[22:25], v34 offset:3072
	ds_read_b128 v[10:13], v206
	ds_read_b128 v[14:17], v206 offset:1024
	ds_read_b128 v[2:5], v206 offset:2048
	ds_read_b128 v[6:9], v206 offset:3072
	s_add_u32 s6, s42, 0x70080
	s_addc_u32 s7, s43, 0
	s_add_i32 s84, s72, 0xc000
	v_lshl_add_u64 v[216:217], s[6:7], 0, v[174:175]
	s_mov_b32 m0, s84
	s_add_i32 s85, s72, 0xe000
	ds_read_b128 v[178:181], v189
	ds_read_b128 v[182:185], v189 offset:1024
	ds_read_b128 v[198:201], v189 offset:2048
	ds_read_b128 v[202:205], v189 offset:3072
	ds_read_b128 v[208:211], v189 offset:4096
	ds_read_b128 v[212:215], v189 offset:5120
	ds_read_b128 v[222:225], v189 offset:6144
	ds_read_b128 v[226:229], v189 offset:7168
	global_load_lds_dwordx4 v[216:217], off
	v_lshl_add_u64 v[216:217], s[6:7], 0, v[170:171]
	s_mov_b32 m0, s85
	s_nop 0
	global_load_lds_dwordx4 v[216:217], off
	s_waitcnt vmcnt(8)
	s_waitcnt lgkmcnt(0)
	s_barrier
	s_setprio 1
	s_waitcnt lgkmcnt(0)
	v_mfma_f32_16x16x128_f8f6f4 v[160:163], v[26:33], v[178:185], 0
	v_mfma_f32_16x16x128_f8f6f4 v[156:159], v[18:25], v[178:185], 0
	v_mfma_f32_16x16x128_f8f6f4 v[148:151], v[18:25], v[198:205], 0
	v_mfma_f32_16x16x128_f8f6f4 v[152:155], v[26:33], v[198:205], 0
	v_mfma_f32_16x16x128_f8f6f4 v[144:147], v[26:33], v[208:215], 0
	v_mfma_f32_16x16x128_f8f6f4 v[140:143], v[18:25], v[208:215], 0
	v_mfma_f32_16x16x128_f8f6f4 v[132:135], v[18:25], v[222:229], 0
	v_mfma_f32_16x16x128_f8f6f4 v[136:139], v[26:33], v[222:229], 0
	s_setprio 0
	s_setprio 1
	v_mfma_f32_16x16x128_f8f6f4 v[128:131], v[10:17], v[178:185], 0
	v_mfma_f32_16x16x128_f8f6f4 v[124:127], v[2:9], v[178:185], 0
	v_mfma_f32_16x16x128_f8f6f4 v[116:119], v[2:9], v[198:205], 0
	v_mfma_f32_16x16x128_f8f6f4 v[120:123], v[10:17], v[198:205], 0
	v_mfma_f32_16x16x128_f8f6f4 v[112:115], v[10:17], v[208:215], 0
	v_mfma_f32_16x16x128_f8f6f4 v[108:111], v[2:9], v[208:215], 0
	v_mfma_f32_16x16x128_f8f6f4 v[100:103], v[2:9], v[222:229], 0
	v_mfma_f32_16x16x128_f8f6f4 v[104:107], v[10:17], v[222:229], 0
	s_setprio 0
	s_barrier
	v_lshl_add_u64 v[198:199], v[196:197], 0, v[172:173]
	s_add_i32 s54, s54, s71
	v_lshl_add_u64 v[200:201], v[198:199], 0, s[28:29]
	s_mov_b32 m0, s54
	ds_read_b128 v[178:181], v189 offset:16384
	ds_read_b128 v[182:185], v189 offset:17408
	ds_read_b128 v[208:211], v189 offset:18432
	ds_read_b128 v[212:215], v189 offset:19456
	ds_read_b128 v[222:225], v189 offset:20480
	ds_read_b128 v[226:229], v189 offset:21504
	ds_read_b128 v[230:233], v189 offset:22528
	ds_read_b128 v[234:237], v189 offset:23552
	global_load_lds_dwordx4 v[200:201], off
	v_lshl_add_u64 v[200:201], v[196:197], 0, v[168:169]
	s_add_i32 s55, s54, 0x2000
	v_lshl_add_u64 v[202:203], v[200:201], 0, s[28:29]
	s_mov_b32 m0, s55
	s_mov_b64 s[6:7], 0x70100
	global_load_lds_dwordx4 v[202:203], off
	v_lshl_add_u64 v[202:203], v[196:197], 0, s[6:7]
	s_add_i32 s65, s65, s71
	v_lshl_add_u64 v[204:205], v[202:203], 0, v[172:173]
	s_mov_b32 m0, s65
	s_add_i32 s67, s65, 0x2000
	global_load_lds_dwordx4 v[204:205], off
	v_lshl_add_u64 v[202:203], v[202:203], 0, v[168:169]
	s_mov_b32 m0, s67
	s_nop 0
	global_load_lds_dwordx4 v[202:203], off
	v_lshl_add_u64 v[202:203], s[42:43], 0, v[174:175]
	v_lshl_add_u64 v[204:205], v[202:203], 0, s[28:29]
	s_mov_b32 m0, s72
	s_nop 0
	global_load_lds_dwordx4 v[204:205], off
	v_lshl_add_u64 v[204:205], s[42:43], 0, v[170:171]
	v_lshl_add_u64 v[216:217], v[204:205], 0, s[28:29]
	s_mov_b32 m0, s73
	s_nop 0
	global_load_lds_dwordx4 v[216:217], off
	s_waitcnt vmcnt(8)
	s_waitcnt lgkmcnt(0)
	s_barrier
	s_setprio 1
	s_waitcnt lgkmcnt(0)
	v_mfma_f32_16x16x128_f8f6f4 v[96:99], v[26:33], v[178:185], 0
	v_mfma_f32_16x16x128_f8f6f4 v[92:95], v[18:25], v[178:185], 0
	v_mfma_f32_16x16x128_f8f6f4 v[84:87], v[18:25], v[208:215], 0
	v_mfma_f32_16x16x128_f8f6f4 v[88:91], v[26:33], v[208:215], 0
	v_mfma_f32_16x16x128_f8f6f4 v[80:83], v[26:33], v[222:229], 0
	v_mfma_f32_16x16x128_f8f6f4 v[76:79], v[18:25], v[222:229], 0
	v_mfma_f32_16x16x128_f8f6f4 v[68:71], v[18:25], v[230:237], 0
	v_mfma_f32_16x16x128_f8f6f4 v[72:75], v[26:33], v[230:237], 0
	s_setprio 0
	s_setprio 1
	v_mfma_f32_16x16x128_f8f6f4 v[64:67], v[10:17], v[178:185], 0
	v_mfma_f32_16x16x128_f8f6f4 v[60:63], v[2:9], v[178:185], 0
	v_mfma_f32_16x16x128_f8f6f4 v[52:55], v[2:9], v[208:215], 0
	v_mfma_f32_16x16x128_f8f6f4 v[56:59], v[10:17], v[208:215], 0
	v_mfma_f32_16x16x128_f8f6f4 v[48:51], v[10:17], v[222:229], 0
	v_mfma_f32_16x16x128_f8f6f4 v[44:47], v[2:9], v[222:229], 0
	v_mfma_f32_16x16x128_f8f6f4 v[36:39], v[2:9], v[230:237], 0
	v_mfma_f32_16x16x128_f8f6f4 v[40:43], v[10:17], v[230:237], 0
	s_setprio 0
	s_barrier
	s_add_i32 s50, 0, 0x18000
	s_add_i32 s63, 0, 0x1c000
	v_add_u32_e32 v207, s50, v167
	v_add_u32_e32 v208, s63, v167
	ds_read_b128 v[26:29], v207
	ds_read_b128 v[30:33], v207 offset:1024
	ds_read_b128 v[18:21], v207 offset:2048
	ds_read_b128 v[22:25], v207 offset:3072
	ds_read_b128 v[10:13], v208
	ds_read_b128 v[14:17], v208 offset:1024
	ds_read_b128 v[2:5], v208 offset:2048
	ds_read_b128 v[6:9], v208 offset:3072
	s_add_u32 s6, s42, 0x70100
	s_addc_u32 s7, s43, 0
	s_mov_b32 m0, s74
	v_lshl_add_u64 v[218:219], s[6:7], 0, v[174:175]
	ds_read_b128 v[178:181], v189 offset:32768
	ds_read_b128 v[182:185], v189 offset:33792
	ds_read_b128 v[210:213], v189 offset:34816
	ds_read_b128 v[214:217], v189 offset:35840
	ds_read_b128 v[222:225], v189 offset:36864
	ds_read_b128 v[226:229], v189 offset:37888
	ds_read_b128 v[230:233], v189 offset:38912
	ds_read_b128 v[234:237], v189 offset:39936
	global_load_lds_dwordx4 v[218:219], off
	v_lshl_add_u64 v[218:219], s[6:7], 0, v[170:171]
	s_mov_b32 m0, s75
	s_nop 0
	global_load_lds_dwordx4 v[218:219], off
	s_waitcnt vmcnt(8)
	s_waitcnt lgkmcnt(0)
	s_barrier
	s_setprio 1
	s_waitcnt lgkmcnt(0)
	v_mfma_f32_16x16x128_f8f6f4 v[160:163], v[26:33], v[178:185], v[160:163]
	v_mfma_f32_16x16x128_f8f6f4 v[156:159], v[18:25], v[178:185], v[156:159]
	v_mfma_f32_16x16x128_f8f6f4 v[148:151], v[18:25], v[210:217], v[148:151]
	v_mfma_f32_16x16x128_f8f6f4 v[152:155], v[26:33], v[210:217], v[152:155]
	v_mfma_f32_16x16x128_f8f6f4 v[144:147], v[26:33], v[222:229], v[144:147]
	v_mfma_f32_16x16x128_f8f6f4 v[140:143], v[18:25], v[222:229], v[140:143]
	v_mfma_f32_16x16x128_f8f6f4 v[132:135], v[18:25], v[230:237], v[132:135]
	v_mfma_f32_16x16x128_f8f6f4 v[136:139], v[26:33], v[230:237], v[136:139]
	s_setprio 0
	s_setprio 1
	v_mfma_f32_16x16x128_f8f6f4 v[128:131], v[10:17], v[178:185], v[128:131]
	v_mfma_f32_16x16x128_f8f6f4 v[124:127], v[2:9], v[178:185], v[124:127]
	v_mfma_f32_16x16x128_f8f6f4 v[116:119], v[2:9], v[210:217], v[116:119]
	v_mfma_f32_16x16x128_f8f6f4 v[120:123], v[10:17], v[210:217], v[120:123]
	v_mfma_f32_16x16x128_f8f6f4 v[112:115], v[10:17], v[222:229], v[112:115]
	v_mfma_f32_16x16x128_f8f6f4 v[108:111], v[2:9], v[222:229], v[108:111]
	v_mfma_f32_16x16x128_f8f6f4 v[100:103], v[2:9], v[230:237], v[100:103]
	v_mfma_f32_16x16x128_f8f6f4 v[104:107], v[10:17], v[230:237], v[104:107]
	s_setprio 0
	s_barrier
	s_mov_b64 s[6:7], 0x180
	s_add_i32 s50, s50, s71
	v_lshl_add_u64 v[198:199], v[198:199], 0, s[6:7]
	s_mov_b32 m0, s50
	s_add_i32 s51, s50, 0x2000
	ds_read_b128 v[178:181], v189 offset:49152
	ds_read_b128 v[182:185], v189 offset:50176
	ds_read_b128 v[210:213], v189 offset:51200
	ds_read_b128 v[214:217], v189 offset:52224
	ds_read_b128 v[222:225], v189 offset:53248
	ds_read_b128 v[226:229], v189 offset:54272
	ds_read_b128 v[230:233], v189 offset:55296
	ds_read_b128 v[234:237], v189 offset:56320
	global_load_lds_dwordx4 v[198:199], off
	v_lshl_add_u64 v[198:199], v[200:201], 0, s[6:7]
	s_mov_b32 m0, s51
	s_add_i32 s63, s63, s71
	global_load_lds_dwordx4 v[198:199], off
	v_lshl_add_u64 v[198:199], v[196:197], 0, s[26:27]
	v_lshl_add_u64 v[200:201], v[198:199], 0, v[172:173]
	s_mov_b32 m0, s63
	s_add_i32 s64, s63, 0x2000
	global_load_lds_dwordx4 v[200:201], off
	v_lshl_add_u64 v[198:199], v[198:199], 0, v[168:169]
	s_mov_b32 m0, s64
	s_nop 0
	global_load_lds_dwordx4 v[198:199], off
	v_lshl_add_u64 v[198:199], v[202:203], 0, s[6:7]
	s_mov_b32 m0, s77
	s_nop 0
	global_load_lds_dwordx4 v[198:199], off
	v_lshl_add_u64 v[198:199], v[204:205], 0, s[6:7]
	s_mov_b32 m0, s78
	s_nop 0
	global_load_lds_dwordx4 v[198:199], off
	s_waitcnt vmcnt(8)
	s_waitcnt lgkmcnt(0)
	s_barrier
	s_setprio 1
	s_waitcnt lgkmcnt(0)
	v_mfma_f32_16x16x128_f8f6f4 v[96:99], v[26:33], v[178:185], v[96:99]
	v_mfma_f32_16x16x128_f8f6f4 v[92:95], v[18:25], v[178:185], v[92:95]
	v_mfma_f32_16x16x128_f8f6f4 v[84:87], v[18:25], v[210:217], v[84:87]
	v_mfma_f32_16x16x128_f8f6f4 v[88:91], v[26:33], v[210:217], v[88:91]
	v_mfma_f32_16x16x128_f8f6f4 v[80:83], v[26:33], v[222:229], v[80:83]
	v_mfma_f32_16x16x128_f8f6f4 v[76:79], v[18:25], v[222:229], v[76:79]
	v_mfma_f32_16x16x128_f8f6f4 v[68:71], v[18:25], v[230:237], v[68:71]
	v_mfma_f32_16x16x128_f8f6f4 v[72:75], v[26:33], v[230:237], v[72:75]
	s_setprio 0
	s_setprio 1
	v_mfma_f32_16x16x128_f8f6f4 v[64:67], v[10:17], v[178:185], v[64:67]
	v_mfma_f32_16x16x128_f8f6f4 v[60:63], v[2:9], v[178:185], v[60:63]
	v_mfma_f32_16x16x128_f8f6f4 v[52:55], v[2:9], v[210:217], v[52:55]
	v_mfma_f32_16x16x128_f8f6f4 v[56:59], v[10:17], v[210:217], v[56:59]
	v_mfma_f32_16x16x128_f8f6f4 v[48:51], v[10:17], v[222:229], v[48:51]
	v_mfma_f32_16x16x128_f8f6f4 v[44:47], v[2:9], v[222:229], v[44:47]
	v_mfma_f32_16x16x128_f8f6f4 v[36:39], v[2:9], v[230:237], v[36:39]
	v_mfma_f32_16x16x128_f8f6f4 v[40:43], v[10:17], v[230:237], v[40:43]
	s_setprio 0
	s_barrier
	s_mov_b64 s[6:7], 0x200
	v_lshl_add_u64 v[18:19], v[196:197], 0, s[6:7]
	s_mov_b32 s86, 0
.LBB0_900:
	ds_read_b128 v[2:5], v34
	ds_read_b128 v[6:9], v34 offset:1024
	ds_read_b128 v[10:13], v34 offset:2048
	ds_read_b128 v[14:17], v34 offset:3072
	ds_read_b128 v[178:181], v206
	ds_read_b128 v[182:185], v206 offset:1024
	ds_read_b128 v[196:199], v206 offset:2048
	ds_read_b128 v[200:203], v206 offset:3072
	s_add_u32 s6, s42, 0x200
	s_addc_u32 s7, s43, 0
	s_cmp_eq_u32 s86, 24
	s_cselect_b64 vcc, -1, 0
	s_cselect_b32 s7, s52, s7
	s_cselect_b32 s6, s53, s6
	v_cndmask_b32_e32 v21, v19, v195, vcc
	v_cndmask_b32_e32 v20, v18, v194, vcc
	s_mov_b32 m0, s84
	v_lshl_add_u64 v[30:31], s[42:43], 0, v[190:191]
	ds_read_b128 v[22:25], v189
	ds_read_b128 v[26:29], v189 offset:1024
	ds_read_b128 v[210:213], v189 offset:2048
	ds_read_b128 v[214:217], v189 offset:3072
	ds_read_b128 v[222:225], v189 offset:4096
	ds_read_b128 v[226:229], v189 offset:5120
	ds_read_b128 v[230:233], v189 offset:6144
	ds_read_b128 v[234:237], v189 offset:7168
	global_load_lds_dwordx4 v[30:31], off
	v_lshl_add_u64 v[30:31], s[42:43], 0, v[192:193]
	s_mov_b32 m0, s85
	s_nop 0
	global_load_lds_dwordx4 v[30:31], off
	s_waitcnt vmcnt(8)
	s_waitcnt lgkmcnt(0)
	s_barrier
	s_setprio 1
	s_waitcnt lgkmcnt(0)
	v_mfma_f32_16x16x128_f8f6f4 v[160:163], v[2:9], v[22:29], v[160:163]
	v_mfma_f32_16x16x128_f8f6f4 v[156:159], v[10:17], v[22:29], v[156:159]
	v_mfma_f32_16x16x128_f8f6f4 v[148:151], v[10:17], v[210:217], v[148:151]
	v_mfma_f32_16x16x128_f8f6f4 v[152:155], v[2:9], v[210:217], v[152:155]
	v_mfma_f32_16x16x128_f8f6f4 v[144:147], v[2:9], v[222:229], v[144:147]
	v_mfma_f32_16x16x128_f8f6f4 v[140:143], v[10:17], v[222:229], v[140:143]
	v_mfma_f32_16x16x128_f8f6f4 v[132:135], v[10:17], v[230:237], v[132:135]
	v_mfma_f32_16x16x128_f8f6f4 v[136:139], v[2:9], v[230:237], v[136:139]
	s_setprio 0
	s_setprio 1
	v_mfma_f32_16x16x128_f8f6f4 v[128:131], v[178:185], v[22:29], v[128:131]
	v_mfma_f32_16x16x128_f8f6f4 v[124:127], v[196:203], v[22:29], v[124:127]
	v_mfma_f32_16x16x128_f8f6f4 v[116:119], v[196:203], v[210:217], v[116:119]
	v_mfma_f32_16x16x128_f8f6f4 v[120:123], v[178:185], v[210:217], v[120:123]
	v_mfma_f32_16x16x128_f8f6f4 v[112:115], v[178:185], v[222:229], v[112:115]
	v_mfma_f32_16x16x128_f8f6f4 v[108:111], v[196:203], v[222:229], v[108:111]
	v_mfma_f32_16x16x128_f8f6f4 v[100:103], v[196:203], v[230:237], v[100:103]
	v_mfma_f32_16x16x128_f8f6f4 v[104:107], v[178:185], v[230:237], v[104:107]
	s_setprio 0
	s_barrier
	s_mov_b32 m0, s54
	v_lshl_add_u64 v[22:23], v[20:21], 0, v[172:173]
	ds_read_b128 v[210:213], v189 offset:16384
	ds_read_b128 v[214:217], v189 offset:17408
	ds_read_b128 v[222:225], v189 offset:18432
	ds_read_b128 v[226:229], v189 offset:19456
	ds_read_b128 v[230:233], v189 offset:20480
	ds_read_b128 v[234:237], v189 offset:21504
	ds_read_b128 v[238:241], v189 offset:22528
	ds_read_b128 v[242:245], v189 offset:23552
	global_load_lds_dwordx4 v[22:23], off
	v_lshl_add_u64 v[24:25], v[20:21], 0, v[168:169]
	s_mov_b32 m0, s55
	v_lshl_add_u64 v[26:27], v[20:21], 0, s[2:3]
	global_load_lds_dwordx4 v[24:25], off
	v_lshl_add_u64 v[28:29], v[26:27], 0, v[172:173]
	s_mov_b32 m0, s65
	v_lshl_add_u64 v[26:27], v[26:27], 0, v[168:169]
	global_load_lds_dwordx4 v[28:29], off
	s_mov_b32 m0, s67
	v_lshl_add_u64 v[28:29], s[6:7], 0, v[170:171]
	global_load_lds_dwordx4 v[26:27], off
	v_lshl_add_u64 v[26:27], s[6:7], 0, v[174:175]
	s_mov_b32 m0, s72
	s_nop 0
	global_load_lds_dwordx4 v[26:27], off
	s_mov_b32 m0, s73
	s_nop 0
	global_load_lds_dwordx4 v[28:29], off
	s_waitcnt vmcnt(8)
	s_waitcnt lgkmcnt(0)
	s_barrier
	s_setprio 1
	s_waitcnt lgkmcnt(0)
	v_mfma_f32_16x16x128_f8f6f4 v[96:99], v[2:9], v[210:217], v[96:99]
	v_mfma_f32_16x16x128_f8f6f4 v[92:95], v[10:17], v[210:217], v[92:95]
	v_mfma_f32_16x16x128_f8f6f4 v[84:87], v[10:17], v[222:229], v[84:87]
	v_mfma_f32_16x16x128_f8f6f4 v[88:91], v[2:9], v[222:229], v[88:91]
	v_mfma_f32_16x16x128_f8f6f4 v[80:83], v[2:9], v[230:237], v[80:83]
	v_mfma_f32_16x16x128_f8f6f4 v[76:79], v[10:17], v[230:237], v[76:79]
	v_mfma_f32_16x16x128_f8f6f4 v[68:71], v[10:17], v[238:245], v[68:71]
	v_mfma_f32_16x16x128_f8f6f4 v[72:75], v[2:9], v[238:245], v[72:75]
	s_setprio 0
	s_setprio 1
	v_mfma_f32_16x16x128_f8f6f4 v[64:67], v[178:185], v[210:217], v[64:67]
	v_mfma_f32_16x16x128_f8f6f4 v[60:63], v[196:203], v[210:217], v[60:63]
	v_mfma_f32_16x16x128_f8f6f4 v[52:55], v[196:203], v[222:229], v[52:55]
	v_mfma_f32_16x16x128_f8f6f4 v[56:59], v[178:185], v[222:229], v[56:59]
	v_mfma_f32_16x16x128_f8f6f4 v[48:51], v[178:185], v[230:237], v[48:51]
	v_mfma_f32_16x16x128_f8f6f4 v[44:47], v[196:203], v[230:237], v[44:47]
	v_mfma_f32_16x16x128_f8f6f4 v[36:39], v[196:203], v[238:245], v[36:39]
	v_mfma_f32_16x16x128_f8f6f4 v[40:43], v[178:185], v[238:245], v[40:43]
	s_setprio 0
	s_barrier
	ds_read_b128 v[178:181], v207
	ds_read_b128 v[182:185], v207 offset:1024
	ds_read_b128 v[196:199], v207 offset:2048
	ds_read_b128 v[200:203], v207 offset:3072
	ds_read_b128 v[10:13], v208
	ds_read_b128 v[14:17], v208 offset:1024
	ds_read_b128 v[2:5], v208 offset:2048
	ds_read_b128 v[6:9], v208 offset:3072
	s_add_u32 s6, s6, 0x70000
	s_addc_u32 s7, s7, 0
	s_mov_b32 m0, s74
	v_lshl_add_u64 v[30:31], s[6:7], 0, v[174:175]
	ds_read_b128 v[210:213], v189 offset:32768
	ds_read_b128 v[214:217], v189 offset:33792
	ds_read_b128 v[222:225], v189 offset:34816
	ds_read_b128 v[226:229], v189 offset:35840
	ds_read_b128 v[230:233], v189 offset:36864
	ds_read_b128 v[234:237], v189 offset:37888
	ds_read_b128 v[238:241], v189 offset:38912
	ds_read_b128 v[242:245], v189 offset:39936
	global_load_lds_dwordx4 v[30:31], off
	v_lshl_add_u64 v[30:31], s[6:7], 0, v[170:171]
	s_mov_b32 m0, s75
	s_nop 0
	global_load_lds_dwordx4 v[30:31], off
	s_waitcnt vmcnt(8)
	s_waitcnt lgkmcnt(0)
	s_barrier
	s_setprio 1
	s_waitcnt lgkmcnt(0)
	v_mfma_f32_16x16x128_f8f6f4 v[160:163], v[178:185], v[210:217], v[160:163]
	v_mfma_f32_16x16x128_f8f6f4 v[156:159], v[196:203], v[210:217], v[156:159]
	v_mfma_f32_16x16x128_f8f6f4 v[148:151], v[196:203], v[222:229], v[148:151]
	v_mfma_f32_16x16x128_f8f6f4 v[152:155], v[178:185], v[222:229], v[152:155]
	v_mfma_f32_16x16x128_f8f6f4 v[144:147], v[178:185], v[230:237], v[144:147]
	v_mfma_f32_16x16x128_f8f6f4 v[140:143], v[196:203], v[230:237], v[140:143]
	v_mfma_f32_16x16x128_f8f6f4 v[132:135], v[196:203], v[238:245], v[132:135]
	v_mfma_f32_16x16x128_f8f6f4 v[136:139], v[178:185], v[238:245], v[136:139]
	s_setprio 0
	s_setprio 1
	v_mfma_f32_16x16x128_f8f6f4 v[128:131], v[10:17], v[210:217], v[128:131]
	v_mfma_f32_16x16x128_f8f6f4 v[124:127], v[2:9], v[210:217], v[124:127]
	v_mfma_f32_16x16x128_f8f6f4 v[116:119], v[2:9], v[222:229], v[116:119]
	v_mfma_f32_16x16x128_f8f6f4 v[120:123], v[10:17], v[222:229], v[120:123]
	v_mfma_f32_16x16x128_f8f6f4 v[112:115], v[10:17], v[230:237], v[112:115]
	v_mfma_f32_16x16x128_f8f6f4 v[108:111], v[2:9], v[230:237], v[108:111]
	v_mfma_f32_16x16x128_f8f6f4 v[100:103], v[2:9], v[238:245], v[100:103]
	v_mfma_f32_16x16x128_f8f6f4 v[104:107], v[10:17], v[238:245], v[104:107]
	s_setprio 0
	s_barrier
	s_mov_b32 m0, s50
	v_lshl_add_u64 v[22:23], v[22:23], 0, s[18:19]
	ds_read_b128 v[210:213], v189 offset:49152
	ds_read_b128 v[214:217], v189 offset:50176
	ds_read_b128 v[222:225], v189 offset:51200
	ds_read_b128 v[226:229], v189 offset:52224
	ds_read_b128 v[230:233], v189 offset:53248
	ds_read_b128 v[234:237], v189 offset:54272
	ds_read_b128 v[238:241], v189 offset:55296
	ds_read_b128 v[242:245], v189 offset:56320
	global_load_lds_dwordx4 v[22:23], off
	v_lshl_add_u64 v[22:23], v[24:25], 0, s[18:19]
	s_mov_b32 m0, s51
	v_lshl_add_u64 v[20:21], v[20:21], 0, s[34:35]
	global_load_lds_dwordx4 v[22:23], off
	v_lshl_add_u64 v[22:23], v[20:21], 0, v[172:173]
	s_mov_b32 m0, s63
	v_lshl_add_u64 v[20:21], v[20:21], 0, v[168:169]
	global_load_lds_dwordx4 v[22:23], off
	s_mov_b32 m0, s64
	s_nop 0
	global_load_lds_dwordx4 v[20:21], off
	v_lshl_add_u64 v[20:21], v[26:27], 0, s[18:19]
	s_mov_b32 m0, s77
	s_nop 0
	global_load_lds_dwordx4 v[20:21], off
	v_lshl_add_u64 v[20:21], v[28:29], 0, s[18:19]
	s_mov_b32 m0, s78
	s_nop 0
	global_load_lds_dwordx4 v[20:21], off
	s_waitcnt vmcnt(8)
	s_waitcnt lgkmcnt(0)
	s_barrier
	s_setprio 1
	s_waitcnt lgkmcnt(0)
	v_mfma_f32_16x16x128_f8f6f4 v[96:99], v[178:185], v[210:217], v[96:99]
	v_mfma_f32_16x16x128_f8f6f4 v[92:95], v[196:203], v[210:217], v[92:95]
	v_mfma_f32_16x16x128_f8f6f4 v[84:87], v[196:203], v[222:229], v[84:87]
	v_mfma_f32_16x16x128_f8f6f4 v[88:91], v[178:185], v[222:229], v[88:91]
	v_mfma_f32_16x16x128_f8f6f4 v[80:83], v[178:185], v[230:237], v[80:83]
	v_mfma_f32_16x16x128_f8f6f4 v[76:79], v[196:203], v[230:237], v[76:79]
	v_mfma_f32_16x16x128_f8f6f4 v[68:71], v[196:203], v[238:245], v[68:71]
	v_mfma_f32_16x16x128_f8f6f4 v[72:75], v[178:185], v[238:245], v[72:75]
	s_setprio 0
	s_setprio 1
	v_mfma_f32_16x16x128_f8f6f4 v[64:67], v[10:17], v[210:217], v[64:67]
	v_mfma_f32_16x16x128_f8f6f4 v[60:63], v[2:9], v[210:217], v[60:63]
	v_mfma_f32_16x16x128_f8f6f4 v[52:55], v[2:9], v[222:229], v[52:55]
	v_mfma_f32_16x16x128_f8f6f4 v[56:59], v[10:17], v[222:229], v[56:59]
	v_mfma_f32_16x16x128_f8f6f4 v[48:51], v[10:17], v[230:237], v[48:51]
	v_mfma_f32_16x16x128_f8f6f4 v[44:47], v[2:9], v[230:237], v[44:47]
	v_mfma_f32_16x16x128_f8f6f4 v[36:39], v[2:9], v[238:245], v[36:39]
	v_mfma_f32_16x16x128_f8f6f4 v[40:43], v[10:17], v[238:245], v[40:43]
	s_setprio 0
	s_barrier
	s_add_i32 s86, s86, 2
	s_add_u32 s42, s42, 0x100
	s_addc_u32 s43, s43, 0
	s_cmp_gt_u32 s86, 25
	v_lshl_add_u64 v[18:19], v[18:19], 0, s[28:29]
	s_cbranch_scc0 .LBB0_900
	s_and_b64 vcc, exec, s[36:37]
	s_mov_b64 s[84:85], s[24:25]
	s_cbranch_vccz .LBB0_903
	s_barrier

.LBB0_953:
	s_add_u32 s95, s30, 0x200
	s_addc_u32 s96, s31, 0
	s_add_i32 s65, 0, 0x14000
	s_add_i32 s67, 0, 0x10000
	v_add_u32_e32 v199, s65, v167
	v_add_u32_e32 v200, s67, v167
	ds_read_b128 v[10:13], v199
	ds_read_b128 v[14:17], v199 offset:1024
	ds_read_b128 v[2:5], v199 offset:2048
	ds_read_b128 v[6:9], v199 offset:3072
	ds_read_b128 v[22:25], v200 offset:3072
	ds_read_b128 v[18:21], v200 offset:2048
	ds_read_b128 v[30:33], v200 offset:1024
	ds_read_b128 v[26:29], v200
	s_lshl_b32 s14, s94, 10
	s_add_i32 s97, s14, 0
	s_add_i32 s97, s97, 0x20400
	v_mov_b32_e32 v191, v35
	v_mov_b32_e32 v175, v35
	s_add_i32 s83, s52, 0xc000
	v_readlane_b32 s26, v253, 28
	s_mov_b32 m0, s83
	v_readlane_b32 s27, v253, 29
	s_add_i32 s53, s52, 0xe000
	ds_read_b128 v[178:181], v169
	ds_read_b128 v[182:185], v169 offset:1024
	ds_read_b128 v[202:205], v169 offset:2048
	ds_read_b128 v[206:209], v169 offset:3072
	ds_read_b128 v[210:213], v169 offset:4096
	ds_read_b128 v[214:217], v169 offset:5120
	ds_read_b128 v[222:225], v169 offset:6144
	ds_read_b128 v[226:229], v169 offset:7168
	global_load_lds_dwordx4 v190, s[26:27]
	s_mov_b32 m0, s53
	s_nop 0
	global_load_lds_dwordx4 v174, s[26:27]
	s_waitcnt vmcnt(8)
	s_waitcnt lgkmcnt(0)
	s_barrier
	s_setprio 1
	s_waitcnt lgkmcnt(0)
	v_mfma_f32_16x16x128_f8f6f4 v[160:163], v[26:33], v[178:185], 0
	v_mfma_f32_16x16x128_f8f6f4 v[156:159], v[18:25], v[178:185], 0
	v_mfma_f32_16x16x128_f8f6f4 v[148:151], v[18:25], v[202:209], 0
	v_mfma_f32_16x16x128_f8f6f4 v[152:155], v[26:33], v[202:209], 0
	v_mfma_f32_16x16x128_f8f6f4 v[144:147], v[26:33], v[210:217], 0
	v_mfma_f32_16x16x128_f8f6f4 v[140:143], v[18:25], v[210:217], 0
	v_mfma_f32_16x16x128_f8f6f4 v[132:135], v[18:25], v[222:229], 0
	v_mfma_f32_16x16x128_f8f6f4 v[136:139], v[26:33], v[222:229], 0
	s_setprio 0
	s_setprio 1
	v_mfma_f32_16x16x128_f8f6f4 v[128:131], v[10:17], v[178:185], 0
	v_mfma_f32_16x16x128_f8f6f4 v[124:127], v[2:9], v[178:185], 0
	v_mfma_f32_16x16x128_f8f6f4 v[116:119], v[2:9], v[202:209], 0
	v_mfma_f32_16x16x128_f8f6f4 v[120:123], v[10:17], v[202:209], 0
	v_mfma_f32_16x16x128_f8f6f4 v[112:115], v[10:17], v[210:217], 0
	v_mfma_f32_16x16x128_f8f6f4 v[108:111], v[2:9], v[210:217], 0
	v_mfma_f32_16x16x128_f8f6f4 v[100:103], v[2:9], v[222:229], 0
	v_mfma_f32_16x16x128_f8f6f4 v[104:107], v[10:17], v[222:229], 0
	s_setprio 0
	s_barrier
	v_lshl_add_u64 v[194:195], s[30:31], 0, v[170:171]
	s_add_i32 s67, s67, s82
	v_lshl_add_u64 v[196:197], v[194:195], 0, s[28:29]
	s_mov_b32 m0, s67
	s_add_i32 s55, s67, 0x2000
	ds_read_b128 v[178:181], v169 offset:16384
	ds_read_b128 v[182:185], v169 offset:17408
	ds_read_b128 v[202:205], v169 offset:18432
	ds_read_b128 v[206:209], v169 offset:19456
	ds_read_b128 v[210:213], v169 offset:20480
	ds_read_b128 v[214:217], v169 offset:21504
	ds_read_b128 v[222:225], v169 offset:22528
	ds_read_b128 v[226:229], v169 offset:23552
	global_load_lds_dwordx4 v[196:197], off
	v_lshl_add_u64 v[196:197], s[30:31], 0, v[172:173]
	s_add_u32 s46, s30, 0x20100
	v_lshl_add_u64 v[218:219], v[196:197], 0, s[28:29]
	s_mov_b32 m0, s55
	s_addc_u32 s47, s31, 0
	s_add_i32 s65, s65, s82
	global_load_lds_dwordx4 v[218:219], off
	v_lshl_add_u64 v[218:219], s[46:47], 0, v[170:171]
	s_mov_b32 m0, s65
	s_add_i32 s54, s65, 0x2000
	global_load_lds_dwordx4 v[218:219], off
	v_lshl_add_u64 v[218:219], s[46:47], 0, v[172:173]
	s_mov_b32 m0, s54
	v_readlane_b32 s26, v253, 37
	global_load_lds_dwordx4 v[218:219], off
	s_mov_b32 m0, s52
	v_readlane_b32 s27, v253, 38
	s_nop 4
	global_load_lds_dwordx4 v34, s[26:27]
	s_mov_b32 m0, s84
	s_nop 0
	global_load_lds_dwordx4 v192, s[26:27]
	s_waitcnt vmcnt(8)
	s_waitcnt lgkmcnt(0)
	s_barrier
	s_setprio 1
	s_waitcnt lgkmcnt(0)
	v_mfma_f32_16x16x128_f8f6f4 v[96:99], v[26:33], v[178:185], 0
	v_mfma_f32_16x16x128_f8f6f4 v[92:95], v[18:25], v[178:185], 0
	v_mfma_f32_16x16x128_f8f6f4 v[84:87], v[18:25], v[202:209], 0
	v_mfma_f32_16x16x128_f8f6f4 v[88:91], v[26:33], v[202:209], 0
	v_mfma_f32_16x16x128_f8f6f4 v[80:83], v[26:33], v[210:217], 0
	v_mfma_f32_16x16x128_f8f6f4 v[76:79], v[18:25], v[210:217], 0
	v_mfma_f32_16x16x128_f8f6f4 v[68:71], v[18:25], v[222:229], 0
	v_mfma_f32_16x16x128_f8f6f4 v[72:75], v[26:33], v[222:229], 0
	s_setprio 0
	s_setprio 1
	v_mfma_f32_16x16x128_f8f6f4 v[64:67], v[10:17], v[178:185], 0
	v_mfma_f32_16x16x128_f8f6f4 v[60:63], v[2:9], v[178:185], 0
	v_mfma_f32_16x16x128_f8f6f4 v[52:55], v[2:9], v[202:209], 0
	v_mfma_f32_16x16x128_f8f6f4 v[56:59], v[10:17], v[202:209], 0
	v_mfma_f32_16x16x128_f8f6f4 v[48:51], v[10:17], v[210:217], 0
	v_mfma_f32_16x16x128_f8f6f4 v[44:47], v[2:9], v[210:217], 0
	v_mfma_f32_16x16x128_f8f6f4 v[36:39], v[2:9], v[222:229], 0
	v_mfma_f32_16x16x128_f8f6f4 v[40:43], v[10:17], v[222:229], 0
	s_setprio 0
	s_barrier
	s_add_i32 s50, 0, 0x18000
	s_add_i32 s64, 0, 0x1c000
	v_add_u32_e32 v201, s50, v167
	v_add_u32_e32 v202, s64, v167
	ds_read_b128 v[26:29], v201
	ds_read_b128 v[30:33], v201 offset:1024
	ds_read_b128 v[18:21], v201 offset:2048
	ds_read_b128 v[22:25], v201 offset:3072
	ds_read_b128 v[10:13], v202
	ds_read_b128 v[14:17], v202 offset:1024
	ds_read_b128 v[2:5], v202 offset:2048
	ds_read_b128 v[6:9], v202 offset:3072
	s_mov_b32 m0, s85
	ds_read_b128 v[178:181], v169 offset:32768
	ds_read_b128 v[182:185], v169 offset:33792
	ds_read_b128 v[204:207], v169 offset:34816
	ds_read_b128 v[208:211], v169 offset:35840
	ds_read_b128 v[212:215], v169 offset:36864
	ds_read_b128 v[216:219], v169 offset:37888
	ds_read_b128 v[222:225], v169 offset:38912
	ds_read_b128 v[226:229], v169 offset:39936
	global_load_lds_dwordx4 v189, s[26:27]
	s_mov_b32 m0, s86
	s_nop 0
	global_load_lds_dwordx4 v198, s[26:27]
	s_waitcnt vmcnt(8)
	s_waitcnt lgkmcnt(0)
	s_barrier
	s_setprio 1
	s_waitcnt lgkmcnt(0)
	v_mfma_f32_16x16x128_f8f6f4 v[160:163], v[26:33], v[178:185], v[160:163]
	v_mfma_f32_16x16x128_f8f6f4 v[156:159], v[18:25], v[178:185], v[156:159]
	v_mfma_f32_16x16x128_f8f6f4 v[148:151], v[18:25], v[204:211], v[148:151]
	v_mfma_f32_16x16x128_f8f6f4 v[152:155], v[26:33], v[204:211], v[152:155]
	v_mfma_f32_16x16x128_f8f6f4 v[144:147], v[26:33], v[212:219], v[144:147]
	v_mfma_f32_16x16x128_f8f6f4 v[140:143], v[18:25], v[212:219], v[140:143]
	v_mfma_f32_16x16x128_f8f6f4 v[132:135], v[18:25], v[222:229], v[132:135]
	v_mfma_f32_16x16x128_f8f6f4 v[136:139], v[26:33], v[222:229], v[136:139]
	s_setprio 0
	s_setprio 1
	v_mfma_f32_16x16x128_f8f6f4 v[128:131], v[10:17], v[178:185], v[128:131]
	v_mfma_f32_16x16x128_f8f6f4 v[124:127], v[2:9], v[178:185], v[124:127]
	v_mfma_f32_16x16x128_f8f6f4 v[116:119], v[2:9], v[204:211], v[116:119]
	v_mfma_f32_16x16x128_f8f6f4 v[120:123], v[10:17], v[204:211], v[120:123]
	v_mfma_f32_16x16x128_f8f6f4 v[112:115], v[10:17], v[212:219], v[112:115]
	v_mfma_f32_16x16x128_f8f6f4 v[108:111], v[2:9], v[212:219], v[108:111]
	v_mfma_f32_16x16x128_f8f6f4 v[100:103], v[2:9], v[222:229], v[100:103]
	v_mfma_f32_16x16x128_f8f6f4 v[104:107], v[10:17], v[222:229], v[104:107]
	s_setprio 0
	s_barrier
	s_add_i32 s50, s50, s82
	s_mov_b64 s[26:27], 0x180
	s_add_i32 s51, s50, 0x2000
	v_lshl_add_u64 v[194:195], v[194:195], 0, s[26:27]
	s_mov_b32 m0, s50
	s_add_u32 s30, s30, 0x20180
	ds_read_b128 v[178:181], v169 offset:49152
	ds_read_b128 v[182:185], v169 offset:50176
	ds_read_b128 v[204:207], v169 offset:51200
	ds_read_b128 v[208:211], v169 offset:52224
	ds_read_b128 v[212:215], v169 offset:53248
	ds_read_b128 v[216:219], v169 offset:54272
	ds_read_b128 v[222:225], v169 offset:55296
	ds_read_b128 v[226:229], v169 offset:56320
	global_load_lds_dwordx4 v[194:195], off
	v_lshl_add_u64 v[194:195], v[196:197], 0, s[26:27]
	s_mov_b32 m0, s51
	s_addc_u32 s31, s31, 0
	s_add_i32 s64, s64, s82
	global_load_lds_dwordx4 v[194:195], off
	v_lshl_add_u64 v[194:195], s[30:31], 0, v[170:171]
	s_mov_b32 m0, s64
	s_add_i32 s63, s64, 0x2000
	global_load_lds_dwordx4 v[194:195], off
	v_lshl_add_u64 v[194:195], s[30:31], 0, v[172:173]
	s_mov_b32 m0, s63
	v_readlane_b32 s26, v253, 39
	global_load_lds_dwordx4 v[194:195], off
	s_mov_b32 m0, s90
	v_readlane_b32 s27, v253, 40
	s_nop 4
	global_load_lds_dwordx4 v34, s[26:27]
	s_mov_b32 m0, s91
	s_nop 0
	global_load_lds_dwordx4 v192, s[26:27]
	s_waitcnt vmcnt(8)
	s_waitcnt lgkmcnt(0)
	s_barrier
	s_setprio 1
	s_waitcnt lgkmcnt(0)
	v_mfma_f32_16x16x128_f8f6f4 v[96:99], v[26:33], v[178:185], v[96:99]
	v_mfma_f32_16x16x128_f8f6f4 v[92:95], v[18:25], v[178:185], v[92:95]
	v_mfma_f32_16x16x128_f8f6f4 v[84:87], v[18:25], v[204:211], v[84:87]
	v_mfma_f32_16x16x128_f8f6f4 v[88:91], v[26:33], v[204:211], v[88:91]
	v_mfma_f32_16x16x128_f8f6f4 v[80:83], v[26:33], v[212:219], v[80:83]
	v_mfma_f32_16x16x128_f8f6f4 v[76:79], v[18:25], v[212:219], v[76:79]
	v_mfma_f32_16x16x128_f8f6f4 v[68:71], v[18:25], v[222:229], v[68:71]
	v_mfma_f32_16x16x128_f8f6f4 v[72:75], v[26:33], v[222:229], v[72:75]
	s_setprio 0
	s_setprio 1
	v_mfma_f32_16x16x128_f8f6f4 v[64:67], v[10:17], v[178:185], v[64:67]
	v_mfma_f32_16x16x128_f8f6f4 v[60:63], v[2:9], v[178:185], v[60:63]
	v_mfma_f32_16x16x128_f8f6f4 v[52:55], v[2:9], v[204:211], v[52:55]
	v_mfma_f32_16x16x128_f8f6f4 v[56:59], v[10:17], v[204:211], v[56:59]
	v_mfma_f32_16x16x128_f8f6f4 v[48:51], v[10:17], v[212:219], v[48:51]
	v_mfma_f32_16x16x128_f8f6f4 v[44:47], v[2:9], v[212:219], v[44:47]
	v_mfma_f32_16x16x128_f8f6f4 v[36:39], v[2:9], v[222:229], v[36:39]
	v_mfma_f32_16x16x128_f8f6f4 v[40:43], v[10:17], v[222:229], v[40:43]
	s_setprio 0
	s_barrier
	v_lshl_add_u64 v[18:19], s[26:27], 0, v[174:175]
	v_lshl_add_u64 v[20:21], s[26:27], 0, v[190:191]
	s_mov_b32 s75, 0
	s_mov_b64 s[30:31], 0
	s_branch .LBB0_955
.LBB0_954:
	ds_read_b128 v[178:181], v200
	ds_read_b128 v[182:185], v200 offset:1024
	ds_read_b128 v[204:207], v200 offset:2048
	ds_read_b128 v[208:211], v200 offset:3072
	ds_read_b128 v[10:13], v199
	ds_read_b128 v[14:17], v199 offset:1024
	ds_read_b128 v[2:5], v199 offset:2048
	ds_read_b128 v[6:9], v199 offset:3072
	s_add_u32 s14, s30, 0x200
	s_addc_u32 vcc_lo, s31, 0
	s_and_b64 s[48:49], s[46:47], exec
	s_cselect_b32 s14, 0, s14
	s_cselect_b32 s49, 0, vcc_lo
	s_add_u32 s48, s20, s14
	s_addc_u32 s49, s21, s49
	s_add_u32 s14, s95, s30
	s_addc_u32 vcc_lo, s96, s31
	s_and_b64 s[46:47], s[46:47], exec
	s_cselect_b32 s47, s43, vcc_lo
	s_cselect_b32 s46, s42, s14
	s_mov_b32 m0, s83
	v_lshl_add_u64 v[30:31], v[20:21], 0, s[30:31]
	ds_read_b128 v[22:25], v169
	ds_read_b128 v[26:29], v169 offset:1024
	ds_read_b128 v[212:215], v169 offset:2048
	ds_read_b128 v[216:219], v169 offset:3072
	ds_read_b128 v[222:225], v169 offset:4096
	ds_read_b128 v[226:229], v169 offset:5120
	ds_read_b128 v[230:233], v169 offset:6144
	ds_read_b128 v[234:237], v169 offset:7168
	global_load_lds_dwordx4 v[30:31], off
	v_lshl_add_u64 v[30:31], v[18:19], 0, s[30:31]
	s_mov_b32 m0, s53
	s_nop 0
	global_load_lds_dwordx4 v[30:31], off
	s_waitcnt vmcnt(8)
	s_waitcnt lgkmcnt(0)
	s_barrier
	s_setprio 1
	s_waitcnt lgkmcnt(0)
	v_mfma_f32_16x16x128_f8f6f4 v[160:163], v[178:185], v[22:29], v[160:163]
	v_mfma_f32_16x16x128_f8f6f4 v[156:159], v[204:211], v[22:29], v[156:159]
	v_mfma_f32_16x16x128_f8f6f4 v[148:151], v[204:211], v[212:219], v[148:151]
	v_mfma_f32_16x16x128_f8f6f4 v[152:155], v[178:185], v[212:219], v[152:155]
	v_mfma_f32_16x16x128_f8f6f4 v[144:147], v[178:185], v[222:229], v[144:147]
	v_mfma_f32_16x16x128_f8f6f4 v[140:143], v[204:211], v[222:229], v[140:143]
	v_mfma_f32_16x16x128_f8f6f4 v[132:135], v[204:211], v[230:237], v[132:135]
	v_mfma_f32_16x16x128_f8f6f4 v[136:139], v[178:185], v[230:237], v[136:139]
	s_setprio 0
	s_setprio 1
	v_mfma_f32_16x16x128_f8f6f4 v[128:131], v[10:17], v[22:29], v[128:131]
	v_mfma_f32_16x16x128_f8f6f4 v[124:127], v[2:9], v[22:29], v[124:127]
	v_mfma_f32_16x16x128_f8f6f4 v[116:119], v[2:9], v[212:219], v[116:119]
	v_mfma_f32_16x16x128_f8f6f4 v[120:123], v[10:17], v[212:219], v[120:123]
	v_mfma_f32_16x16x128_f8f6f4 v[112:115], v[10:17], v[222:229], v[112:115]
	v_mfma_f32_16x16x128_f8f6f4 v[108:111], v[2:9], v[222:229], v[108:111]
	v_mfma_f32_16x16x128_f8f6f4 v[100:103], v[2:9], v[230:237], v[100:103]
	v_mfma_f32_16x16x128_f8f6f4 v[104:107], v[10:17], v[230:237], v[104:107]
	s_setprio 0
	s_barrier
	s_mov_b32 m0, s67
	v_lshl_add_u64 v[22:23], s[46:47], 0, v[170:171]
	s_add_u32 vcc_lo, s46, 0x20000
	ds_read_b128 v[212:215], v169 offset:16384
	ds_read_b128 v[216:219], v169 offset:17408
	ds_read_b128 v[222:225], v169 offset:18432
	ds_read_b128 v[226:229], v169 offset:19456
	ds_read_b128 v[230:233], v169 offset:20480
	ds_read_b128 v[234:237], v169 offset:21504
	ds_read_b128 v[238:241], v169 offset:22528
	ds_read_b128 v[242:245], v169 offset:23552
	global_load_lds_dwordx4 v[22:23], off
	v_lshl_add_u64 v[24:25], s[46:47], 0, v[172:173]
	s_mov_b32 m0, s55
	s_addc_u32 vcc_hi, s47, 0
	global_load_lds_dwordx4 v[24:25], off
	v_lshl_add_u64 v[26:27], vcc, 0, v[170:171]
	s_mov_b32 m0, s65
	v_mov_b32_e32 v193, v35
	global_load_lds_dwordx4 v[26:27], off
	v_lshl_add_u64 v[26:27], vcc, 0, v[172:173]
	s_mov_b32 m0, s54
	v_lshl_add_u64 v[28:29], s[48:49], 0, v[34:35]
	global_load_lds_dwordx4 v[26:27], off
	s_mov_b32 m0, s52
	v_lshl_add_u64 v[26:27], s[48:49], 0, v[192:193]
	global_load_lds_dwordx4 v34, s[48:49]
	s_mov_b32 m0, s84
	s_nop 0
	global_load_lds_dwordx4 v192, s[48:49]
	s_waitcnt vmcnt(8)
	s_waitcnt lgkmcnt(0)
	s_barrier
	s_setprio 1
	s_waitcnt lgkmcnt(0)
	v_mfma_f32_16x16x128_f8f6f4 v[96:99], v[178:185], v[212:219], v[96:99]
	v_mfma_f32_16x16x128_f8f6f4 v[92:95], v[204:211], v[212:219], v[92:95]
	v_mfma_f32_16x16x128_f8f6f4 v[84:87], v[204:211], v[222:229], v[84:87]
	v_mfma_f32_16x16x128_f8f6f4 v[88:91], v[178:185], v[222:229], v[88:91]
	v_mfma_f32_16x16x128_f8f6f4 v[80:83], v[178:185], v[230:237], v[80:83]
	v_mfma_f32_16x16x128_f8f6f4 v[76:79], v[204:211], v[230:237], v[76:79]
	v_mfma_f32_16x16x128_f8f6f4 v[68:71], v[204:211], v[238:245], v[68:71]
	v_mfma_f32_16x16x128_f8f6f4 v[72:75], v[178:185], v[238:245], v[72:75]
	s_setprio 0
	s_setprio 1
	v_mfma_f32_16x16x128_f8f6f4 v[64:67], v[10:17], v[212:219], v[64:67]
	v_mfma_f32_16x16x128_f8f6f4 v[60:63], v[2:9], v[212:219], v[60:63]
	v_mfma_f32_16x16x128_f8f6f4 v[52:55], v[2:9], v[222:229], v[52:55]
	v_mfma_f32_16x16x128_f8f6f4 v[56:59], v[10:17], v[222:229], v[56:59]
	v_mfma_f32_16x16x128_f8f6f4 v[48:51], v[10:17], v[230:237], v[48:51]
	v_mfma_f32_16x16x128_f8f6f4 v[44:47], v[2:9], v[230:237], v[44:47]
	v_mfma_f32_16x16x128_f8f6f4 v[36:39], v[2:9], v[238:245], v[36:39]
	v_mfma_f32_16x16x128_f8f6f4 v[40:43], v[10:17], v[238:245], v[40:43]
	s_setprio 0
	s_barrier
	ds_read_b128 v[178:181], v201
	ds_read_b128 v[182:185], v201 offset:1024
	ds_read_b128 v[204:207], v201 offset:2048
	ds_read_b128 v[208:211], v201 offset:3072
	ds_read_b128 v[10:13], v202
	ds_read_b128 v[14:17], v202 offset:1024
	ds_read_b128 v[2:5], v202 offset:2048
	ds_read_b128 v[6:9], v202 offset:3072
	s_mov_b32 m0, s85
	ds_read_b128 v[212:215], v169 offset:32768
	ds_read_b128 v[216:219], v169 offset:33792
	ds_read_b128 v[222:225], v169 offset:34816
	ds_read_b128 v[226:229], v169 offset:35840
	ds_read_b128 v[230:233], v169 offset:36864
	ds_read_b128 v[234:237], v169 offset:37888
	ds_read_b128 v[238:241], v169 offset:38912
	ds_read_b128 v[242:245], v169 offset:39936
	global_load_lds_dwordx4 v189, s[48:49]
	s_mov_b32 m0, s86
	s_nop 0
	global_load_lds_dwordx4 v198, s[48:49]
	s_waitcnt vmcnt(8)
	s_waitcnt lgkmcnt(0)
	s_barrier
	s_setprio 1
	s_waitcnt lgkmcnt(0)
	v_mfma_f32_16x16x128_f8f6f4 v[160:163], v[178:185], v[212:219], v[160:163]
	v_mfma_f32_16x16x128_f8f6f4 v[156:159], v[204:211], v[212:219], v[156:159]
	v_mfma_f32_16x16x128_f8f6f4 v[148:151], v[204:211], v[222:229], v[148:151]
	v_mfma_f32_16x16x128_f8f6f4 v[152:155], v[178:185], v[222:229], v[152:155]
	v_mfma_f32_16x16x128_f8f6f4 v[144:147], v[178:185], v[230:237], v[144:147]
	v_mfma_f32_16x16x128_f8f6f4 v[140:143], v[204:211], v[230:237], v[140:143]
	v_mfma_f32_16x16x128_f8f6f4 v[132:135], v[204:211], v[238:245], v[132:135]
	v_mfma_f32_16x16x128_f8f6f4 v[136:139], v[178:185], v[238:245], v[136:139]
	s_setprio 0
	s_setprio 1
	v_mfma_f32_16x16x128_f8f6f4 v[128:131], v[10:17], v[212:219], v[128:131]
	v_mfma_f32_16x16x128_f8f6f4 v[124:127], v[2:9], v[212:219], v[124:127]
	v_mfma_f32_16x16x128_f8f6f4 v[116:119], v[2:9], v[222:229], v[116:119]
	v_mfma_f32_16x16x128_f8f6f4 v[120:123], v[10:17], v[222:229], v[120:123]
	v_mfma_f32_16x16x128_f8f6f4 v[112:115], v[10:17], v[230:237], v[112:115]
	v_mfma_f32_16x16x128_f8f6f4 v[108:111], v[2:9], v[230:237], v[108:111]
	v_mfma_f32_16x16x128_f8f6f4 v[100:103], v[2:9], v[238:245], v[100:103]
	v_mfma_f32_16x16x128_f8f6f4 v[104:107], v[10:17], v[238:245], v[104:107]
	s_setprio 0
	s_barrier
	s_mov_b32 m0, s50
	v_lshl_add_u64 v[22:23], v[22:23], 0, s[18:19]
	s_add_u32 s46, s46, 0x20080
	ds_read_b128 v[212:215], v169 offset:49152
	ds_read_b128 v[216:219], v169 offset:50176
	ds_read_b128 v[222:225], v169 offset:51200
	ds_read_b128 v[226:229], v169 offset:52224
	ds_read_b128 v[230:233], v169 offset:53248
	ds_read_b128 v[234:237], v169 offset:54272
	ds_read_b128 v[238:241], v169 offset:55296
	ds_read_b128 v[242:245], v169 offset:56320
	global_load_lds_dwordx4 v[22:23], off
	v_lshl_add_u64 v[22:23], v[24:25], 0, s[18:19]
	s_mov_b32 m0, s51
	s_addc_u32 s47, s47, 0
	global_load_lds_dwordx4 v[22:23], off
	v_lshl_add_u64 v[22:23], s[46:47], 0, v[170:171]
	s_mov_b32 m0, s64
	s_nop 0
	global_load_lds_dwordx4 v[22:23], off
	v_lshl_add_u64 v[22:23], s[46:47], 0, v[172:173]
	s_mov_b32 m0, s63
	s_nop 0
	global_load_lds_dwordx4 v[22:23], off
	v_lshl_add_u64 v[22:23], v[28:29], 0, s[18:19]
	s_mov_b32 m0, s90
	s_nop 0
	global_load_lds_dwordx4 v[22:23], off
	v_lshl_add_u64 v[22:23], v[26:27], 0, s[18:19]
	s_mov_b32 m0, s91
	s_nop 0
	global_load_lds_dwordx4 v[22:23], off
	s_waitcnt vmcnt(8)
	s_waitcnt lgkmcnt(0)
	s_barrier
	s_setprio 1
	s_waitcnt lgkmcnt(0)
	v_mfma_f32_16x16x128_f8f6f4 v[96:99], v[178:185], v[212:219], v[96:99]
	v_mfma_f32_16x16x128_f8f6f4 v[92:95], v[204:211], v[212:219], v[92:95]
	v_mfma_f32_16x16x128_f8f6f4 v[84:87], v[204:211], v[222:229], v[84:87]
	v_mfma_f32_16x16x128_f8f6f4 v[88:91], v[178:185], v[222:229], v[88:91]
	v_mfma_f32_16x16x128_f8f6f4 v[80:83], v[178:185], v[230:237], v[80:83]
	v_mfma_f32_16x16x128_f8f6f4 v[76:79], v[204:211], v[230:237], v[76:79]
	v_mfma_f32_16x16x128_f8f6f4 v[68:71], v[204:211], v[238:245], v[68:71]
	v_mfma_f32_16x16x128_f8f6f4 v[72:75], v[178:185], v[238:245], v[72:75]
	s_setprio 0
	s_setprio 1
	v_mfma_f32_16x16x128_f8f6f4 v[64:67], v[10:17], v[212:219], v[64:67]
	v_mfma_f32_16x16x128_f8f6f4 v[60:63], v[2:9], v[212:219], v[60:63]
	v_mfma_f32_16x16x128_f8f6f4 v[52:55], v[2:9], v[222:229], v[52:55]
	v_mfma_f32_16x16x128_f8f6f4 v[56:59], v[10:17], v[222:229], v[56:59]
	v_mfma_f32_16x16x128_f8f6f4 v[48:51], v[10:17], v[230:237], v[48:51]
	v_mfma_f32_16x16x128_f8f6f4 v[44:47], v[2:9], v[230:237], v[44:47]
	v_mfma_f32_16x16x128_f8f6f4 v[36:39], v[2:9], v[238:245], v[36:39]
	v_mfma_f32_16x16x128_f8f6f4 v[40:43], v[10:17], v[238:245], v[40:43]
	s_setprio 0
	s_barrier
	s_add_i32 s75, s75, 2
	s_add_u32 s30, s30, 0x100
	s_addc_u32 s31, s31, 0
	s_cmp_gt_u32 s75, 5
	s_cbranch_scc1 .LBB0_957

.LBB0_1086:
	s_lshl_b32 s10, s51, 18
	s_add_u32 s10, s20, s10
	s_addc_u32 s11, s21, 0
	s_and_b64 s[16:17], s[4:5], exec
	s_cselect_b32 s54, s11, s31
	s_cselect_b32 s55, s10, s30
	s_lshl_b32 s14, s50, 18
	s_add_u32 s16, s15, s14
	s_addc_u32 s17, s26, 0
	s_and_b64 s[36:37], s[4:5], exec
	s_cselect_b32 s56, s17, s23
	s_cselect_b32 s57, s16, s22
	s_add_i32 s60, 0, 0x10000
	s_add_i32 s62, 0, 0x14000
	v_add_u32_e32 v198, s60, v196
	v_add_u32_e32 v199, s62, v196
	ds_read_b128 v[26:29], v198
	ds_read_b128 v[30:33], v198 offset:1024
	ds_read_b128 v[18:21], v198 offset:2048
	ds_read_b128 v[22:25], v198 offset:3072
	ds_read_b128 v[10:13], v199
	ds_read_b128 v[14:17], v199 offset:1024
	ds_read_b128 v[2:5], v199 offset:2048
	ds_read_b128 v[6:9], v199 offset:3072
	s_add_u32 s36, s30, 0x20080
	s_addc_u32 s37, s31, 0
	s_add_i32 s58, s41, 0xc000
	v_lshl_add_u64 v[174:175], s[36:37], 0, v[168:169]
	s_mov_b32 m0, s58
	s_add_i32 s59, s41, 0xe000
	ds_read_b128 v[200:203], v197
	ds_read_b128 v[204:207], v197 offset:1024
	ds_read_b128 v[222:225], v197 offset:2048
	ds_read_b128 v[226:229], v197 offset:3072
	ds_read_b128 v[230:233], v197 offset:4096
	ds_read_b128 v[234:237], v197 offset:5120
	ds_read_b128 v[238:241], v197 offset:6144
	ds_read_b128 v[242:245], v197 offset:7168
	global_load_lds_dwordx4 v[174:175], off
	v_lshl_add_u64 v[174:175], s[36:37], 0, v[166:167]
	s_mov_b32 m0, s59
	s_nop 0
	global_load_lds_dwordx4 v[174:175], off
	s_waitcnt vmcnt(8)
	s_waitcnt lgkmcnt(0)
	s_barrier
	s_setprio 1
	s_waitcnt lgkmcnt(0)
	v_mfma_f32_16x16x128_f8f6f4 v[160:163], v[26:33], v[200:207], 0
	v_mfma_f32_16x16x128_f8f6f4 v[156:159], v[18:25], v[200:207], 0
	v_mfma_f32_16x16x128_f8f6f4 v[148:151], v[18:25], v[222:229], 0
	v_mfma_f32_16x16x128_f8f6f4 v[152:155], v[26:33], v[222:229], 0
	v_mfma_f32_16x16x128_f8f6f4 v[144:147], v[26:33], v[230:237], 0
	v_mfma_f32_16x16x128_f8f6f4 v[140:143], v[18:25], v[230:237], 0
	v_mfma_f32_16x16x128_f8f6f4 v[132:135], v[18:25], v[238:245], 0
	v_mfma_f32_16x16x128_f8f6f4 v[136:139], v[26:33], v[238:245], 0
	s_setprio 0
	s_setprio 1
	v_mfma_f32_16x16x128_f8f6f4 v[128:131], v[10:17], v[200:207], 0
	v_mfma_f32_16x16x128_f8f6f4 v[124:127], v[2:9], v[200:207], 0
	v_mfma_f32_16x16x128_f8f6f4 v[116:119], v[2:9], v[222:229], 0
	v_mfma_f32_16x16x128_f8f6f4 v[120:123], v[10:17], v[222:229], 0
	v_mfma_f32_16x16x128_f8f6f4 v[112:115], v[10:17], v[230:237], 0
	v_mfma_f32_16x16x128_f8f6f4 v[108:111], v[2:9], v[230:237], 0
	v_mfma_f32_16x16x128_f8f6f4 v[100:103], v[2:9], v[238:245], 0
	v_mfma_f32_16x16x128_f8f6f4 v[104:107], v[10:17], v[238:245], 0
	s_setprio 0
	s_barrier
	s_add_i32 s60, s60, s40
	v_lshl_add_u64 v[174:175], s[22:23], 0, v[34:35]
	s_add_i32 s61, s60, 0x2000
	v_lshl_add_u64 v[178:179], v[174:175], 0, s[28:29]
	s_mov_b32 m0, s60
	v_lshl_add_u64 v[190:191], s[22:23], 0, v[164:165]
	s_add_u32 s36, s22, 0x20100
	ds_read_b128 v[200:203], v197 offset:16384
	ds_read_b128 v[204:207], v197 offset:17408
	ds_read_b128 v[222:225], v197 offset:18432
	ds_read_b128 v[226:229], v197 offset:19456
	ds_read_b128 v[230:233], v197 offset:20480
	ds_read_b128 v[234:237], v197 offset:21504
	ds_read_b128 v[238:241], v197 offset:22528
	ds_read_b128 v[242:245], v197 offset:23552
	global_load_lds_dwordx4 v[178:179], off
	v_lshl_add_u64 v[178:179], v[190:191], 0, s[28:29]
	s_mov_b32 m0, s61
	s_addc_u32 s37, s23, 0
	s_add_i32 s62, s62, s40
	global_load_lds_dwordx4 v[178:179], off
	v_lshl_add_u64 v[178:179], s[36:37], 0, v[34:35]
	s_mov_b32 m0, s62
	s_add_i32 s63, s62, 0x2000
	global_load_lds_dwordx4 v[178:179], off
	v_lshl_add_u64 v[178:179], s[36:37], 0, v[164:165]
	s_mov_b32 m0, s63
	v_lshl_add_u64 v[192:193], s[30:31], 0, v[168:169]
	global_load_lds_dwordx4 v[178:179], off
	v_lshl_add_u64 v[178:179], v[192:193], 0, s[28:29]
	s_mov_b32 m0, s41
	v_lshl_add_u64 v[194:195], s[30:31], 0, v[166:167]
	global_load_lds_dwordx4 v[178:179], off
	v_lshl_add_u64 v[178:179], v[194:195], 0, s[28:29]
	s_mov_b32 m0, s42
	s_nop 0
	global_load_lds_dwordx4 v[178:179], off
	s_waitcnt vmcnt(8)
	s_waitcnt lgkmcnt(0)
	s_barrier
	s_setprio 1
	s_waitcnt lgkmcnt(0)
	v_mfma_f32_16x16x128_f8f6f4 v[96:99], v[26:33], v[200:207], 0
	v_mfma_f32_16x16x128_f8f6f4 v[92:95], v[18:25], v[200:207], 0
	v_mfma_f32_16x16x128_f8f6f4 v[84:87], v[18:25], v[222:229], 0
	v_mfma_f32_16x16x128_f8f6f4 v[88:91], v[26:33], v[222:229], 0
	v_mfma_f32_16x16x128_f8f6f4 v[80:83], v[26:33], v[230:237], 0
	v_mfma_f32_16x16x128_f8f6f4 v[76:79], v[18:25], v[230:237], 0
	v_mfma_f32_16x16x128_f8f6f4 v[68:71], v[18:25], v[238:245], 0
	v_mfma_f32_16x16x128_f8f6f4 v[72:75], v[26:33], v[238:245], 0
	s_setprio 0
	s_setprio 1
	v_mfma_f32_16x16x128_f8f6f4 v[64:67], v[10:17], v[200:207], 0
	v_mfma_f32_16x16x128_f8f6f4 v[60:63], v[2:9], v[200:207], 0
	v_mfma_f32_16x16x128_f8f6f4 v[52:55], v[2:9], v[222:229], 0
	v_mfma_f32_16x16x128_f8f6f4 v[56:59], v[10:17], v[222:229], 0
	v_mfma_f32_16x16x128_f8f6f4 v[48:51], v[10:17], v[230:237], 0
	v_mfma_f32_16x16x128_f8f6f4 v[44:47], v[2:9], v[230:237], 0
	v_mfma_f32_16x16x128_f8f6f4 v[36:39], v[2:9], v[238:245], 0
	v_mfma_f32_16x16x128_f8f6f4 v[40:43], v[10:17], v[238:245], 0
	s_setprio 0
	s_barrier
	s_add_i32 s64, 0, 0x18000
	s_add_i32 s66, 0, 0x1c000
	v_add_u32_e32 v200, s64, v196
	v_add_u32_e32 v201, s66, v196
	ds_read_b128 v[26:29], v200
	ds_read_b128 v[30:33], v200 offset:1024
	ds_read_b128 v[18:21], v200 offset:2048
	ds_read_b128 v[22:25], v200 offset:3072
	ds_read_b128 v[10:13], v201
	ds_read_b128 v[14:17], v201 offset:1024
	ds_read_b128 v[2:5], v201 offset:2048
	ds_read_b128 v[6:9], v201 offset:3072
	s_add_u32 s36, s30, 0x20100
	s_addc_u32 s37, s31, 0
	s_mov_b32 m0, s43
	v_lshl_add_u64 v[178:179], s[36:37], 0, v[168:169]
	ds_read_b128 v[202:205], v197 offset:32768
	ds_read_b128 v[206:209], v197 offset:33792
	ds_read_b128 v[222:225], v197 offset:34816
	ds_read_b128 v[226:229], v197 offset:35840
	ds_read_b128 v[230:233], v197 offset:36864
	ds_read_b128 v[234:237], v197 offset:37888
	ds_read_b128 v[238:241], v197 offset:38912
	ds_read_b128 v[242:245], v197 offset:39936
	global_load_lds_dwordx4 v[178:179], off
	v_lshl_add_u64 v[178:179], s[36:37], 0, v[166:167]
	s_mov_b32 m0, s44
	s_nop 0
	global_load_lds_dwordx4 v[178:179], off
	s_waitcnt vmcnt(8)
	s_waitcnt lgkmcnt(0)
	s_barrier
	s_setprio 1
	s_waitcnt lgkmcnt(0)
	v_mfma_f32_16x16x128_f8f6f4 v[160:163], v[26:33], v[202:209], v[160:163]
	v_mfma_f32_16x16x128_f8f6f4 v[156:159], v[18:25], v[202:209], v[156:159]
	v_mfma_f32_16x16x128_f8f6f4 v[148:151], v[18:25], v[222:229], v[148:151]
	v_mfma_f32_16x16x128_f8f6f4 v[152:155], v[26:33], v[222:229], v[152:155]
	v_mfma_f32_16x16x128_f8f6f4 v[144:147], v[26:33], v[230:237], v[144:147]
	v_mfma_f32_16x16x128_f8f6f4 v[140:143], v[18:25], v[230:237], v[140:143]
	v_mfma_f32_16x16x128_f8f6f4 v[132:135], v[18:25], v[238:245], v[132:135]
	v_mfma_f32_16x16x128_f8f6f4 v[136:139], v[26:33], v[238:245], v[136:139]
	s_setprio 0
	s_setprio 1
	v_mfma_f32_16x16x128_f8f6f4 v[128:131], v[10:17], v[202:209], v[128:131]
	v_mfma_f32_16x16x128_f8f6f4 v[124:127], v[2:9], v[202:209], v[124:127]
	v_mfma_f32_16x16x128_f8f6f4 v[116:119], v[2:9], v[222:229], v[116:119]
	v_mfma_f32_16x16x128_f8f6f4 v[120:123], v[10:17], v[222:229], v[120:123]
	v_mfma_f32_16x16x128_f8f6f4 v[112:115], v[10:17], v[230:237], v[112:115]
	v_mfma_f32_16x16x128_f8f6f4 v[108:111], v[2:9], v[230:237], v[108:111]
	v_mfma_f32_16x16x128_f8f6f4 v[100:103], v[2:9], v[238:245], v[100:103]
	v_mfma_f32_16x16x128_f8f6f4 v[104:107], v[10:17], v[238:245], v[104:107]
	s_setprio 0
	s_barrier
	s_add_i32 s64, s64, s40
	s_mov_b64 s[24:25], 0x180
	s_add_i32 s65, s64, 0x2000
	v_lshl_add_u64 v[174:175], v[174:175], 0, s[24:25]
	s_mov_b32 m0, s64
	s_add_u32 s36, s22, 0x20180
	ds_read_b128 v[202:205], v197 offset:49152
	ds_read_b128 v[206:209], v197 offset:50176
	ds_read_b128 v[222:225], v197 offset:51200
	ds_read_b128 v[226:229], v197 offset:52224
	ds_read_b128 v[230:233], v197 offset:53248
	ds_read_b128 v[234:237], v197 offset:54272
	ds_read_b128 v[238:241], v197 offset:55296
	ds_read_b128 v[242:245], v197 offset:56320
	global_load_lds_dwordx4 v[174:175], off
	v_lshl_add_u64 v[174:175], v[190:191], 0, s[24:25]
	s_mov_b32 m0, s65
	s_addc_u32 s37, s23, 0
	s_add_i32 s66, s66, s40
	global_load_lds_dwordx4 v[174:175], off
	v_lshl_add_u64 v[174:175], s[36:37], 0, v[34:35]
	s_mov_b32 m0, s66
	s_add_i32 s67, s66, 0x2000
	global_load_lds_dwordx4 v[174:175], off
	v_lshl_add_u64 v[174:175], s[36:37], 0, v[164:165]
	s_mov_b32 m0, s67
	s_nop 0
	global_load_lds_dwordx4 v[174:175], off
	v_lshl_add_u64 v[174:175], v[192:193], 0, s[24:25]
	s_mov_b32 m0, s47
	s_nop 0
	global_load_lds_dwordx4 v[174:175], off
	v_lshl_add_u64 v[174:175], v[194:195], 0, s[24:25]
	s_mov_b32 m0, s48
	s_nop 0
	global_load_lds_dwordx4 v[174:175], off
	s_waitcnt vmcnt(8)
	s_waitcnt lgkmcnt(0)
	s_barrier
	s_setprio 1
	s_waitcnt lgkmcnt(0)
	v_mfma_f32_16x16x128_f8f6f4 v[96:99], v[26:33], v[202:209], v[96:99]
	v_mfma_f32_16x16x128_f8f6f4 v[92:95], v[18:25], v[202:209], v[92:95]
	v_mfma_f32_16x16x128_f8f6f4 v[84:87], v[18:25], v[222:229], v[84:87]
	v_mfma_f32_16x16x128_f8f6f4 v[88:91], v[26:33], v[222:229], v[88:91]
	v_mfma_f32_16x16x128_f8f6f4 v[80:83], v[26:33], v[230:237], v[80:83]
	v_mfma_f32_16x16x128_f8f6f4 v[76:79], v[18:25], v[230:237], v[76:79]
	v_mfma_f32_16x16x128_f8f6f4 v[68:71], v[18:25], v[238:245], v[68:71]
	v_mfma_f32_16x16x128_f8f6f4 v[72:75], v[26:33], v[238:245], v[72:75]
	s_setprio 0
	s_setprio 1
	v_mfma_f32_16x16x128_f8f6f4 v[64:67], v[10:17], v[202:209], v[64:67]
	v_mfma_f32_16x16x128_f8f6f4 v[60:63], v[2:9], v[202:209], v[60:63]
	v_mfma_f32_16x16x128_f8f6f4 v[52:55], v[2:9], v[222:229], v[52:55]
	v_mfma_f32_16x16x128_f8f6f4 v[56:59], v[10:17], v[222:229], v[56:59]
	v_mfma_f32_16x16x128_f8f6f4 v[48:51], v[10:17], v[230:237], v[48:51]
	v_mfma_f32_16x16x128_f8f6f4 v[44:47], v[2:9], v[230:237], v[44:47]
	v_mfma_f32_16x16x128_f8f6f4 v[36:39], v[2:9], v[238:245], v[36:39]
	v_mfma_f32_16x16x128_f8f6f4 v[40:43], v[10:17], v[238:245], v[40:43]
	s_setprio 0
	s_barrier
	s_add_u32 s30, s30, 0x20180
	s_addc_u32 s31, s31, 0
	s_add_u32 s68, s22, 0x200
	s_addc_u32 s69, s23, 0
	s_mov_b32 s70, 0
.LBB0_1087:
	ds_read_b128 v[2:5], v198
	ds_read_b128 v[6:9], v198 offset:1024
	ds_read_b128 v[10:13], v198 offset:2048
	ds_read_b128 v[14:17], v198 offset:3072
	ds_read_b128 v[18:21], v199
	ds_read_b128 v[22:25], v199 offset:1024
	ds_read_b128 v[26:29], v199 offset:2048
	ds_read_b128 v[30:33], v199 offset:3072
	s_add_u32 s14, s30, 0xfffe0080
	s_addc_u32 s22, s31, -1
	s_cmp_eq_u32 s70, 4
	s_cselect_b32 s37, s54, s22
	s_cselect_b32 s36, s55, s14
	s_cselect_b32 s23, s56, s69
	s_cselect_b32 s22, s57, s68
	s_mov_b32 m0, s58
	v_lshl_add_u64 v[174:175], s[30:31], 0, v[170:171]
	ds_read_b128 v[202:205], v197
	ds_read_b128 v[206:209], v197 offset:1024
	ds_read_b128 v[222:225], v197 offset:2048
	ds_read_b128 v[226:229], v197 offset:3072
	ds_read_b128 v[230:233], v197 offset:4096
	ds_read_b128 v[234:237], v197 offset:5120
	ds_read_b128 v[238:241], v197 offset:6144
	ds_read_b128 v[242:245], v197 offset:7168
	global_load_lds_dwordx4 v[174:175], off
	v_lshl_add_u64 v[174:175], s[30:31], 0, v[172:173]
	s_mov_b32 m0, s59
	s_nop 0
	global_load_lds_dwordx4 v[174:175], off
	s_waitcnt vmcnt(8)
	s_waitcnt lgkmcnt(0)
	s_barrier
	s_setprio 1
	s_waitcnt lgkmcnt(0)
	v_mfma_f32_16x16x128_f8f6f4 v[160:163], v[2:9], v[202:209], v[160:163]
	v_mfma_f32_16x16x128_f8f6f4 v[156:159], v[10:17], v[202:209], v[156:159]
	v_mfma_f32_16x16x128_f8f6f4 v[148:151], v[10:17], v[222:229], v[148:151]
	v_mfma_f32_16x16x128_f8f6f4 v[152:155], v[2:9], v[222:229], v[152:155]
	v_mfma_f32_16x16x128_f8f6f4 v[144:147], v[2:9], v[230:237], v[144:147]
	v_mfma_f32_16x16x128_f8f6f4 v[140:143], v[10:17], v[230:237], v[140:143]
	v_mfma_f32_16x16x128_f8f6f4 v[132:135], v[10:17], v[238:245], v[132:135]
	v_mfma_f32_16x16x128_f8f6f4 v[136:139], v[2:9], v[238:245], v[136:139]
	s_setprio 0
	s_setprio 1
	v_mfma_f32_16x16x128_f8f6f4 v[128:131], v[18:25], v[202:209], v[128:131]
	v_mfma_f32_16x16x128_f8f6f4 v[124:127], v[26:33], v[202:209], v[124:127]
	v_mfma_f32_16x16x128_f8f6f4 v[116:119], v[26:33], v[222:229], v[116:119]
	v_mfma_f32_16x16x128_f8f6f4 v[120:123], v[18:25], v[222:229], v[120:123]
	v_mfma_f32_16x16x128_f8f6f4 v[112:115], v[18:25], v[230:237], v[112:115]
	v_mfma_f32_16x16x128_f8f6f4 v[108:111], v[26:33], v[230:237], v[108:111]
	v_mfma_f32_16x16x128_f8f6f4 v[100:103], v[26:33], v[238:245], v[100:103]
	v_mfma_f32_16x16x128_f8f6f4 v[104:107], v[18:25], v[238:245], v[104:107]
	s_setprio 0
	s_barrier
	s_mov_b32 m0, s60
	v_lshl_add_u64 v[174:175], s[22:23], 0, v[34:35]
	s_add_u32 s72, s22, 0x20000
	ds_read_b128 v[202:205], v197 offset:16384
	ds_read_b128 v[206:209], v197 offset:17408
	ds_read_b128 v[222:225], v197 offset:18432
	ds_read_b128 v[226:229], v197 offset:19456
	ds_read_b128 v[230:233], v197 offset:20480
	ds_read_b128 v[234:237], v197 offset:21504
	ds_read_b128 v[238:241], v197 offset:22528
	ds_read_b128 v[242:245], v197 offset:23552
	global_load_lds_dwordx4 v[174:175], off
	v_lshl_add_u64 v[190:191], s[22:23], 0, v[164:165]
	s_mov_b32 m0, s61
	s_addc_u32 s73, s23, 0
	global_load_lds_dwordx4 v[190:191], off
	v_lshl_add_u64 v[178:179], s[72:73], 0, v[34:35]
	s_mov_b32 m0, s62
	v_lshl_add_u64 v[192:193], s[36:37], 0, v[168:169]
	global_load_lds_dwordx4 v[178:179], off
	v_lshl_add_u64 v[178:179], s[72:73], 0, v[164:165]
	s_mov_b32 m0, s63
	v_lshl_add_u64 v[194:195], s[36:37], 0, v[166:167]
	global_load_lds_dwordx4 v[178:179], off
	s_mov_b32 m0, s41
	s_nop 0
	global_load_lds_dwordx4 v[192:193], off
	s_mov_b32 m0, s42
	s_nop 0
	global_load_lds_dwordx4 v[194:195], off
	s_waitcnt vmcnt(8)
	s_waitcnt lgkmcnt(0)
	s_barrier
	s_setprio 1
	s_waitcnt lgkmcnt(0)
	v_mfma_f32_16x16x128_f8f6f4 v[96:99], v[2:9], v[202:209], v[96:99]
	v_mfma_f32_16x16x128_f8f6f4 v[92:95], v[10:17], v[202:209], v[92:95]
	v_mfma_f32_16x16x128_f8f6f4 v[84:87], v[10:17], v[222:229], v[84:87]
	v_mfma_f32_16x16x128_f8f6f4 v[88:91], v[2:9], v[222:229], v[88:91]
	v_mfma_f32_16x16x128_f8f6f4 v[80:83], v[2:9], v[230:237], v[80:83]
	v_mfma_f32_16x16x128_f8f6f4 v[76:79], v[10:17], v[230:237], v[76:79]
	v_mfma_f32_16x16x128_f8f6f4 v[68:71], v[10:17], v[238:245], v[68:71]
	v_mfma_f32_16x16x128_f8f6f4 v[72:75], v[2:9], v[238:245], v[72:75]
	s_setprio 0
	s_setprio 1
	v_mfma_f32_16x16x128_f8f6f4 v[64:67], v[18:25], v[202:209], v[64:67]
	v_mfma_f32_16x16x128_f8f6f4 v[60:63], v[26:33], v[202:209], v[60:63]
	v_mfma_f32_16x16x128_f8f6f4 v[52:55], v[26:33], v[222:229], v[52:55]
	v_mfma_f32_16x16x128_f8f6f4 v[56:59], v[18:25], v[222:229], v[56:59]
	v_mfma_f32_16x16x128_f8f6f4 v[48:51], v[18:25], v[230:237], v[48:51]
	v_mfma_f32_16x16x128_f8f6f4 v[44:47], v[26:33], v[230:237], v[44:47]
	v_mfma_f32_16x16x128_f8f6f4 v[36:39], v[26:33], v[238:245], v[36:39]
	v_mfma_f32_16x16x128_f8f6f4 v[40:43], v[18:25], v[238:245], v[40:43]
	s_setprio 0
	s_barrier
	ds_read_b128 v[26:29], v200
	ds_read_b128 v[30:33], v200 offset:1024
	ds_read_b128 v[18:21], v200 offset:2048
	ds_read_b128 v[22:25], v200 offset:3072
	ds_read_b128 v[10:13], v201
	ds_read_b128 v[14:17], v201 offset:1024
	ds_read_b128 v[2:5], v201 offset:2048
	ds_read_b128 v[6:9], v201 offset:3072
	s_add_u32 s36, s36, 0x20000
	s_addc_u32 s37, s37, 0
	s_mov_b32 m0, s43
	v_lshl_add_u64 v[178:179], s[36:37], 0, v[168:169]
	ds_read_b128 v[202:205], v197 offset:32768
	ds_read_b128 v[206:209], v197 offset:33792
	ds_read_b128 v[222:225], v197 offset:34816
	ds_read_b128 v[226:229], v197 offset:35840
	ds_read_b128 v[230:233], v197 offset:36864
	ds_read_b128 v[234:237], v197 offset:37888
	ds_read_b128 v[238:241], v197 offset:38912
	ds_read_b128 v[242:245], v197 offset:39936
	global_load_lds_dwordx4 v[178:179], off
	v_lshl_add_u64 v[178:179], s[36:37], 0, v[166:167]
	s_mov_b32 m0, s44
	s_nop 0
	global_load_lds_dwordx4 v[178:179], off
	s_waitcnt vmcnt(8)
	s_waitcnt lgkmcnt(0)
	s_barrier
	s_setprio 1
	s_waitcnt lgkmcnt(0)
	v_mfma_f32_16x16x128_f8f6f4 v[160:163], v[26:33], v[202:209], v[160:163]
	v_mfma_f32_16x16x128_f8f6f4 v[156:159], v[18:25], v[202:209], v[156:159]
	v_mfma_f32_16x16x128_f8f6f4 v[148:151], v[18:25], v[222:229], v[148:151]
	v_mfma_f32_16x16x128_f8f6f4 v[152:155], v[26:33], v[222:229], v[152:155]
	v_mfma_f32_16x16x128_f8f6f4 v[144:147], v[26:33], v[230:237], v[144:147]
	v_mfma_f32_16x16x128_f8f6f4 v[140:143], v[18:25], v[230:237], v[140:143]
	v_mfma_f32_16x16x128_f8f6f4 v[132:135], v[18:25], v[238:245], v[132:135]
	v_mfma_f32_16x16x128_f8f6f4 v[136:139], v[26:33], v[238:245], v[136:139]
	s_setprio 0
	s_setprio 1
	v_mfma_f32_16x16x128_f8f6f4 v[128:131], v[10:17], v[202:209], v[128:131]
	v_mfma_f32_16x16x128_f8f6f4 v[124:127], v[2:9], v[202:209], v[124:127]
	v_mfma_f32_16x16x128_f8f6f4 v[116:119], v[2:9], v[222:229], v[116:119]
	v_mfma_f32_16x16x128_f8f6f4 v[120:123], v[10:17], v[222:229], v[120:123]
	v_mfma_f32_16x16x128_f8f6f4 v[112:115], v[10:17], v[230:237], v[112:115]
	v_mfma_f32_16x16x128_f8f6f4 v[108:111], v[2:9], v[230:237], v[108:111]
	v_mfma_f32_16x16x128_f8f6f4 v[100:103], v[2:9], v[238:245], v[100:103]
	v_mfma_f32_16x16x128_f8f6f4 v[104:107], v[10:17], v[238:245], v[104:107]
	s_setprio 0
	s_barrier
	s_mov_b32 m0, s64
	v_lshl_add_u64 v[174:175], v[174:175], 0, s[18:19]
	s_add_u32 s22, s22, 0x20080
	ds_read_b128 v[202:205], v197 offset:49152
	ds_read_b128 v[206:209], v197 offset:50176
	ds_read_b128 v[222:225], v197 offset:51200
	ds_read_b128 v[226:229], v197 offset:52224
	ds_read_b128 v[230:233], v197 offset:53248
	ds_read_b128 v[234:237], v197 offset:54272
	ds_read_b128 v[238:241], v197 offset:55296
	ds_read_b128 v[242:245], v197 offset:56320
	global_load_lds_dwordx4 v[174:175], off
	v_lshl_add_u64 v[174:175], v[190:191], 0, s[18:19]
	s_mov_b32 m0, s65
	s_addc_u32 s23, s23, 0
	global_load_lds_dwordx4 v[174:175], off
	v_lshl_add_u64 v[174:175], s[22:23], 0, v[34:35]
	s_mov_b32 m0, s66
	s_nop 0
	global_load_lds_dwordx4 v[174:175], off
	v_lshl_add_u64 v[174:175], s[22:23], 0, v[164:165]
	s_mov_b32 m0, s67
	s_nop 0
	global_load_lds_dwordx4 v[174:175], off
	v_lshl_add_u64 v[174:175], v[192:193], 0, s[18:19]
	s_mov_b32 m0, s47
	s_nop 0
	global_load_lds_dwordx4 v[174:175], off
	v_lshl_add_u64 v[174:175], v[194:195], 0, s[18:19]
	s_mov_b32 m0, s48
	s_nop 0
	global_load_lds_dwordx4 v[174:175], off
	s_waitcnt vmcnt(8)
	s_waitcnt lgkmcnt(0)
	s_barrier
	s_setprio 1
	s_waitcnt lgkmcnt(0)
	v_mfma_f32_16x16x128_f8f6f4 v[96:99], v[26:33], v[202:209], v[96:99]
	v_mfma_f32_16x16x128_f8f6f4 v[92:95], v[18:25], v[202:209], v[92:95]
	v_mfma_f32_16x16x128_f8f6f4 v[84:87], v[18:25], v[222:229], v[84:87]
	v_mfma_f32_16x16x128_f8f6f4 v[88:91], v[26:33], v[222:229], v[88:91]
	v_mfma_f32_16x16x128_f8f6f4 v[80:83], v[26:33], v[230:237], v[80:83]
	v_mfma_f32_16x16x128_f8f6f4 v[76:79], v[18:25], v[230:237], v[76:79]
	v_mfma_f32_16x16x128_f8f6f4 v[68:71], v[18:25], v[238:245], v[68:71]
	v_mfma_f32_16x16x128_f8f6f4 v[72:75], v[26:33], v[238:245], v[72:75]
	s_setprio 0
	s_setprio 1
	v_mfma_f32_16x16x128_f8f6f4 v[64:67], v[10:17], v[202:209], v[64:67]
	v_mfma_f32_16x16x128_f8f6f4 v[60:63], v[2:9], v[202:209], v[60:63]
	v_mfma_f32_16x16x128_f8f6f4 v[52:55], v[2:9], v[222:229], v[52:55]
	v_mfma_f32_16x16x128_f8f6f4 v[56:59], v[10:17], v[222:229], v[56:59]
	v_mfma_f32_16x16x128_f8f6f4 v[48:51], v[10:17], v[230:237], v[48:51]
	v_mfma_f32_16x16x128_f8f6f4 v[44:47], v[2:9], v[230:237], v[44:47]
	v_mfma_f32_16x16x128_f8f6f4 v[36:39], v[2:9], v[238:245], v[36:39]
	v_mfma_f32_16x16x128_f8f6f4 v[40:43], v[10:17], v[238:245], v[40:43]
	s_setprio 0
	s_barrier
	s_add_i32 s70, s70, 2
	s_add_u32 s30, s30, 0x100
	s_addc_u32 s31, s31, 0
	s_add_u32 s68, s68, 0x100
	s_addc_u32 s69, s69, 0
	s_cmp_gt_u32 s70, 5
	s_cbranch_scc0 .LBB0_1087
	s_and_b64 vcc, exec, s[8:9]
	s_cbranch_vccz .LBB0_1090
	s_barrier

.LBB0_1160:
	s_add_u32 s22, s30, 0x100
	s_addc_u32 s23, s31, 0
	s_add_i32 s65, 0, 0x10000
	s_cmp_eq_u32 s64, 18
	s_cselect_b32 s41, s58, s23
	s_cselect_b32 s40, s59, s22
	s_cselect_b32 s37, s60, s63
	s_cselect_b32 s36, s61, s62
	s_add_i32 s66, 0, 0x14000
	v_add_u32_e32 v2, s65, v222
	v_add_u32_e32 v6, s66, v222
	ds_read_b128 v[26:29], v2
	ds_read_b128 v[30:33], v2 offset:1024
	ds_read_b128 v[18:21], v2 offset:2048
	ds_read_b128 v[22:25], v2 offset:3072
	ds_read_b128 v[10:13], v6
	ds_read_b128 v[14:17], v6 offset:1024
	ds_read_b128 v[2:5], v6 offset:2048
	ds_read_b128 v[6:9], v6 offset:3072
	v_lshl_add_u64 v[174:175], s[30:31], 0, v[170:171]
	s_add_i32 m0, s43, 0xc000
	ds_read_b128 v[190:193], v223
	ds_read_b128 v[194:197], v223 offset:1024
	ds_read_b128 v[198:201], v223 offset:2048
	ds_read_b128 v[202:205], v223 offset:3072
	ds_read_b128 v[224:227], v223 offset:4096
	ds_read_b128 v[228:231], v223 offset:5120
	ds_read_b128 v[232:235], v223 offset:6144
	ds_read_b128 v[236:239], v223 offset:7168
	global_load_lds_dwordx4 v[174:175], off
	v_lshl_add_u64 v[174:175], s[30:31], 0, v[172:173]
	s_add_i32 m0, s43, 0xe000
	s_nop 0
	global_load_lds_dwordx4 v[174:175], off
	s_waitcnt vmcnt(8)
	s_waitcnt lgkmcnt(0)
	s_barrier
	s_setprio 1
	s_waitcnt lgkmcnt(0)
	v_mfma_f32_16x16x128_f8f6f4 v[160:163], v[26:33], v[190:197], v[160:163]
	v_mfma_f32_16x16x128_f8f6f4 v[156:159], v[18:25], v[190:197], v[156:159]
	v_mfma_f32_16x16x128_f8f6f4 v[140:143], v[18:25], v[198:205], v[140:143]
	v_mfma_f32_16x16x128_f8f6f4 v[144:147], v[26:33], v[198:205], v[144:147]
	v_mfma_f32_16x16x128_f8f6f4 v[132:135], v[26:33], v[224:231], v[132:135]
	v_mfma_f32_16x16x128_f8f6f4 v[124:127], v[18:25], v[224:231], v[124:127]
	v_mfma_f32_16x16x128_f8f6f4 v[108:111], v[18:25], v[232:239], v[108:111]
	v_mfma_f32_16x16x128_f8f6f4 v[116:119], v[26:33], v[232:239], v[116:119]
	s_setprio 0
	s_setprio 1
	v_mfma_f32_16x16x128_f8f6f4 v[152:155], v[10:17], v[190:197], v[152:155]
	v_mfma_f32_16x16x128_f8f6f4 v[148:151], v[2:9], v[190:197], v[148:151]
	v_mfma_f32_16x16x128_f8f6f4 v[128:131], v[2:9], v[198:205], v[128:131]
	v_mfma_f32_16x16x128_f8f6f4 v[136:139], v[10:17], v[198:205], v[136:139]
	v_mfma_f32_16x16x128_f8f6f4 v[120:123], v[10:17], v[224:231], v[120:123]
	v_mfma_f32_16x16x128_f8f6f4 v[112:115], v[2:9], v[224:231], v[112:115]
	v_mfma_f32_16x16x128_f8f6f4 v[100:103], v[2:9], v[232:239], v[100:103]
	v_mfma_f32_16x16x128_f8f6f4 v[104:107], v[10:17], v[232:239], v[104:107]
	s_setprio 0
	s_barrier
	s_add_i32 s14, s65, s42
	v_lshl_add_u64 v[174:175], s[36:37], 0, v[34:35]
	s_mov_b32 m0, s14
	ds_read_b128 v[196:199], v223 offset:16384
	ds_read_b128 v[200:203], v223 offset:17408
	ds_read_b128 v[204:207], v223 offset:18432
	ds_read_b128 v[208:211], v223 offset:19456
	ds_read_b128 v[224:227], v223 offset:20480
	ds_read_b128 v[228:231], v223 offset:21504
	ds_read_b128 v[232:235], v223 offset:22528
	ds_read_b128 v[236:239], v223 offset:23552
	global_load_lds_dwordx4 v[174:175], off
	s_add_i32 m0, s14, 0x2000
	s_add_u32 s30, s36, 0x58000
	v_lshl_add_u64 v[190:191], s[36:37], 0, v[164:165]
	s_addc_u32 s31, s37, 0
	s_add_i32 s14, s66, s42
	global_load_lds_dwordx4 v[190:191], off
	v_lshl_add_u64 v[178:179], s[30:31], 0, v[34:35]
	s_mov_b32 m0, s14
	v_lshl_add_u64 v[192:193], s[40:41], 0, v[168:169]
	global_load_lds_dwordx4 v[178:179], off
	v_lshl_add_u64 v[178:179], s[30:31], 0, v[164:165]
	s_add_i32 m0, s14, 0x2000
	v_lshl_add_u64 v[194:195], s[40:41], 0, v[166:167]
	global_load_lds_dwordx4 v[178:179], off
	s_mov_b32 m0, s43
	s_nop 0
	global_load_lds_dwordx4 v[192:193], off
	s_mov_b32 m0, s44
	s_nop 0
	global_load_lds_dwordx4 v[194:195], off
	s_waitcnt vmcnt(8)
	s_waitcnt lgkmcnt(0)
	s_barrier
	s_setprio 1
	s_waitcnt lgkmcnt(0)
	v_mfma_f32_16x16x128_f8f6f4 v[96:99], v[26:33], v[196:203], v[96:99]
	v_mfma_f32_16x16x128_f8f6f4 v[92:95], v[18:25], v[196:203], v[92:95]
	v_mfma_f32_16x16x128_f8f6f4 v[76:79], v[18:25], v[204:211], v[76:79]
	v_mfma_f32_16x16x128_f8f6f4 v[84:87], v[26:33], v[204:211], v[84:87]
	v_mfma_f32_16x16x128_f8f6f4 v[68:71], v[26:33], v[224:231], v[68:71]
	v_mfma_f32_16x16x128_f8f6f4 v[60:63], v[18:25], v[224:231], v[60:63]
	v_mfma_f32_16x16x128_f8f6f4 v[44:47], v[18:25], v[232:239], v[44:47]
	v_mfma_f32_16x16x128_f8f6f4 v[52:55], v[26:33], v[232:239], v[52:55]
	s_setprio 0
	s_setprio 1
	v_mfma_f32_16x16x128_f8f6f4 v[88:91], v[10:17], v[196:203], v[88:91]
	v_mfma_f32_16x16x128_f8f6f4 v[80:83], v[2:9], v[196:203], v[80:83]
	v_mfma_f32_16x16x128_f8f6f4 v[64:67], v[2:9], v[204:211], v[64:67]
	v_mfma_f32_16x16x128_f8f6f4 v[72:75], v[10:17], v[204:211], v[72:75]
	v_mfma_f32_16x16x128_f8f6f4 v[56:59], v[10:17], v[224:231], v[56:59]
	v_mfma_f32_16x16x128_f8f6f4 v[48:51], v[2:9], v[224:231], v[48:51]
	v_mfma_f32_16x16x128_f8f6f4 v[36:39], v[2:9], v[232:239], v[36:39]
	v_mfma_f32_16x16x128_f8f6f4 v[40:43], v[10:17], v[232:239], v[40:43]
	s_setprio 0
	s_barrier
	s_add_i32 s14, 0, 0x18000
	s_add_i32 s65, 0, 0x1c000
	v_add_u32_e32 v14, s14, v222
	v_add_u32_e32 v30, s65, v222
	ds_read_b128 v[2:5], v14
	ds_read_b128 v[6:9], v14 offset:1024
	ds_read_b128 v[10:13], v14 offset:2048
	ds_read_b128 v[14:17], v14 offset:3072
	ds_read_b128 v[18:21], v30
	ds_read_b128 v[22:25], v30 offset:1024
	ds_read_b128 v[26:29], v30 offset:2048
	ds_read_b128 v[30:33], v30 offset:3072
	s_add_u32 s30, s40, 0x58000
	s_addc_u32 s31, s41, 0
	s_mov_b32 m0, s45
	v_lshl_add_u64 v[178:179], s[30:31], 0, v[168:169]
	ds_read_b128 v[196:199], v223 offset:32768
	ds_read_b128 v[200:203], v223 offset:33792
	ds_read_b128 v[204:207], v223 offset:34816
	ds_read_b128 v[208:211], v223 offset:35840
	ds_read_b128 v[224:227], v223 offset:36864
	ds_read_b128 v[228:231], v223 offset:37888
	ds_read_b128 v[232:235], v223 offset:38912
	ds_read_b128 v[236:239], v223 offset:39936
	global_load_lds_dwordx4 v[178:179], off
	v_lshl_add_u64 v[178:179], s[30:31], 0, v[166:167]
	s_mov_b32 m0, s46
	s_nop 0
	global_load_lds_dwordx4 v[178:179], off
	s_waitcnt vmcnt(8)
	s_waitcnt lgkmcnt(0)
	s_barrier
	s_setprio 1
	s_waitcnt lgkmcnt(0)
	v_mfma_f32_16x16x128_f8f6f4 v[160:163], v[2:9], v[196:203], v[160:163]
	v_mfma_f32_16x16x128_f8f6f4 v[156:159], v[10:17], v[196:203], v[156:159]
	v_mfma_f32_16x16x128_f8f6f4 v[140:143], v[10:17], v[204:211], v[140:143]
	v_mfma_f32_16x16x128_f8f6f4 v[144:147], v[2:9], v[204:211], v[144:147]
	v_mfma_f32_16x16x128_f8f6f4 v[132:135], v[2:9], v[224:231], v[132:135]
	v_mfma_f32_16x16x128_f8f6f4 v[124:127], v[10:17], v[224:231], v[124:127]
	v_mfma_f32_16x16x128_f8f6f4 v[108:111], v[10:17], v[232:239], v[108:111]
	v_mfma_f32_16x16x128_f8f6f4 v[116:119], v[2:9], v[232:239], v[116:119]
	s_setprio 0
	s_setprio 1
	v_mfma_f32_16x16x128_f8f6f4 v[152:155], v[18:25], v[196:203], v[152:155]
	v_mfma_f32_16x16x128_f8f6f4 v[148:151], v[26:33], v[196:203], v[148:151]
	v_mfma_f32_16x16x128_f8f6f4 v[128:131], v[26:33], v[204:211], v[128:131]
	v_mfma_f32_16x16x128_f8f6f4 v[136:139], v[18:25], v[204:211], v[136:139]
	v_mfma_f32_16x16x128_f8f6f4 v[120:123], v[18:25], v[224:231], v[120:123]
	v_mfma_f32_16x16x128_f8f6f4 v[112:115], v[26:33], v[224:231], v[112:115]
	v_mfma_f32_16x16x128_f8f6f4 v[100:103], v[26:33], v[232:239], v[100:103]
	v_mfma_f32_16x16x128_f8f6f4 v[104:107], v[18:25], v[232:239], v[104:107]
	s_setprio 0
	s_barrier
	s_add_i32 s14, s14, s42
	v_lshl_add_u64 v[174:175], v[174:175], 0, s[18:19]
	s_mov_b32 m0, s14
	ds_read_b128 v[196:199], v223 offset:49152
	ds_read_b128 v[200:203], v223 offset:50176
	ds_read_b128 v[204:207], v223 offset:51200
	ds_read_b128 v[208:211], v223 offset:52224
	ds_read_b128 v[224:227], v223 offset:53248
	ds_read_b128 v[228:231], v223 offset:54272
	ds_read_b128 v[232:235], v223 offset:55296
	ds_read_b128 v[236:239], v223 offset:56320
	global_load_lds_dwordx4 v[174:175], off
	s_add_i32 m0, s14, 0x2000
	s_add_u32 s30, s36, 0x58080
	v_lshl_add_u64 v[174:175], v[190:191], 0, s[18:19]
	s_addc_u32 s31, s37, 0
	s_add_i32 s14, s65, s42
	global_load_lds_dwordx4 v[174:175], off
	v_lshl_add_u64 v[174:175], s[30:31], 0, v[34:35]
	s_mov_b32 m0, s14
	s_nop 0
	global_load_lds_dwordx4 v[174:175], off
	v_lshl_add_u64 v[174:175], s[30:31], 0, v[164:165]
	s_add_i32 m0, s14, 0x2000
	s_nop 0
	global_load_lds_dwordx4 v[174:175], off
	v_lshl_add_u64 v[174:175], v[192:193], 0, s[18:19]
	s_mov_b32 m0, s51
	s_nop 0
	global_load_lds_dwordx4 v[174:175], off
	v_lshl_add_u64 v[174:175], v[194:195], 0, s[18:19]
	s_mov_b32 m0, s52
	s_nop 0
	global_load_lds_dwordx4 v[174:175], off
	s_waitcnt vmcnt(8)
	s_waitcnt lgkmcnt(0)
	s_barrier
	s_setprio 1
	s_waitcnt lgkmcnt(0)
	v_mfma_f32_16x16x128_f8f6f4 v[96:99], v[2:9], v[196:203], v[96:99]
	v_mfma_f32_16x16x128_f8f6f4 v[92:95], v[10:17], v[196:203], v[92:95]
	v_mfma_f32_16x16x128_f8f6f4 v[76:79], v[10:17], v[204:211], v[76:79]
	v_mfma_f32_16x16x128_f8f6f4 v[84:87], v[2:9], v[204:211], v[84:87]
	v_mfma_f32_16x16x128_f8f6f4 v[68:71], v[2:9], v[224:231], v[68:71]
	v_mfma_f32_16x16x128_f8f6f4 v[60:63], v[10:17], v[224:231], v[60:63]
	v_mfma_f32_16x16x128_f8f6f4 v[44:47], v[10:17], v[232:239], v[44:47]
	v_mfma_f32_16x16x128_f8f6f4 v[52:55], v[2:9], v[232:239], v[52:55]
	s_setprio 0
	s_setprio 1
	v_mfma_f32_16x16x128_f8f6f4 v[88:91], v[18:25], v[196:203], v[88:91]
	v_mfma_f32_16x16x128_f8f6f4 v[80:83], v[26:33], v[196:203], v[80:83]
	v_mfma_f32_16x16x128_f8f6f4 v[64:67], v[26:33], v[204:211], v[64:67]
	v_mfma_f32_16x16x128_f8f6f4 v[72:75], v[18:25], v[204:211], v[72:75]
	v_mfma_f32_16x16x128_f8f6f4 v[56:59], v[18:25], v[224:231], v[56:59]
	v_mfma_f32_16x16x128_f8f6f4 v[48:51], v[26:33], v[224:231], v[48:51]
	v_mfma_f32_16x16x128_f8f6f4 v[36:39], v[26:33], v[232:239], v[36:39]
	v_mfma_f32_16x16x128_f8f6f4 v[40:43], v[18:25], v[232:239], v[40:43]
	s_setprio 0
	s_barrier
	s_add_i32 s64, s64, 2
	s_add_u32 s62, s62, 0x100
	s_addc_u32 s63, s63, 0
	s_cmp_gt_u32 s64, 19
	s_mov_b64 s[30:31], s[22:23]
	s_cbranch_scc0 .LBB0_1160
	s_and_b64 vcc, exec, s[8:9]
	s_mov_b32 s58, 0x19b00000
	v_readlane_b32 s59, v255, 10
	s_mov_b32 s60, 0xff61b1e6
	s_mov_b64 s[62:63], 0x800
	s_cbranch_vccz .LBB0_1163
	s_barrier
